# GEMM K-loops: one LDS-DMA stage (2 instrs) moved from the 6-DMA load segment to the next 2-DMA load segment (4/4 balance), counted waits of the SP2 segments vmcnt(8)->vmcnt(6)
# speedup vs baseline: 1.0103x; 1.0008x over previous
.LBB0_378:
	s_add_u32 s28, s36, 0xfff80080
	s_addc_u32 s29, s37, -1
	s_add_i32 s42, 0, 0x10000
	s_cmp_eq_u32 vcc_hi, 28
	s_cselect_b32 s53, s11, s29
	s_cselect_b32 s52, s21, s28
	s_cselect_b32 s51, s41, s79
	s_cselect_b32 s50, vcc_lo, s78
	s_add_i32 s43, 0, 0x14000
	v_add_u32_e32 v140, s42, v169
	v_add_u32_e32 v173, s43, v169
	ds_read_b128 v[128:131], v140
	ds_read_b128 v[132:135], v140 offset:1024
	ds_read_b128 v[136:139], v140 offset:2048
	ds_read_b128 v[140:143], v140 offset:3072
	ds_read_b128 v[156:159], v173
	ds_read_b128 v[160:163], v173 offset:1024
	ds_read_b128 v[164:167], v173 offset:2048
	ds_read_b128 v[174:177], v173 offset:3072
	v_lshl_add_u64 v[182:183], s[36:37], 0, v[152:153]
	s_add_i32 m0, s88, 0xc000
	ds_read_b128 v[178:181], v172
	ds_read_b128 v[194:197], v172 offset:1024
	ds_read_b128 v[198:201], v172 offset:2048
	ds_read_b128 v[202:205], v172 offset:3072
	ds_read_b128 v[206:209], v172 offset:4096
	ds_read_b128 v[224:227], v172 offset:5120
	ds_read_b128 v[228:231], v172 offset:6144
	ds_read_b128 v[232:235], v172 offset:7168
	global_load_lds_dwordx4 v[182:183], off
	v_lshl_add_u64 v[182:183], s[36:37], 0, v[154:155]
	s_add_i32 m0, s88, 0xe000
	s_nop 0
	global_load_lds_dwordx4 v[182:183], off
	s_waitcnt vmcnt(8)
	s_waitcnt lgkmcnt(0)
	s_barrier
	s_setprio 1
	s_waitcnt lgkmcnt(0)
	v_mfma_f32_16x16x32_bf16 v[124:127], v[128:131], v[178:181], v[124:127]
	v_mfma_f32_16x16x32_bf16 v[120:123], v[136:139], v[178:181], v[120:123]
	v_mfma_f32_16x16x32_bf16 v[116:119], v[128:131], v[198:201], v[116:119]
	v_mfma_f32_16x16x32_bf16 v[108:111], v[136:139], v[198:201], v[108:111]
	v_mfma_f32_16x16x32_bf16 v[100:103], v[128:131], v[206:209], v[100:103]
	v_mfma_f32_16x16x32_bf16 v[92:95], v[136:139], v[206:209], v[92:95]
	v_mfma_f32_16x16x32_bf16 v[84:87], v[128:131], v[228:231], v[84:87]
	v_mfma_f32_16x16x32_bf16 v[76:79], v[136:139], v[228:231], v[76:79]
	v_mfma_f32_16x16x32_bf16 v[124:127], v[132:135], v[194:197], v[124:127]
	v_mfma_f32_16x16x32_bf16 v[120:123], v[140:143], v[194:197], v[120:123]
	v_mfma_f32_16x16x32_bf16 v[116:119], v[132:135], v[202:205], v[116:119]
	v_mfma_f32_16x16x32_bf16 v[108:111], v[140:143], v[202:205], v[108:111]
	v_mfma_f32_16x16x32_bf16 v[100:103], v[132:135], v[224:227], v[100:103]
	v_mfma_f32_16x16x32_bf16 v[92:95], v[140:143], v[224:227], v[92:95]
	v_mfma_f32_16x16x32_bf16 v[84:87], v[132:135], v[232:235], v[84:87]
	v_mfma_f32_16x16x32_bf16 v[76:79], v[140:143], v[232:235], v[76:79]
	s_setprio 0
	s_setprio 1
	v_mfma_f32_16x16x32_bf16 v[112:115], v[156:159], v[178:181], v[112:115]
	v_mfma_f32_16x16x32_bf16 v[104:107], v[164:167], v[178:181], v[104:107]
	v_mfma_f32_16x16x32_bf16 v[96:99], v[156:159], v[198:201], v[96:99]
	v_mfma_f32_16x16x32_bf16 v[88:91], v[164:167], v[198:201], v[88:91]
	v_mfma_f32_16x16x32_bf16 v[80:83], v[156:159], v[206:209], v[80:83]
	v_mfma_f32_16x16x32_bf16 v[72:75], v[164:167], v[206:209], v[72:75]
	v_mfma_f32_16x16x32_bf16 v[68:71], v[156:159], v[228:231], v[68:71]
	v_mfma_f32_16x16x32_bf16 v[64:67], v[164:167], v[228:231], v[64:67]
	v_mfma_f32_16x16x32_bf16 v[112:115], v[160:163], v[194:197], v[112:115]
	v_mfma_f32_16x16x32_bf16 v[104:107], v[174:177], v[194:197], v[104:107]
	v_mfma_f32_16x16x32_bf16 v[96:99], v[160:163], v[202:205], v[96:99]
	v_mfma_f32_16x16x32_bf16 v[88:91], v[174:177], v[202:205], v[88:91]
	v_mfma_f32_16x16x32_bf16 v[80:83], v[160:163], v[224:227], v[80:83]
	v_mfma_f32_16x16x32_bf16 v[72:75], v[174:177], v[224:227], v[72:75]
	v_mfma_f32_16x16x32_bf16 v[68:71], v[160:163], v[232:235], v[68:71]
	v_mfma_f32_16x16x32_bf16 v[64:67], v[174:177], v[232:235], v[64:67]
	s_setprio 0
	s_barrier
	s_add_i32 s28, s42, s62
	v_lshl_add_u64 v[182:183], s[50:51], 0, v[146:147]
	s_mov_b32 m0, s28
	ds_read_b128 v[178:181], v172 offset:16384
	ds_read_b128 v[194:197], v172 offset:17408
	ds_read_b128 v[198:201], v172 offset:18432
	ds_read_b128 v[202:205], v172 offset:19456
	ds_read_b128 v[206:209], v172 offset:20480
	ds_read_b128 v[224:227], v172 offset:21504
	ds_read_b128 v[228:231], v172 offset:22528
	ds_read_b128 v[232:235], v172 offset:23552
	global_load_lds_dwordx4 v[182:183], off
	s_add_i32 m0, s28, 0x2000
	s_add_u32 s28, s50, 0x80000
	v_lshl_add_u64 v[210:211], s[50:51], 0, v[150:151]
	s_addc_u32 s29, s51, 0
	s_add_i32 s42, s43, s62
	global_load_lds_dwordx4 v[210:211], off
	v_lshl_add_u64 v[236:237], s[28:29], 0, v[146:147]
	s_mov_b32 m0, s42
	v_lshl_add_u64 v[238:239], s[52:53], 0, v[148:149]
	global_load_lds_dwordx4 v[236:237], off
	v_lshl_add_u64 v[236:237], s[28:29], 0, v[150:151]
	s_add_i32 m0, s42, 0x2000
	s_nop 0
	global_load_lds_dwordx4 v[236:237], off
	v_lshl_add_u64 v[236:237], s[52:53], 0, v[144:145]
	s_waitcnt vmcnt(6)
	s_waitcnt lgkmcnt(0)
	s_barrier
	s_setprio 1
	s_waitcnt lgkmcnt(0)
	v_mfma_f32_16x16x32_bf16 v[60:63], v[128:131], v[178:181], v[60:63]
	v_mfma_f32_16x16x32_bf16 v[56:59], v[136:139], v[178:181], v[56:59]
	v_mfma_f32_16x16x32_bf16 v[52:55], v[128:131], v[198:201], v[52:55]
	v_mfma_f32_16x16x32_bf16 v[44:47], v[136:139], v[198:201], v[44:47]
	v_mfma_f32_16x16x32_bf16 v[36:39], v[128:131], v[206:209], v[36:39]
	v_mfma_f32_16x16x32_bf16 v[28:31], v[136:139], v[206:209], v[28:31]
	v_mfma_f32_16x16x32_bf16 v[20:23], v[128:131], v[228:231], v[20:23]
	v_mfma_f32_16x16x32_bf16 v[12:15], v[136:139], v[228:231], v[12:15]
	v_mfma_f32_16x16x32_bf16 v[60:63], v[132:135], v[194:197], v[60:63]
	v_mfma_f32_16x16x32_bf16 v[56:59], v[140:143], v[194:197], v[56:59]
	v_mfma_f32_16x16x32_bf16 v[52:55], v[132:135], v[202:205], v[52:55]
	v_mfma_f32_16x16x32_bf16 v[44:47], v[140:143], v[202:205], v[44:47]
	v_mfma_f32_16x16x32_bf16 v[36:39], v[132:135], v[224:227], v[36:39]
	v_mfma_f32_16x16x32_bf16 v[28:31], v[140:143], v[224:227], v[28:31]
	v_mfma_f32_16x16x32_bf16 v[20:23], v[132:135], v[232:235], v[20:23]
	v_mfma_f32_16x16x32_bf16 v[12:15], v[140:143], v[232:235], v[12:15]
	s_setprio 0
	s_setprio 1
	v_mfma_f32_16x16x32_bf16 v[48:51], v[156:159], v[178:181], v[48:51]
	v_mfma_f32_16x16x32_bf16 v[40:43], v[164:167], v[178:181], v[40:43]
	v_mfma_f32_16x16x32_bf16 v[32:35], v[156:159], v[198:201], v[32:35]
	v_mfma_f32_16x16x32_bf16 v[24:27], v[164:167], v[198:201], v[24:27]
	v_mfma_f32_16x16x32_bf16 v[16:19], v[156:159], v[206:209], v[16:19]
	v_mfma_f32_16x16x32_bf16 v[8:11], v[164:167], v[206:209], v[8:11]
	v_mfma_f32_16x16x32_bf16 v[4:7], v[156:159], v[228:231], v[4:7]
	v_mfma_f32_16x16x32_bf16 v[0:3], v[164:167], v[228:231], v[0:3]
	v_mfma_f32_16x16x32_bf16 v[48:51], v[160:163], v[194:197], v[48:51]
	v_mfma_f32_16x16x32_bf16 v[40:43], v[174:177], v[194:197], v[40:43]
	v_mfma_f32_16x16x32_bf16 v[32:35], v[160:163], v[202:205], v[32:35]
	v_mfma_f32_16x16x32_bf16 v[24:27], v[174:177], v[202:205], v[24:27]
	v_mfma_f32_16x16x32_bf16 v[16:19], v[160:163], v[224:227], v[16:19]
	v_mfma_f32_16x16x32_bf16 v[8:11], v[174:177], v[224:227], v[8:11]
	v_mfma_f32_16x16x32_bf16 v[4:7], v[160:163], v[232:235], v[4:7]
	v_mfma_f32_16x16x32_bf16 v[0:3], v[174:177], v[232:235], v[0:3]
	s_setprio 0
	s_barrier
	s_add_i32 s42, 0, 0x18000
	s_add_i32 s43, 0, 0x1c000
	v_add_u32_e32 v140, s42, v169
	v_add_u32_e32 v173, s43, v169
	ds_read_b128 v[128:131], v140
	ds_read_b128 v[132:135], v140 offset:1024
	ds_read_b128 v[136:139], v140 offset:2048
	ds_read_b128 v[140:143], v140 offset:3072
	ds_read_b128 v[156:159], v173
	ds_read_b128 v[160:163], v173 offset:1024
	ds_read_b128 v[164:167], v173 offset:2048
	ds_read_b128 v[174:177], v173 offset:3072
	s_add_u32 s28, s52, 0x80000
	s_addc_u32 s29, s53, 0
	s_mov_b32 m0, s26
	v_lshl_add_u64 v[240:241], s[28:29], 0, v[144:145]
	ds_read_b128 v[178:181], v172 offset:32768
	ds_read_b128 v[194:197], v172 offset:33792
	ds_read_b128 v[198:201], v172 offset:34816
	ds_read_b128 v[202:205], v172 offset:35840
	ds_read_b128 v[206:209], v172 offset:36864
	ds_read_b128 v[224:227], v172 offset:37888
	ds_read_b128 v[228:231], v172 offset:38912
	ds_read_b128 v[232:235], v172 offset:39936
	global_load_lds_dwordx4 v[240:241], off
	v_lshl_add_u64 v[240:241], s[28:29], 0, v[148:149]
	s_mov_b32 m0, s27
	s_nop 0
	global_load_lds_dwordx4 v[240:241], off
	s_mov_b32 m0, s88
	s_nop 0
	global_load_lds_dwordx4 v[236:237], off
	s_mov_b32 m0, s89
	s_nop 0
	global_load_lds_dwordx4 v[238:239], off
	s_waitcnt vmcnt(8)
	s_waitcnt lgkmcnt(0)
	s_barrier
	s_setprio 1
	s_waitcnt lgkmcnt(0)
	v_mfma_f32_16x16x32_bf16 v[124:127], v[128:131], v[178:181], v[124:127]
	v_mfma_f32_16x16x32_bf16 v[120:123], v[136:139], v[178:181], v[120:123]
	v_mfma_f32_16x16x32_bf16 v[116:119], v[128:131], v[198:201], v[116:119]
	v_mfma_f32_16x16x32_bf16 v[108:111], v[136:139], v[198:201], v[108:111]
	v_mfma_f32_16x16x32_bf16 v[100:103], v[128:131], v[206:209], v[100:103]
	v_mfma_f32_16x16x32_bf16 v[92:95], v[136:139], v[206:209], v[92:95]
	v_mfma_f32_16x16x32_bf16 v[84:87], v[128:131], v[228:231], v[84:87]
	v_mfma_f32_16x16x32_bf16 v[76:79], v[136:139], v[228:231], v[76:79]
	v_mfma_f32_16x16x32_bf16 v[124:127], v[132:135], v[194:197], v[124:127]
	v_mfma_f32_16x16x32_bf16 v[120:123], v[140:143], v[194:197], v[120:123]
	v_mfma_f32_16x16x32_bf16 v[116:119], v[132:135], v[202:205], v[116:119]
	v_mfma_f32_16x16x32_bf16 v[108:111], v[140:143], v[202:205], v[108:111]
	v_mfma_f32_16x16x32_bf16 v[100:103], v[132:135], v[224:227], v[100:103]
	v_mfma_f32_16x16x32_bf16 v[92:95], v[140:143], v[224:227], v[92:95]
	v_mfma_f32_16x16x32_bf16 v[84:87], v[132:135], v[232:235], v[84:87]
	v_mfma_f32_16x16x32_bf16 v[76:79], v[140:143], v[232:235], v[76:79]
	s_setprio 0
	s_setprio 1
	v_mfma_f32_16x16x32_bf16 v[112:115], v[156:159], v[178:181], v[112:115]
	v_mfma_f32_16x16x32_bf16 v[104:107], v[164:167], v[178:181], v[104:107]
	v_mfma_f32_16x16x32_bf16 v[96:99], v[156:159], v[198:201], v[96:99]
	v_mfma_f32_16x16x32_bf16 v[88:91], v[164:167], v[198:201], v[88:91]
	v_mfma_f32_16x16x32_bf16 v[80:83], v[156:159], v[206:209], v[80:83]
	v_mfma_f32_16x16x32_bf16 v[72:75], v[164:167], v[206:209], v[72:75]
	v_mfma_f32_16x16x32_bf16 v[68:71], v[156:159], v[228:231], v[68:71]
	v_mfma_f32_16x16x32_bf16 v[64:67], v[164:167], v[228:231], v[64:67]
	v_mfma_f32_16x16x32_bf16 v[112:115], v[160:163], v[194:197], v[112:115]
	v_mfma_f32_16x16x32_bf16 v[104:107], v[174:177], v[194:197], v[104:107]
	v_mfma_f32_16x16x32_bf16 v[96:99], v[160:163], v[202:205], v[96:99]
	v_mfma_f32_16x16x32_bf16 v[88:91], v[174:177], v[202:205], v[88:91]
	v_mfma_f32_16x16x32_bf16 v[80:83], v[160:163], v[224:227], v[80:83]
	v_mfma_f32_16x16x32_bf16 v[72:75], v[174:177], v[224:227], v[72:75]
	v_mfma_f32_16x16x32_bf16 v[68:71], v[160:163], v[232:235], v[68:71]
	v_mfma_f32_16x16x32_bf16 v[64:67], v[174:177], v[232:235], v[64:67]
	s_setprio 0
	s_barrier
	s_add_i32 s28, s42, s62
	v_lshl_add_u64 v[182:183], v[182:183], 0, s[68:69]
	s_mov_b32 m0, s28
	ds_read_b128 v[178:181], v172 offset:49152
	ds_read_b128 v[194:197], v172 offset:50176
	ds_read_b128 v[198:201], v172 offset:51200
	ds_read_b128 v[202:205], v172 offset:52224
	ds_read_b128 v[206:209], v172 offset:53248
	ds_read_b128 v[224:227], v172 offset:54272
	ds_read_b128 v[228:231], v172 offset:55296
	ds_read_b128 v[232:235], v172 offset:56320
	global_load_lds_dwordx4 v[182:183], off
	s_add_i32 m0, s28, 0x2000
	s_add_u32 s28, s50, 0x80080
	v_lshl_add_u64 v[182:183], v[210:211], 0, s[68:69]
	s_addc_u32 s29, s51, 0
	s_add_i32 s42, s43, s62
	global_load_lds_dwordx4 v[182:183], off
	v_lshl_add_u64 v[182:183], s[28:29], 0, v[146:147]
	s_mov_b32 m0, s42
	s_nop 0
	global_load_lds_dwordx4 v[182:183], off
	v_lshl_add_u64 v[182:183], s[28:29], 0, v[150:151]
	s_add_i32 m0, s42, 0x2000
	s_nop 0
	global_load_lds_dwordx4 v[182:183], off
	v_lshl_add_u64 v[182:183], v[236:237], 0, s[68:69]
	s_mov_b32 m0, s94
	s_nop 0
	global_load_lds_dwordx4 v[182:183], off
	v_lshl_add_u64 v[182:183], v[238:239], 0, s[68:69]
	s_mov_b32 m0, s95
	s_nop 0
	global_load_lds_dwordx4 v[182:183], off
	s_waitcnt vmcnt(6)
	s_waitcnt lgkmcnt(0)
	s_barrier
	s_setprio 1
	s_waitcnt lgkmcnt(0)
	v_mfma_f32_16x16x32_bf16 v[60:63], v[128:131], v[178:181], v[60:63]
	v_mfma_f32_16x16x32_bf16 v[56:59], v[136:139], v[178:181], v[56:59]
	v_mfma_f32_16x16x32_bf16 v[52:55], v[128:131], v[198:201], v[52:55]
	v_mfma_f32_16x16x32_bf16 v[44:47], v[136:139], v[198:201], v[44:47]
	v_mfma_f32_16x16x32_bf16 v[36:39], v[128:131], v[206:209], v[36:39]
	v_mfma_f32_16x16x32_bf16 v[28:31], v[136:139], v[206:209], v[28:31]
	v_mfma_f32_16x16x32_bf16 v[20:23], v[128:131], v[228:231], v[20:23]
	v_mfma_f32_16x16x32_bf16 v[12:15], v[136:139], v[228:231], v[12:15]
	v_mfma_f32_16x16x32_bf16 v[60:63], v[132:135], v[194:197], v[60:63]
	v_mfma_f32_16x16x32_bf16 v[56:59], v[140:143], v[194:197], v[56:59]
	v_mfma_f32_16x16x32_bf16 v[52:55], v[132:135], v[202:205], v[52:55]
	v_mfma_f32_16x16x32_bf16 v[44:47], v[140:143], v[202:205], v[44:47]
	v_mfma_f32_16x16x32_bf16 v[36:39], v[132:135], v[224:227], v[36:39]
	v_mfma_f32_16x16x32_bf16 v[28:31], v[140:143], v[224:227], v[28:31]
	v_mfma_f32_16x16x32_bf16 v[20:23], v[132:135], v[232:235], v[20:23]
	v_mfma_f32_16x16x32_bf16 v[12:15], v[140:143], v[232:235], v[12:15]
	s_setprio 0
	s_setprio 1
	v_mfma_f32_16x16x32_bf16 v[48:51], v[156:159], v[178:181], v[48:51]
	v_mfma_f32_16x16x32_bf16 v[40:43], v[164:167], v[178:181], v[40:43]
	v_mfma_f32_16x16x32_bf16 v[32:35], v[156:159], v[198:201], v[32:35]
	v_mfma_f32_16x16x32_bf16 v[24:27], v[164:167], v[198:201], v[24:27]
	v_mfma_f32_16x16x32_bf16 v[16:19], v[156:159], v[206:209], v[16:19]
	v_mfma_f32_16x16x32_bf16 v[8:11], v[164:167], v[206:209], v[8:11]
	v_mfma_f32_16x16x32_bf16 v[4:7], v[156:159], v[228:231], v[4:7]
	v_mfma_f32_16x16x32_bf16 v[0:3], v[164:167], v[228:231], v[0:3]
	v_mfma_f32_16x16x32_bf16 v[48:51], v[160:163], v[194:197], v[48:51]
	v_mfma_f32_16x16x32_bf16 v[40:43], v[174:177], v[194:197], v[40:43]
	v_mfma_f32_16x16x32_bf16 v[32:35], v[160:163], v[202:205], v[32:35]
	v_mfma_f32_16x16x32_bf16 v[24:27], v[174:177], v[202:205], v[24:27]
	v_mfma_f32_16x16x32_bf16 v[16:19], v[160:163], v[224:227], v[16:19]
	v_mfma_f32_16x16x32_bf16 v[8:11], v[174:177], v[224:227], v[8:11]
	v_mfma_f32_16x16x32_bf16 v[4:7], v[160:163], v[232:235], v[4:7]
	v_mfma_f32_16x16x32_bf16 v[0:3], v[174:177], v[232:235], v[0:3]
	s_setprio 0
	s_barrier
	s_add_i32 vcc_hi, vcc_hi, 2
	s_add_u32 s36, s36, 0x100
	s_addc_u32 s37, s37, 0
	s_add_u32 s78, s78, 0x100
	s_addc_u32 s79, s79, 0
	s_cmp_gt_u32 vcc_hi, 29
	s_cbranch_scc0 .LBB0_378
	s_and_b64 vcc, exec, s[14:15]
	s_cbranch_vccz .LBB0_381
	s_barrier

.LBB0_682:
	s_add_u32 s18, s16, 0x100
	s_addc_u32 s19, s17, 0
	s_add_u32 s28, s45, s16
	s_addc_u32 s29, s46, s17
	s_cmp_eq_u32 s47, 4
	s_cselect_b32 s36, 0, s18
	s_cselect_b32 s37, 0, s19
	s_cselect_b32 s30, s44, s28
	s_cselect_b32 s31, s9, s29
	s_add_u32 s36, s64, s36
	s_addc_u32 s37, s65, s37
	s_add_i32 s28, 0, 0x10000
	s_add_i32 s29, 0, 0x14000
	v_add_u32_e32 v168, s28, v154
	v_add_u32_e32 v194, s29, v154
	ds_read_b128 v[156:159], v168
	ds_read_b128 v[160:163], v168 offset:1024
	ds_read_b128 v[164:167], v168 offset:2048
	ds_read_b128 v[168:171], v168 offset:3072
	ds_read_b128 v[172:175], v194
	ds_read_b128 v[176:179], v194 offset:1024
	ds_read_b128 v[180:183], v194 offset:2048
	ds_read_b128 v[194:197], v194 offset:3072
	v_lshl_add_u64 v[210:211], v[150:151], 0, s[16:17]
	s_add_i32 m0, s20, 0xc000
	ds_read_b128 v[198:201], v155
	ds_read_b128 v[202:205], v155 offset:1024
	ds_read_b128 v[206:209], v155 offset:2048
	ds_read_b128 v[224:227], v155 offset:3072
	ds_read_b128 v[228:231], v155 offset:4096
	ds_read_b128 v[232:235], v155 offset:5120
	ds_read_b128 v[236:239], v155 offset:6144
	ds_read_b128 v[240:243], v155 offset:7168
	global_load_lds_dwordx4 v[210:211], off
	v_lshl_add_u64 v[210:211], v[152:153], 0, s[16:17]
	s_add_i32 m0, s20, 0xe000
	s_nop 0
	global_load_lds_dwordx4 v[210:211], off
	s_waitcnt vmcnt(8)
	s_waitcnt lgkmcnt(0)
	s_barrier
	s_setprio 1
	s_waitcnt lgkmcnt(0)
	v_mfma_f32_16x16x32_bf16 v[124:127], v[156:159], v[198:201], v[124:127]
	v_mfma_f32_16x16x32_bf16 v[120:123], v[164:167], v[198:201], v[120:123]
	v_mfma_f32_16x16x32_bf16 v[116:119], v[156:159], v[206:209], v[116:119]
	v_mfma_f32_16x16x32_bf16 v[108:111], v[164:167], v[206:209], v[108:111]
	v_mfma_f32_16x16x32_bf16 v[100:103], v[156:159], v[228:231], v[100:103]
	v_mfma_f32_16x16x32_bf16 v[92:95], v[164:167], v[228:231], v[92:95]
	v_mfma_f32_16x16x32_bf16 v[84:87], v[156:159], v[236:239], v[84:87]
	v_mfma_f32_16x16x32_bf16 v[76:79], v[164:167], v[236:239], v[76:79]
	v_mfma_f32_16x16x32_bf16 v[124:127], v[160:163], v[202:205], v[124:127]
	v_mfma_f32_16x16x32_bf16 v[120:123], v[168:171], v[202:205], v[120:123]
	v_mfma_f32_16x16x32_bf16 v[116:119], v[160:163], v[224:227], v[116:119]
	v_mfma_f32_16x16x32_bf16 v[108:111], v[168:171], v[224:227], v[108:111]
	v_mfma_f32_16x16x32_bf16 v[100:103], v[160:163], v[232:235], v[100:103]
	v_mfma_f32_16x16x32_bf16 v[92:95], v[168:171], v[232:235], v[92:95]
	v_mfma_f32_16x16x32_bf16 v[84:87], v[160:163], v[240:243], v[84:87]
	v_mfma_f32_16x16x32_bf16 v[76:79], v[168:171], v[240:243], v[76:79]
	s_setprio 0
	s_setprio 1
	v_mfma_f32_16x16x32_bf16 v[112:115], v[172:175], v[198:201], v[112:115]
	v_mfma_f32_16x16x32_bf16 v[104:107], v[180:183], v[198:201], v[104:107]
	v_mfma_f32_16x16x32_bf16 v[96:99], v[172:175], v[206:209], v[96:99]
	v_mfma_f32_16x16x32_bf16 v[88:91], v[180:183], v[206:209], v[88:91]
	v_mfma_f32_16x16x32_bf16 v[80:83], v[172:175], v[228:231], v[80:83]
	v_mfma_f32_16x16x32_bf16 v[72:75], v[180:183], v[228:231], v[72:75]
	v_mfma_f32_16x16x32_bf16 v[68:71], v[172:175], v[236:239], v[68:71]
	v_mfma_f32_16x16x32_bf16 v[64:67], v[180:183], v[236:239], v[64:67]
	v_mfma_f32_16x16x32_bf16 v[112:115], v[176:179], v[202:205], v[112:115]
	v_mfma_f32_16x16x32_bf16 v[104:107], v[194:197], v[202:205], v[104:107]
	v_mfma_f32_16x16x32_bf16 v[96:99], v[176:179], v[224:227], v[96:99]
	v_mfma_f32_16x16x32_bf16 v[88:91], v[194:197], v[224:227], v[88:91]
	v_mfma_f32_16x16x32_bf16 v[80:83], v[176:179], v[232:235], v[80:83]
	v_mfma_f32_16x16x32_bf16 v[72:75], v[194:197], v[232:235], v[72:75]
	v_mfma_f32_16x16x32_bf16 v[68:71], v[176:179], v[240:243], v[68:71]
	v_mfma_f32_16x16x32_bf16 v[64:67], v[194:197], v[240:243], v[64:67]
	s_setprio 0
	s_barrier
	s_add_i32 s16, s28, s4
	v_lshl_add_u64 v[210:211], s[30:31], 0, v[184:185]
	s_mov_b32 m0, s16
	ds_read_b128 v[198:201], v155 offset:16384
	ds_read_b128 v[202:205], v155 offset:17408
	ds_read_b128 v[206:209], v155 offset:18432
	ds_read_b128 v[224:227], v155 offset:19456
	ds_read_b128 v[228:231], v155 offset:20480
	ds_read_b128 v[232:235], v155 offset:21504
	ds_read_b128 v[236:239], v155 offset:22528
	ds_read_b128 v[240:243], v155 offset:23552
	global_load_lds_dwordx4 v[210:211], off
	s_add_i32 m0, s16, 0x2000
	s_add_u32 s16, s30, 0x20000
	v_lshl_add_u64 v[244:245], s[30:31], 0, v[128:129]
	s_addc_u32 s17, s31, 0
	s_add_i32 s28, s29, s4
	global_load_lds_dwordx4 v[244:245], off
	v_lshl_add_u64 v[246:247], s[16:17], 0, v[184:185]
	s_mov_b32 m0, s28
	v_lshl_add_u64 v[218:219], s[36:37], 0, v[130:131]
	global_load_lds_dwordx4 v[246:247], off
	v_lshl_add_u64 v[246:247], s[16:17], 0, v[128:129]
	s_add_i32 m0, s28, 0x2000
	s_nop 0
	global_load_lds_dwordx4 v[246:247], off
	v_lshl_add_u64 v[246:247], s[36:37], 0, v[132:133]
	s_waitcnt vmcnt(6)
	s_waitcnt lgkmcnt(0)
	s_barrier
	s_setprio 1
	s_waitcnt lgkmcnt(0)
	v_mfma_f32_16x16x32_bf16 v[60:63], v[156:159], v[198:201], v[60:63]
	v_mfma_f32_16x16x32_bf16 v[56:59], v[164:167], v[198:201], v[56:59]
	v_mfma_f32_16x16x32_bf16 v[52:55], v[156:159], v[206:209], v[52:55]
	v_mfma_f32_16x16x32_bf16 v[44:47], v[164:167], v[206:209], v[44:47]
	v_mfma_f32_16x16x32_bf16 v[36:39], v[156:159], v[228:231], v[36:39]
	v_mfma_f32_16x16x32_bf16 v[28:31], v[164:167], v[228:231], v[28:31]
	v_mfma_f32_16x16x32_bf16 v[20:23], v[156:159], v[236:239], v[20:23]
	v_mfma_f32_16x16x32_bf16 v[12:15], v[164:167], v[236:239], v[12:15]
	v_mfma_f32_16x16x32_bf16 v[60:63], v[160:163], v[202:205], v[60:63]
	v_mfma_f32_16x16x32_bf16 v[56:59], v[168:171], v[202:205], v[56:59]
	v_mfma_f32_16x16x32_bf16 v[52:55], v[160:163], v[224:227], v[52:55]
	v_mfma_f32_16x16x32_bf16 v[44:47], v[168:171], v[224:227], v[44:47]
	v_mfma_f32_16x16x32_bf16 v[36:39], v[160:163], v[232:235], v[36:39]
	v_mfma_f32_16x16x32_bf16 v[28:31], v[168:171], v[232:235], v[28:31]
	v_mfma_f32_16x16x32_bf16 v[20:23], v[160:163], v[240:243], v[20:23]
	v_mfma_f32_16x16x32_bf16 v[12:15], v[168:171], v[240:243], v[12:15]
	s_setprio 0
	s_setprio 1
	v_mfma_f32_16x16x32_bf16 v[48:51], v[172:175], v[198:201], v[48:51]
	v_mfma_f32_16x16x32_bf16 v[40:43], v[180:183], v[198:201], v[40:43]
	v_mfma_f32_16x16x32_bf16 v[32:35], v[172:175], v[206:209], v[32:35]
	v_mfma_f32_16x16x32_bf16 v[24:27], v[180:183], v[206:209], v[24:27]
	v_mfma_f32_16x16x32_bf16 v[16:19], v[172:175], v[228:231], v[16:19]
	v_mfma_f32_16x16x32_bf16 v[8:11], v[180:183], v[228:231], v[8:11]
	v_mfma_f32_16x16x32_bf16 v[4:7], v[172:175], v[236:239], v[4:7]
	v_mfma_f32_16x16x32_bf16 v[0:3], v[180:183], v[236:239], v[0:3]
	v_mfma_f32_16x16x32_bf16 v[48:51], v[176:179], v[202:205], v[48:51]
	v_mfma_f32_16x16x32_bf16 v[40:43], v[194:197], v[202:205], v[40:43]
	v_mfma_f32_16x16x32_bf16 v[32:35], v[176:179], v[224:227], v[32:35]
	v_mfma_f32_16x16x32_bf16 v[24:27], v[194:197], v[224:227], v[24:27]
	v_mfma_f32_16x16x32_bf16 v[16:19], v[176:179], v[232:235], v[16:19]
	v_mfma_f32_16x16x32_bf16 v[8:11], v[194:197], v[232:235], v[8:11]
	v_mfma_f32_16x16x32_bf16 v[4:7], v[176:179], v[240:243], v[4:7]
	v_mfma_f32_16x16x32_bf16 v[0:3], v[194:197], v[240:243], v[0:3]
	s_setprio 0
	s_barrier
	s_add_i32 s28, 0, 0x18000
	s_add_i32 s29, 0, 0x1c000
	v_add_u32_e32 v168, s28, v154
	v_add_u32_e32 v194, s29, v154
	ds_read_b128 v[156:159], v168
	ds_read_b128 v[160:163], v168 offset:1024
	ds_read_b128 v[164:167], v168 offset:2048
	ds_read_b128 v[168:171], v168 offset:3072
	ds_read_b128 v[172:175], v194
	ds_read_b128 v[176:179], v194 offset:1024
	ds_read_b128 v[180:183], v194 offset:2048
	ds_read_b128 v[194:197], v194 offset:3072
	s_add_u32 s16, s36, 0x20000
	s_addc_u32 s17, s37, 0
	s_mov_b32 m0, s26
	v_lshl_add_u64 v[216:217], s[16:17], 0, v[132:133]
	ds_read_b128 v[198:201], v155 offset:32768
	ds_read_b128 v[202:205], v155 offset:33792
	ds_read_b128 v[206:209], v155 offset:34816
	ds_read_b128 v[224:227], v155 offset:35840
	ds_read_b128 v[228:231], v155 offset:36864
	ds_read_b128 v[232:235], v155 offset:37888
	ds_read_b128 v[236:239], v155 offset:38912
	ds_read_b128 v[240:243], v155 offset:39936
	global_load_lds_dwordx4 v[216:217], off
	v_lshl_add_u64 v[216:217], s[16:17], 0, v[130:131]
	s_mov_b32 m0, s27
	s_nop 0
	global_load_lds_dwordx4 v[216:217], off
	s_mov_b32 m0, s20
	s_nop 0
	global_load_lds_dwordx4 v[246:247], off
	s_mov_b32 m0, s21
	s_nop 0
	global_load_lds_dwordx4 v[218:219], off
	s_waitcnt vmcnt(8)
	s_waitcnt lgkmcnt(0)
	s_barrier
	s_setprio 1
	s_waitcnt lgkmcnt(0)
	v_mfma_f32_16x16x32_bf16 v[124:127], v[156:159], v[198:201], v[124:127]
	v_mfma_f32_16x16x32_bf16 v[120:123], v[164:167], v[198:201], v[120:123]
	v_mfma_f32_16x16x32_bf16 v[116:119], v[156:159], v[206:209], v[116:119]
	v_mfma_f32_16x16x32_bf16 v[108:111], v[164:167], v[206:209], v[108:111]
	v_mfma_f32_16x16x32_bf16 v[100:103], v[156:159], v[228:231], v[100:103]
	v_mfma_f32_16x16x32_bf16 v[92:95], v[164:167], v[228:231], v[92:95]
	v_mfma_f32_16x16x32_bf16 v[84:87], v[156:159], v[236:239], v[84:87]
	v_mfma_f32_16x16x32_bf16 v[76:79], v[164:167], v[236:239], v[76:79]
	v_mfma_f32_16x16x32_bf16 v[124:127], v[160:163], v[202:205], v[124:127]
	v_mfma_f32_16x16x32_bf16 v[120:123], v[168:171], v[202:205], v[120:123]
	v_mfma_f32_16x16x32_bf16 v[116:119], v[160:163], v[224:227], v[116:119]
	v_mfma_f32_16x16x32_bf16 v[108:111], v[168:171], v[224:227], v[108:111]
	v_mfma_f32_16x16x32_bf16 v[100:103], v[160:163], v[232:235], v[100:103]
	v_mfma_f32_16x16x32_bf16 v[92:95], v[168:171], v[232:235], v[92:95]
	v_mfma_f32_16x16x32_bf16 v[84:87], v[160:163], v[240:243], v[84:87]
	v_mfma_f32_16x16x32_bf16 v[76:79], v[168:171], v[240:243], v[76:79]
	s_setprio 0
	s_setprio 1
	v_mfma_f32_16x16x32_bf16 v[112:115], v[172:175], v[198:201], v[112:115]
	v_mfma_f32_16x16x32_bf16 v[104:107], v[180:183], v[198:201], v[104:107]
	v_mfma_f32_16x16x32_bf16 v[96:99], v[172:175], v[206:209], v[96:99]
	v_mfma_f32_16x16x32_bf16 v[88:91], v[180:183], v[206:209], v[88:91]
	v_mfma_f32_16x16x32_bf16 v[80:83], v[172:175], v[228:231], v[80:83]
	v_mfma_f32_16x16x32_bf16 v[72:75], v[180:183], v[228:231], v[72:75]
	v_mfma_f32_16x16x32_bf16 v[68:71], v[172:175], v[236:239], v[68:71]
	v_mfma_f32_16x16x32_bf16 v[64:67], v[180:183], v[236:239], v[64:67]
	v_mfma_f32_16x16x32_bf16 v[112:115], v[176:179], v[202:205], v[112:115]
	v_mfma_f32_16x16x32_bf16 v[104:107], v[194:197], v[202:205], v[104:107]
	v_mfma_f32_16x16x32_bf16 v[96:99], v[176:179], v[224:227], v[96:99]
	v_mfma_f32_16x16x32_bf16 v[88:91], v[194:197], v[224:227], v[88:91]
	v_mfma_f32_16x16x32_bf16 v[80:83], v[176:179], v[232:235], v[80:83]
	v_mfma_f32_16x16x32_bf16 v[72:75], v[194:197], v[232:235], v[72:75]
	v_mfma_f32_16x16x32_bf16 v[68:71], v[176:179], v[240:243], v[68:71]
	v_mfma_f32_16x16x32_bf16 v[64:67], v[194:197], v[240:243], v[64:67]
	s_setprio 0
	s_barrier
	s_add_i32 s16, s28, s4
	v_lshl_add_u64 v[210:211], v[210:211], 0, s[68:69]
	s_mov_b32 m0, s16
	ds_read_b128 v[198:201], v155 offset:49152
	ds_read_b128 v[202:205], v155 offset:50176
	ds_read_b128 v[206:209], v155 offset:51200
	ds_read_b128 v[224:227], v155 offset:52224
	ds_read_b128 v[228:231], v155 offset:53248
	ds_read_b128 v[232:235], v155 offset:54272
	ds_read_b128 v[236:239], v155 offset:55296
	ds_read_b128 v[240:243], v155 offset:56320
	global_load_lds_dwordx4 v[210:211], off
	s_add_i32 m0, s16, 0x2000
	s_add_u32 s16, s30, 0x20080
	v_lshl_add_u64 v[210:211], v[244:245], 0, s[68:69]
	s_addc_u32 s17, s31, 0
	s_add_i32 s28, s29, s4
	global_load_lds_dwordx4 v[210:211], off
	v_lshl_add_u64 v[210:211], s[16:17], 0, v[184:185]
	s_mov_b32 m0, s28
	s_nop 0
	global_load_lds_dwordx4 v[210:211], off
	v_lshl_add_u64 v[210:211], s[16:17], 0, v[128:129]
	s_add_i32 m0, s28, 0x2000
	s_nop 0
	global_load_lds_dwordx4 v[210:211], off
	v_lshl_add_u64 v[210:211], v[246:247], 0, s[68:69]
	s_mov_b32 m0, s38
	s_nop 0
	global_load_lds_dwordx4 v[210:211], off
	v_lshl_add_u64 v[210:211], v[218:219], 0, s[68:69]
	s_mov_b32 m0, s39
	s_nop 0
	global_load_lds_dwordx4 v[210:211], off
	s_waitcnt vmcnt(6)
	s_waitcnt lgkmcnt(0)
	s_barrier
	s_setprio 1
	s_waitcnt lgkmcnt(0)
	v_mfma_f32_16x16x32_bf16 v[60:63], v[156:159], v[198:201], v[60:63]
	v_mfma_f32_16x16x32_bf16 v[56:59], v[164:167], v[198:201], v[56:59]
	v_mfma_f32_16x16x32_bf16 v[52:55], v[156:159], v[206:209], v[52:55]
	v_mfma_f32_16x16x32_bf16 v[44:47], v[164:167], v[206:209], v[44:47]
	v_mfma_f32_16x16x32_bf16 v[36:39], v[156:159], v[228:231], v[36:39]
	v_mfma_f32_16x16x32_bf16 v[28:31], v[164:167], v[228:231], v[28:31]
	v_mfma_f32_16x16x32_bf16 v[20:23], v[156:159], v[236:239], v[20:23]
	v_mfma_f32_16x16x32_bf16 v[12:15], v[164:167], v[236:239], v[12:15]
	v_mfma_f32_16x16x32_bf16 v[60:63], v[160:163], v[202:205], v[60:63]
	v_mfma_f32_16x16x32_bf16 v[56:59], v[168:171], v[202:205], v[56:59]
	v_mfma_f32_16x16x32_bf16 v[52:55], v[160:163], v[224:227], v[52:55]
	v_mfma_f32_16x16x32_bf16 v[44:47], v[168:171], v[224:227], v[44:47]
	v_mfma_f32_16x16x32_bf16 v[36:39], v[160:163], v[232:235], v[36:39]
	v_mfma_f32_16x16x32_bf16 v[28:31], v[168:171], v[232:235], v[28:31]
	v_mfma_f32_16x16x32_bf16 v[20:23], v[160:163], v[240:243], v[20:23]
	v_mfma_f32_16x16x32_bf16 v[12:15], v[168:171], v[240:243], v[12:15]
	s_setprio 0
	s_setprio 1
	v_mfma_f32_16x16x32_bf16 v[48:51], v[172:175], v[198:201], v[48:51]
	v_mfma_f32_16x16x32_bf16 v[40:43], v[180:183], v[198:201], v[40:43]
	v_mfma_f32_16x16x32_bf16 v[32:35], v[172:175], v[206:209], v[32:35]
	v_mfma_f32_16x16x32_bf16 v[24:27], v[180:183], v[206:209], v[24:27]
	v_mfma_f32_16x16x32_bf16 v[16:19], v[172:175], v[228:231], v[16:19]
	v_mfma_f32_16x16x32_bf16 v[8:11], v[180:183], v[228:231], v[8:11]
	v_mfma_f32_16x16x32_bf16 v[4:7], v[172:175], v[236:239], v[4:7]
	v_mfma_f32_16x16x32_bf16 v[0:3], v[180:183], v[236:239], v[0:3]
	v_mfma_f32_16x16x32_bf16 v[48:51], v[176:179], v[202:205], v[48:51]
	v_mfma_f32_16x16x32_bf16 v[40:43], v[194:197], v[202:205], v[40:43]
	v_mfma_f32_16x16x32_bf16 v[32:35], v[176:179], v[224:227], v[32:35]
	v_mfma_f32_16x16x32_bf16 v[24:27], v[194:197], v[224:227], v[24:27]
	v_mfma_f32_16x16x32_bf16 v[16:19], v[176:179], v[232:235], v[16:19]
	v_mfma_f32_16x16x32_bf16 v[8:11], v[194:197], v[232:235], v[8:11]
	v_mfma_f32_16x16x32_bf16 v[4:7], v[176:179], v[240:243], v[4:7]
	v_mfma_f32_16x16x32_bf16 v[0:3], v[194:197], v[240:243], v[0:3]
	s_setprio 0
	s_barrier
	s_add_i32 s47, s47, 2
	s_cmp_gt_u32 s47, 5
	s_mov_b64 s[16:17], s[18:19]
	s_cbranch_scc0 .LBB0_682
	s_and_b64 vcc, exec, s[6:7]
	s_cbranch_vccz .LBB0_685
	s_barrier

.LBB0_805:
	s_add_u32 s28, s30, 0xfff80080
	s_addc_u32 s29, s31, -1
	s_add_i32 s38, 0, 0x10000
	s_cmp_eq_u32 s78, 28
	s_cselect_b32 s45, s9, s29
	s_cselect_b32 s44, s11, s28
	s_cselect_b32 s41, s60, s63
	s_cselect_b32 s40, s61, s62
	s_add_i32 s39, 0, 0x14000
	v_add_u32_e32 v154, s38, v143
	v_add_u32_e32 v170, s39, v143
	ds_read_b128 v[138:141], v154
	ds_read_b128 v[146:149], v154 offset:1024
	ds_read_b128 v[150:153], v154 offset:2048
	ds_read_b128 v[154:157], v154 offset:3072
	ds_read_b128 v[158:161], v170
	ds_read_b128 v[162:165], v170 offset:1024
	ds_read_b128 v[166:169], v170 offset:2048
	ds_read_b128 v[170:173], v170 offset:3072
	v_lshl_add_u64 v[182:183], s[30:31], 0, v[134:135]
	s_add_i32 m0, s21, 0xc000
	ds_read_b128 v[174:177], v145
	ds_read_b128 v[178:181], v145 offset:1024
	ds_read_b128 v[194:197], v145 offset:2048
	ds_read_b128 v[198:201], v145 offset:3072
	ds_read_b128 v[202:205], v145 offset:4096
	ds_read_b128 v[206:209], v145 offset:5120
	ds_read_b128 v[224:227], v145 offset:6144
	ds_read_b128 v[228:231], v145 offset:7168
	global_load_lds_dwordx4 v[182:183], off
	v_lshl_add_u64 v[182:183], s[30:31], 0, v[136:137]
	s_add_i32 m0, s21, 0xe000
	s_nop 0
	global_load_lds_dwordx4 v[182:183], off
	s_waitcnt vmcnt(8)
	s_waitcnt lgkmcnt(0)
	s_barrier
	s_setprio 1
	s_waitcnt lgkmcnt(0)
	v_mfma_f32_16x16x32_bf16 v[124:127], v[138:141], v[174:177], v[124:127]
	v_mfma_f32_16x16x32_bf16 v[120:123], v[150:153], v[174:177], v[120:123]
	v_mfma_f32_16x16x32_bf16 v[116:119], v[138:141], v[194:197], v[116:119]
	v_mfma_f32_16x16x32_bf16 v[104:107], v[150:153], v[194:197], v[104:107]
	v_mfma_f32_16x16x32_bf16 v[100:103], v[138:141], v[202:205], v[100:103]
	v_mfma_f32_16x16x32_bf16 v[88:91], v[150:153], v[202:205], v[88:91]
	v_mfma_f32_16x16x32_bf16 v[84:87], v[138:141], v[224:227], v[84:87]
	v_mfma_f32_16x16x32_bf16 v[72:75], v[150:153], v[224:227], v[72:75]
	v_mfma_f32_16x16x32_bf16 v[124:127], v[146:149], v[178:181], v[124:127]
	v_mfma_f32_16x16x32_bf16 v[120:123], v[154:157], v[178:181], v[120:123]
	v_mfma_f32_16x16x32_bf16 v[116:119], v[146:149], v[198:201], v[116:119]
	v_mfma_f32_16x16x32_bf16 v[104:107], v[154:157], v[198:201], v[104:107]
	v_mfma_f32_16x16x32_bf16 v[100:103], v[146:149], v[206:209], v[100:103]
	v_mfma_f32_16x16x32_bf16 v[88:91], v[154:157], v[206:209], v[88:91]
	v_mfma_f32_16x16x32_bf16 v[84:87], v[146:149], v[228:231], v[84:87]
	v_mfma_f32_16x16x32_bf16 v[72:75], v[154:157], v[228:231], v[72:75]
	s_setprio 0
	s_setprio 1
	v_mfma_f32_16x16x32_bf16 v[112:115], v[158:161], v[174:177], v[112:115]
	v_mfma_f32_16x16x32_bf16 v[108:111], v[166:169], v[174:177], v[108:111]
	v_mfma_f32_16x16x32_bf16 v[96:99], v[158:161], v[194:197], v[96:99]
	v_mfma_f32_16x16x32_bf16 v[92:95], v[166:169], v[194:197], v[92:95]
	v_mfma_f32_16x16x32_bf16 v[80:83], v[158:161], v[202:205], v[80:83]
	v_mfma_f32_16x16x32_bf16 v[76:79], v[166:169], v[202:205], v[76:79]
	v_mfma_f32_16x16x32_bf16 v[68:71], v[158:161], v[224:227], v[68:71]
	v_mfma_f32_16x16x32_bf16 v[64:67], v[166:169], v[224:227], v[64:67]
	v_mfma_f32_16x16x32_bf16 v[112:115], v[162:165], v[178:181], v[112:115]
	v_mfma_f32_16x16x32_bf16 v[108:111], v[170:173], v[178:181], v[108:111]
	v_mfma_f32_16x16x32_bf16 v[96:99], v[162:165], v[198:201], v[96:99]
	v_mfma_f32_16x16x32_bf16 v[92:95], v[170:173], v[198:201], v[92:95]
	v_mfma_f32_16x16x32_bf16 v[80:83], v[162:165], v[206:209], v[80:83]
	v_mfma_f32_16x16x32_bf16 v[76:79], v[170:173], v[206:209], v[76:79]
	v_mfma_f32_16x16x32_bf16 v[68:71], v[162:165], v[228:231], v[68:71]
	v_mfma_f32_16x16x32_bf16 v[64:67], v[170:173], v[228:231], v[64:67]
	s_setprio 0
	s_barrier
	s_add_i32 s28, s38, s20
	v_lshl_add_u64 v[182:183], s[40:41], 0, v[184:185]
	s_mov_b32 m0, s28
	ds_read_b128 v[174:177], v145 offset:16384
	ds_read_b128 v[178:181], v145 offset:17408
	ds_read_b128 v[194:197], v145 offset:18432
	ds_read_b128 v[198:201], v145 offset:19456
	ds_read_b128 v[202:205], v145 offset:20480
	ds_read_b128 v[206:209], v145 offset:21504
	ds_read_b128 v[224:227], v145 offset:22528
	ds_read_b128 v[228:231], v145 offset:23552
	global_load_lds_dwordx4 v[182:183], off
	s_add_i32 m0, s28, 0x2000
	s_add_u32 s28, s40, 0x80000
	v_lshl_add_u64 v[210:211], s[40:41], 0, v[128:129]
	s_addc_u32 s29, s41, 0
	s_add_i32 s38, s39, s20
	global_load_lds_dwordx4 v[210:211], off
	v_lshl_add_u64 v[216:217], s[28:29], 0, v[184:185]
	s_mov_b32 m0, s38
	v_lshl_add_u64 v[218:219], s[44:45], 0, v[130:131]
	global_load_lds_dwordx4 v[216:217], off
	v_lshl_add_u64 v[216:217], s[28:29], 0, v[128:129]
	s_add_i32 m0, s38, 0x2000
	s_nop 0
	global_load_lds_dwordx4 v[216:217], off
	v_lshl_add_u64 v[216:217], s[44:45], 0, v[132:133]
	s_waitcnt vmcnt(6)
	s_waitcnt lgkmcnt(0)
	s_barrier
	s_setprio 1
	s_waitcnt lgkmcnt(0)
	v_mfma_f32_16x16x32_bf16 v[60:63], v[138:141], v[174:177], v[60:63]
	v_mfma_f32_16x16x32_bf16 v[56:59], v[150:153], v[174:177], v[56:59]
	v_mfma_f32_16x16x32_bf16 v[52:55], v[138:141], v[194:197], v[52:55]
	v_mfma_f32_16x16x32_bf16 v[40:43], v[150:153], v[194:197], v[40:43]
	v_mfma_f32_16x16x32_bf16 v[36:39], v[138:141], v[202:205], v[36:39]
	v_mfma_f32_16x16x32_bf16 v[24:27], v[150:153], v[202:205], v[24:27]
	v_mfma_f32_16x16x32_bf16 v[20:23], v[138:141], v[224:227], v[20:23]
	v_mfma_f32_16x16x32_bf16 v[8:11], v[150:153], v[224:227], v[8:11]
	v_mfma_f32_16x16x32_bf16 v[60:63], v[146:149], v[178:181], v[60:63]
	v_mfma_f32_16x16x32_bf16 v[56:59], v[154:157], v[178:181], v[56:59]
	v_mfma_f32_16x16x32_bf16 v[52:55], v[146:149], v[198:201], v[52:55]
	v_mfma_f32_16x16x32_bf16 v[40:43], v[154:157], v[198:201], v[40:43]
	v_mfma_f32_16x16x32_bf16 v[36:39], v[146:149], v[206:209], v[36:39]
	v_mfma_f32_16x16x32_bf16 v[24:27], v[154:157], v[206:209], v[24:27]
	v_mfma_f32_16x16x32_bf16 v[20:23], v[146:149], v[228:231], v[20:23]
	v_mfma_f32_16x16x32_bf16 v[8:11], v[154:157], v[228:231], v[8:11]
	s_setprio 0
	s_setprio 1
	v_mfma_f32_16x16x32_bf16 v[48:51], v[158:161], v[174:177], v[48:51]
	v_mfma_f32_16x16x32_bf16 v[44:47], v[166:169], v[174:177], v[44:47]
	v_mfma_f32_16x16x32_bf16 v[32:35], v[158:161], v[194:197], v[32:35]
	v_mfma_f32_16x16x32_bf16 v[28:31], v[166:169], v[194:197], v[28:31]
	v_mfma_f32_16x16x32_bf16 v[16:19], v[158:161], v[202:205], v[16:19]
	v_mfma_f32_16x16x32_bf16 v[12:15], v[166:169], v[202:205], v[12:15]
	v_mfma_f32_16x16x32_bf16 v[4:7], v[158:161], v[224:227], v[4:7]
	v_mfma_f32_16x16x32_bf16 v[0:3], v[166:169], v[224:227], v[0:3]
	v_mfma_f32_16x16x32_bf16 v[48:51], v[162:165], v[178:181], v[48:51]
	v_mfma_f32_16x16x32_bf16 v[44:47], v[170:173], v[178:181], v[44:47]
	v_mfma_f32_16x16x32_bf16 v[32:35], v[162:165], v[198:201], v[32:35]
	v_mfma_f32_16x16x32_bf16 v[28:31], v[170:173], v[198:201], v[28:31]
	v_mfma_f32_16x16x32_bf16 v[16:19], v[162:165], v[206:209], v[16:19]
	v_mfma_f32_16x16x32_bf16 v[12:15], v[170:173], v[206:209], v[12:15]
	v_mfma_f32_16x16x32_bf16 v[4:7], v[162:165], v[228:231], v[4:7]
	v_mfma_f32_16x16x32_bf16 v[0:3], v[170:173], v[228:231], v[0:3]
	s_setprio 0
	s_barrier
	s_add_i32 s38, 0, 0x18000
	s_add_i32 s39, 0, 0x1c000
	v_add_u32_e32 v154, s38, v143
	v_add_u32_e32 v170, s39, v143
	ds_read_b128 v[138:141], v154
	ds_read_b128 v[146:149], v154 offset:1024
	ds_read_b128 v[150:153], v154 offset:2048
	ds_read_b128 v[154:157], v154 offset:3072
	ds_read_b128 v[158:161], v170
	ds_read_b128 v[162:165], v170 offset:1024
	ds_read_b128 v[166:169], v170 offset:2048
	ds_read_b128 v[170:173], v170 offset:3072
	s_add_u32 s28, s44, 0x80000
	s_addc_u32 s29, s45, 0
	s_mov_b32 m0, s47
	v_lshl_add_u64 v[232:233], s[28:29], 0, v[132:133]
	ds_read_b128 v[174:177], v145 offset:32768
	ds_read_b128 v[178:181], v145 offset:33792
	ds_read_b128 v[194:197], v145 offset:34816
	ds_read_b128 v[198:201], v145 offset:35840
	ds_read_b128 v[202:205], v145 offset:36864
	ds_read_b128 v[206:209], v145 offset:37888
	ds_read_b128 v[224:227], v145 offset:38912
	ds_read_b128 v[228:231], v145 offset:39936
	global_load_lds_dwordx4 v[232:233], off
	v_lshl_add_u64 v[232:233], s[28:29], 0, v[130:131]
	s_mov_b32 m0, s50
	s_nop 0
	global_load_lds_dwordx4 v[232:233], off
	s_mov_b32 m0, s21
	s_nop 0
	global_load_lds_dwordx4 v[216:217], off
	s_mov_b32 m0, s46
	s_nop 0
	global_load_lds_dwordx4 v[218:219], off
	s_waitcnt vmcnt(8)
	s_waitcnt lgkmcnt(0)
	s_barrier
	s_setprio 1
	s_waitcnt lgkmcnt(0)
	v_mfma_f32_16x16x32_bf16 v[124:127], v[138:141], v[174:177], v[124:127]
	v_mfma_f32_16x16x32_bf16 v[120:123], v[150:153], v[174:177], v[120:123]
	v_mfma_f32_16x16x32_bf16 v[116:119], v[138:141], v[194:197], v[116:119]
	v_mfma_f32_16x16x32_bf16 v[104:107], v[150:153], v[194:197], v[104:107]
	v_mfma_f32_16x16x32_bf16 v[100:103], v[138:141], v[202:205], v[100:103]
	v_mfma_f32_16x16x32_bf16 v[88:91], v[150:153], v[202:205], v[88:91]
	v_mfma_f32_16x16x32_bf16 v[84:87], v[138:141], v[224:227], v[84:87]
	v_mfma_f32_16x16x32_bf16 v[72:75], v[150:153], v[224:227], v[72:75]
	v_mfma_f32_16x16x32_bf16 v[124:127], v[146:149], v[178:181], v[124:127]
	v_mfma_f32_16x16x32_bf16 v[120:123], v[154:157], v[178:181], v[120:123]
	v_mfma_f32_16x16x32_bf16 v[116:119], v[146:149], v[198:201], v[116:119]
	v_mfma_f32_16x16x32_bf16 v[104:107], v[154:157], v[198:201], v[104:107]
	v_mfma_f32_16x16x32_bf16 v[100:103], v[146:149], v[206:209], v[100:103]
	v_mfma_f32_16x16x32_bf16 v[88:91], v[154:157], v[206:209], v[88:91]
	v_mfma_f32_16x16x32_bf16 v[84:87], v[146:149], v[228:231], v[84:87]
	v_mfma_f32_16x16x32_bf16 v[72:75], v[154:157], v[228:231], v[72:75]
	s_setprio 0
	s_setprio 1
	v_mfma_f32_16x16x32_bf16 v[112:115], v[158:161], v[174:177], v[112:115]
	v_mfma_f32_16x16x32_bf16 v[108:111], v[166:169], v[174:177], v[108:111]
	v_mfma_f32_16x16x32_bf16 v[96:99], v[158:161], v[194:197], v[96:99]
	v_mfma_f32_16x16x32_bf16 v[92:95], v[166:169], v[194:197], v[92:95]
	v_mfma_f32_16x16x32_bf16 v[80:83], v[158:161], v[202:205], v[80:83]
	v_mfma_f32_16x16x32_bf16 v[76:79], v[166:169], v[202:205], v[76:79]
	v_mfma_f32_16x16x32_bf16 v[68:71], v[158:161], v[224:227], v[68:71]
	v_mfma_f32_16x16x32_bf16 v[64:67], v[166:169], v[224:227], v[64:67]
	v_mfma_f32_16x16x32_bf16 v[112:115], v[162:165], v[178:181], v[112:115]
	v_mfma_f32_16x16x32_bf16 v[108:111], v[170:173], v[178:181], v[108:111]
	v_mfma_f32_16x16x32_bf16 v[96:99], v[162:165], v[198:201], v[96:99]
	v_mfma_f32_16x16x32_bf16 v[92:95], v[170:173], v[198:201], v[92:95]
	v_mfma_f32_16x16x32_bf16 v[80:83], v[162:165], v[206:209], v[80:83]
	v_mfma_f32_16x16x32_bf16 v[76:79], v[170:173], v[206:209], v[76:79]
	v_mfma_f32_16x16x32_bf16 v[68:71], v[162:165], v[228:231], v[68:71]
	v_mfma_f32_16x16x32_bf16 v[64:67], v[170:173], v[228:231], v[64:67]
	s_setprio 0
	s_barrier
	s_add_i32 s28, s38, s20
	v_lshl_add_u64 v[182:183], v[182:183], 0, s[68:69]
	s_mov_b32 m0, s28
	ds_read_b128 v[174:177], v145 offset:49152
	ds_read_b128 v[178:181], v145 offset:50176
	ds_read_b128 v[194:197], v145 offset:51200
	ds_read_b128 v[198:201], v145 offset:52224
	ds_read_b128 v[202:205], v145 offset:53248
	ds_read_b128 v[206:209], v145 offset:54272
	ds_read_b128 v[224:227], v145 offset:55296
	ds_read_b128 v[228:231], v145 offset:56320
	global_load_lds_dwordx4 v[182:183], off
	s_add_i32 m0, s28, 0x2000
	s_add_u32 s28, s40, 0x80080
	v_lshl_add_u64 v[182:183], v[210:211], 0, s[68:69]
	s_addc_u32 s29, s41, 0
	s_add_i32 s38, s39, s20
	global_load_lds_dwordx4 v[182:183], off
	v_lshl_add_u64 v[182:183], s[28:29], 0, v[184:185]
	s_mov_b32 m0, s38
	s_nop 0
	global_load_lds_dwordx4 v[182:183], off
	v_lshl_add_u64 v[182:183], s[28:29], 0, v[128:129]
	s_add_i32 m0, s38, 0x2000
	s_nop 0
	global_load_lds_dwordx4 v[182:183], off
	v_lshl_add_u64 v[182:183], v[216:217], 0, s[68:69]
	s_mov_b32 m0, s51
	s_nop 0
	global_load_lds_dwordx4 v[182:183], off
	v_lshl_add_u64 v[182:183], v[218:219], 0, s[68:69]
	s_mov_b32 m0, s52
	s_nop 0
	global_load_lds_dwordx4 v[182:183], off
	s_waitcnt vmcnt(6)
	s_waitcnt lgkmcnt(0)
	s_barrier
	s_setprio 1
	s_waitcnt lgkmcnt(0)
	v_mfma_f32_16x16x32_bf16 v[60:63], v[138:141], v[174:177], v[60:63]
	v_mfma_f32_16x16x32_bf16 v[56:59], v[150:153], v[174:177], v[56:59]
	v_mfma_f32_16x16x32_bf16 v[52:55], v[138:141], v[194:197], v[52:55]
	v_mfma_f32_16x16x32_bf16 v[40:43], v[150:153], v[194:197], v[40:43]
	v_mfma_f32_16x16x32_bf16 v[36:39], v[138:141], v[202:205], v[36:39]
	v_mfma_f32_16x16x32_bf16 v[24:27], v[150:153], v[202:205], v[24:27]
	v_mfma_f32_16x16x32_bf16 v[20:23], v[138:141], v[224:227], v[20:23]
	v_mfma_f32_16x16x32_bf16 v[8:11], v[150:153], v[224:227], v[8:11]
	v_mfma_f32_16x16x32_bf16 v[60:63], v[146:149], v[178:181], v[60:63]
	v_mfma_f32_16x16x32_bf16 v[56:59], v[154:157], v[178:181], v[56:59]
	v_mfma_f32_16x16x32_bf16 v[52:55], v[146:149], v[198:201], v[52:55]
	v_mfma_f32_16x16x32_bf16 v[40:43], v[154:157], v[198:201], v[40:43]
	v_mfma_f32_16x16x32_bf16 v[36:39], v[146:149], v[206:209], v[36:39]
	v_mfma_f32_16x16x32_bf16 v[24:27], v[154:157], v[206:209], v[24:27]
	v_mfma_f32_16x16x32_bf16 v[20:23], v[146:149], v[228:231], v[20:23]
	v_mfma_f32_16x16x32_bf16 v[8:11], v[154:157], v[228:231], v[8:11]
	s_setprio 0
	s_setprio 1
	v_mfma_f32_16x16x32_bf16 v[48:51], v[158:161], v[174:177], v[48:51]
	v_mfma_f32_16x16x32_bf16 v[44:47], v[166:169], v[174:177], v[44:47]
	v_mfma_f32_16x16x32_bf16 v[32:35], v[158:161], v[194:197], v[32:35]
	v_mfma_f32_16x16x32_bf16 v[28:31], v[166:169], v[194:197], v[28:31]
	v_mfma_f32_16x16x32_bf16 v[16:19], v[158:161], v[202:205], v[16:19]
	v_mfma_f32_16x16x32_bf16 v[12:15], v[166:169], v[202:205], v[12:15]
	v_mfma_f32_16x16x32_bf16 v[4:7], v[158:161], v[224:227], v[4:7]
	v_mfma_f32_16x16x32_bf16 v[0:3], v[166:169], v[224:227], v[0:3]
	v_mfma_f32_16x16x32_bf16 v[48:51], v[162:165], v[178:181], v[48:51]
	v_mfma_f32_16x16x32_bf16 v[44:47], v[170:173], v[178:181], v[44:47]
	v_mfma_f32_16x16x32_bf16 v[32:35], v[162:165], v[198:201], v[32:35]
	v_mfma_f32_16x16x32_bf16 v[28:31], v[170:173], v[198:201], v[28:31]
	v_mfma_f32_16x16x32_bf16 v[16:19], v[162:165], v[206:209], v[16:19]
	v_mfma_f32_16x16x32_bf16 v[12:15], v[170:173], v[206:209], v[12:15]
	v_mfma_f32_16x16x32_bf16 v[4:7], v[162:165], v[228:231], v[4:7]
	v_mfma_f32_16x16x32_bf16 v[0:3], v[170:173], v[228:231], v[0:3]
	s_setprio 0
	s_barrier
	s_add_i32 s78, s78, 2
	s_add_u32 s30, s30, 0x100
	s_addc_u32 s31, s31, 0
	s_add_u32 s62, s62, 0x100
	s_addc_u32 s63, s63, 0
	s_cmp_gt_u32 s78, 29
	s_cbranch_scc0 .LBB0_805
	s_and_b64 vcc, exec, s[6:7]
	s_cbranch_vccz .LBB0_808
	s_barrier

.LBB0_842:
	s_add_u32 s28, s30, 0xfffc0080
	s_addc_u32 s29, s31, -1
	s_add_i32 s42, 0, 0x10000
	s_cmp_eq_u32 s60, 12
	s_cselect_b32 s45, s9, s29
	s_cselect_b32 s44, s11, s28
	s_cselect_b32 s41, s36, s59
	s_cselect_b32 s40, s37, s58
	s_add_i32 s43, 0, 0x14000
	v_add_u32_e32 v154, s42, v147
	v_add_u32_e32 v170, s43, v147
	ds_read_b128 v[138:141], v154
	ds_read_b128 v[142:145], v154 offset:1024
	ds_read_b128 v[150:153], v154 offset:2048
	ds_read_b128 v[154:157], v154 offset:3072
	ds_read_b128 v[158:161], v170
	ds_read_b128 v[162:165], v170 offset:1024
	ds_read_b128 v[166:169], v170 offset:2048
	ds_read_b128 v[170:173], v170 offset:3072
	v_lshl_add_u64 v[182:183], s[30:31], 0, v[134:135]
	s_add_i32 m0, s21, 0xc000
	ds_read_b128 v[174:177], v149
	ds_read_b128 v[178:181], v149 offset:1024
	ds_read_b128 v[194:197], v149 offset:2048
	ds_read_b128 v[198:201], v149 offset:3072
	ds_read_b128 v[202:205], v149 offset:4096
	ds_read_b128 v[206:209], v149 offset:5120
	ds_read_b128 v[224:227], v149 offset:6144
	ds_read_b128 v[228:231], v149 offset:7168
	global_load_lds_dwordx4 v[182:183], off
	v_lshl_add_u64 v[182:183], s[30:31], 0, v[136:137]
	s_add_i32 m0, s21, 0xe000
	s_nop 0
	global_load_lds_dwordx4 v[182:183], off
	s_waitcnt vmcnt(8)
	s_waitcnt lgkmcnt(0)
	s_barrier
	s_setprio 1
	s_waitcnt lgkmcnt(0)
	v_mfma_f32_16x16x32_bf16 v[124:127], v[138:141], v[174:177], v[124:127]
	v_mfma_f32_16x16x32_bf16 v[120:123], v[150:153], v[174:177], v[120:123]
	v_mfma_f32_16x16x32_bf16 v[108:111], v[138:141], v[194:197], v[108:111]
	v_mfma_f32_16x16x32_bf16 v[104:107], v[150:153], v[194:197], v[104:107]
	v_mfma_f32_16x16x32_bf16 v[92:95], v[138:141], v[202:205], v[92:95]
	v_mfma_f32_16x16x32_bf16 v[88:91], v[150:153], v[202:205], v[88:91]
	v_mfma_f32_16x16x32_bf16 v[76:79], v[138:141], v[224:227], v[76:79]
	v_mfma_f32_16x16x32_bf16 v[72:75], v[150:153], v[224:227], v[72:75]
	v_mfma_f32_16x16x32_bf16 v[124:127], v[142:145], v[178:181], v[124:127]
	v_mfma_f32_16x16x32_bf16 v[120:123], v[154:157], v[178:181], v[120:123]
	v_mfma_f32_16x16x32_bf16 v[108:111], v[142:145], v[198:201], v[108:111]
	v_mfma_f32_16x16x32_bf16 v[104:107], v[154:157], v[198:201], v[104:107]
	v_mfma_f32_16x16x32_bf16 v[92:95], v[142:145], v[206:209], v[92:95]
	v_mfma_f32_16x16x32_bf16 v[88:91], v[154:157], v[206:209], v[88:91]
	v_mfma_f32_16x16x32_bf16 v[76:79], v[142:145], v[228:231], v[76:79]
	v_mfma_f32_16x16x32_bf16 v[72:75], v[154:157], v[228:231], v[72:75]
	s_setprio 0
	s_setprio 1
	v_mfma_f32_16x16x32_bf16 v[116:119], v[158:161], v[174:177], v[116:119]
	v_mfma_f32_16x16x32_bf16 v[112:115], v[166:169], v[174:177], v[112:115]
	v_mfma_f32_16x16x32_bf16 v[100:103], v[158:161], v[194:197], v[100:103]
	v_mfma_f32_16x16x32_bf16 v[96:99], v[166:169], v[194:197], v[96:99]
	v_mfma_f32_16x16x32_bf16 v[84:87], v[158:161], v[202:205], v[84:87]
	v_mfma_f32_16x16x32_bf16 v[80:83], v[166:169], v[202:205], v[80:83]
	v_mfma_f32_16x16x32_bf16 v[68:71], v[158:161], v[224:227], v[68:71]
	v_mfma_f32_16x16x32_bf16 v[64:67], v[166:169], v[224:227], v[64:67]
	v_mfma_f32_16x16x32_bf16 v[116:119], v[162:165], v[178:181], v[116:119]
	v_mfma_f32_16x16x32_bf16 v[112:115], v[170:173], v[178:181], v[112:115]
	v_mfma_f32_16x16x32_bf16 v[100:103], v[162:165], v[198:201], v[100:103]
	v_mfma_f32_16x16x32_bf16 v[96:99], v[170:173], v[198:201], v[96:99]
	v_mfma_f32_16x16x32_bf16 v[84:87], v[162:165], v[206:209], v[84:87]
	v_mfma_f32_16x16x32_bf16 v[80:83], v[170:173], v[206:209], v[80:83]
	v_mfma_f32_16x16x32_bf16 v[68:71], v[162:165], v[228:231], v[68:71]
	v_mfma_f32_16x16x32_bf16 v[64:67], v[170:173], v[228:231], v[64:67]
	s_setprio 0
	s_barrier
	s_add_i32 s28, s42, s20
	v_lshl_add_u64 v[182:183], s[40:41], 0, v[184:185]
	s_mov_b32 m0, s28
	ds_read_b128 v[174:177], v149 offset:16384
	ds_read_b128 v[178:181], v149 offset:17408
	ds_read_b128 v[194:197], v149 offset:18432
	ds_read_b128 v[198:201], v149 offset:19456
	ds_read_b128 v[202:205], v149 offset:20480
	ds_read_b128 v[206:209], v149 offset:21504
	ds_read_b128 v[224:227], v149 offset:22528
	ds_read_b128 v[228:231], v149 offset:23552
	global_load_lds_dwordx4 v[182:183], off
	s_add_i32 m0, s28, 0x2000
	s_add_u32 s28, s40, 0x40000
	v_lshl_add_u64 v[210:211], s[40:41], 0, v[128:129]
	s_addc_u32 s29, s41, 0
	s_add_i32 s42, s43, s20
	global_load_lds_dwordx4 v[210:211], off
	v_lshl_add_u64 v[216:217], s[28:29], 0, v[184:185]
	s_mov_b32 m0, s42
	v_lshl_add_u64 v[218:219], s[44:45], 0, v[130:131]
	global_load_lds_dwordx4 v[216:217], off
	v_lshl_add_u64 v[216:217], s[28:29], 0, v[128:129]
	s_add_i32 m0, s42, 0x2000
	s_nop 0
	global_load_lds_dwordx4 v[216:217], off
	v_lshl_add_u64 v[216:217], s[44:45], 0, v[132:133]
	s_waitcnt vmcnt(6)
	s_waitcnt lgkmcnt(0)
	s_barrier
	s_setprio 1
	s_waitcnt lgkmcnt(0)
	v_mfma_f32_16x16x32_bf16 v[60:63], v[138:141], v[174:177], v[60:63]
	v_mfma_f32_16x16x32_bf16 v[56:59], v[150:153], v[174:177], v[56:59]
	v_mfma_f32_16x16x32_bf16 v[44:47], v[138:141], v[194:197], v[44:47]
	v_mfma_f32_16x16x32_bf16 v[40:43], v[150:153], v[194:197], v[40:43]
	v_mfma_f32_16x16x32_bf16 v[28:31], v[138:141], v[202:205], v[28:31]
	v_mfma_f32_16x16x32_bf16 v[24:27], v[150:153], v[202:205], v[24:27]
	v_mfma_f32_16x16x32_bf16 v[12:15], v[138:141], v[224:227], v[12:15]
	v_mfma_f32_16x16x32_bf16 v[8:11], v[150:153], v[224:227], v[8:11]
	v_mfma_f32_16x16x32_bf16 v[60:63], v[142:145], v[178:181], v[60:63]
	v_mfma_f32_16x16x32_bf16 v[56:59], v[154:157], v[178:181], v[56:59]
	v_mfma_f32_16x16x32_bf16 v[44:47], v[142:145], v[198:201], v[44:47]
	v_mfma_f32_16x16x32_bf16 v[40:43], v[154:157], v[198:201], v[40:43]
	v_mfma_f32_16x16x32_bf16 v[28:31], v[142:145], v[206:209], v[28:31]
	v_mfma_f32_16x16x32_bf16 v[24:27], v[154:157], v[206:209], v[24:27]
	v_mfma_f32_16x16x32_bf16 v[12:15], v[142:145], v[228:231], v[12:15]
	v_mfma_f32_16x16x32_bf16 v[8:11], v[154:157], v[228:231], v[8:11]
	s_setprio 0
	s_setprio 1
	v_mfma_f32_16x16x32_bf16 v[52:55], v[158:161], v[174:177], v[52:55]
	v_mfma_f32_16x16x32_bf16 v[48:51], v[166:169], v[174:177], v[48:51]
	v_mfma_f32_16x16x32_bf16 v[36:39], v[158:161], v[194:197], v[36:39]
	v_mfma_f32_16x16x32_bf16 v[32:35], v[166:169], v[194:197], v[32:35]
	v_mfma_f32_16x16x32_bf16 v[20:23], v[158:161], v[202:205], v[20:23]
	v_mfma_f32_16x16x32_bf16 v[16:19], v[166:169], v[202:205], v[16:19]
	v_mfma_f32_16x16x32_bf16 v[4:7], v[158:161], v[224:227], v[4:7]
	v_mfma_f32_16x16x32_bf16 v[0:3], v[166:169], v[224:227], v[0:3]
	v_mfma_f32_16x16x32_bf16 v[52:55], v[162:165], v[178:181], v[52:55]
	v_mfma_f32_16x16x32_bf16 v[48:51], v[170:173], v[178:181], v[48:51]
	v_mfma_f32_16x16x32_bf16 v[36:39], v[162:165], v[198:201], v[36:39]
	v_mfma_f32_16x16x32_bf16 v[32:35], v[170:173], v[198:201], v[32:35]
	v_mfma_f32_16x16x32_bf16 v[20:23], v[162:165], v[206:209], v[20:23]
	v_mfma_f32_16x16x32_bf16 v[16:19], v[170:173], v[206:209], v[16:19]
	v_mfma_f32_16x16x32_bf16 v[4:7], v[162:165], v[228:231], v[4:7]
	v_mfma_f32_16x16x32_bf16 v[0:3], v[170:173], v[228:231], v[0:3]
	s_setprio 0
	s_barrier
	s_add_i32 s42, 0, 0x18000
	s_add_i32 s43, 0, 0x1c000
	v_add_u32_e32 v154, s42, v147
	v_add_u32_e32 v170, s43, v147
	ds_read_b128 v[138:141], v154
	ds_read_b128 v[142:145], v154 offset:1024
	ds_read_b128 v[150:153], v154 offset:2048
	ds_read_b128 v[154:157], v154 offset:3072
	ds_read_b128 v[158:161], v170
	ds_read_b128 v[162:165], v170 offset:1024
	ds_read_b128 v[166:169], v170 offset:2048
	ds_read_b128 v[170:173], v170 offset:3072
	s_add_u32 s28, s44, 0x40000
	s_addc_u32 s29, s45, 0
	s_mov_b32 m0, s27
	v_lshl_add_u64 v[232:233], s[28:29], 0, v[132:133]
	ds_read_b128 v[174:177], v149 offset:32768
	ds_read_b128 v[178:181], v149 offset:33792
	ds_read_b128 v[194:197], v149 offset:34816
	ds_read_b128 v[198:201], v149 offset:35840
	ds_read_b128 v[202:205], v149 offset:36864
	ds_read_b128 v[206:209], v149 offset:37888
	ds_read_b128 v[224:227], v149 offset:38912
	ds_read_b128 v[228:231], v149 offset:39936
	global_load_lds_dwordx4 v[232:233], off
	v_lshl_add_u64 v[232:233], s[28:29], 0, v[130:131]
	s_mov_b32 m0, s46
	s_nop 0
	global_load_lds_dwordx4 v[232:233], off
	s_mov_b32 m0, s21
	s_nop 0
	global_load_lds_dwordx4 v[216:217], off
	s_mov_b32 m0, s26
	s_nop 0
	global_load_lds_dwordx4 v[218:219], off
	s_waitcnt vmcnt(8)
	s_waitcnt lgkmcnt(0)
	s_barrier
	s_setprio 1
	s_waitcnt lgkmcnt(0)
	v_mfma_f32_16x16x32_bf16 v[124:127], v[138:141], v[174:177], v[124:127]
	v_mfma_f32_16x16x32_bf16 v[120:123], v[150:153], v[174:177], v[120:123]
	v_mfma_f32_16x16x32_bf16 v[108:111], v[138:141], v[194:197], v[108:111]
	v_mfma_f32_16x16x32_bf16 v[104:107], v[150:153], v[194:197], v[104:107]
	v_mfma_f32_16x16x32_bf16 v[92:95], v[138:141], v[202:205], v[92:95]
	v_mfma_f32_16x16x32_bf16 v[88:91], v[150:153], v[202:205], v[88:91]
	v_mfma_f32_16x16x32_bf16 v[76:79], v[138:141], v[224:227], v[76:79]
	v_mfma_f32_16x16x32_bf16 v[72:75], v[150:153], v[224:227], v[72:75]
	v_mfma_f32_16x16x32_bf16 v[124:127], v[142:145], v[178:181], v[124:127]
	v_mfma_f32_16x16x32_bf16 v[120:123], v[154:157], v[178:181], v[120:123]
	v_mfma_f32_16x16x32_bf16 v[108:111], v[142:145], v[198:201], v[108:111]
	v_mfma_f32_16x16x32_bf16 v[104:107], v[154:157], v[198:201], v[104:107]
	v_mfma_f32_16x16x32_bf16 v[92:95], v[142:145], v[206:209], v[92:95]
	v_mfma_f32_16x16x32_bf16 v[88:91], v[154:157], v[206:209], v[88:91]
	v_mfma_f32_16x16x32_bf16 v[76:79], v[142:145], v[228:231], v[76:79]
	v_mfma_f32_16x16x32_bf16 v[72:75], v[154:157], v[228:231], v[72:75]
	s_setprio 0
	s_setprio 1
	v_mfma_f32_16x16x32_bf16 v[116:119], v[158:161], v[174:177], v[116:119]
	v_mfma_f32_16x16x32_bf16 v[112:115], v[166:169], v[174:177], v[112:115]
	v_mfma_f32_16x16x32_bf16 v[100:103], v[158:161], v[194:197], v[100:103]
	v_mfma_f32_16x16x32_bf16 v[96:99], v[166:169], v[194:197], v[96:99]
	v_mfma_f32_16x16x32_bf16 v[84:87], v[158:161], v[202:205], v[84:87]
	v_mfma_f32_16x16x32_bf16 v[80:83], v[166:169], v[202:205], v[80:83]
	v_mfma_f32_16x16x32_bf16 v[68:71], v[158:161], v[224:227], v[68:71]
	v_mfma_f32_16x16x32_bf16 v[64:67], v[166:169], v[224:227], v[64:67]
	v_mfma_f32_16x16x32_bf16 v[116:119], v[162:165], v[178:181], v[116:119]
	v_mfma_f32_16x16x32_bf16 v[112:115], v[170:173], v[178:181], v[112:115]
	v_mfma_f32_16x16x32_bf16 v[100:103], v[162:165], v[198:201], v[100:103]
	v_mfma_f32_16x16x32_bf16 v[96:99], v[170:173], v[198:201], v[96:99]
	v_mfma_f32_16x16x32_bf16 v[84:87], v[162:165], v[206:209], v[84:87]
	v_mfma_f32_16x16x32_bf16 v[80:83], v[170:173], v[206:209], v[80:83]
	v_mfma_f32_16x16x32_bf16 v[68:71], v[162:165], v[228:231], v[68:71]
	v_mfma_f32_16x16x32_bf16 v[64:67], v[170:173], v[228:231], v[64:67]
	s_setprio 0
	s_barrier
	s_add_i32 s28, s42, s20
	v_lshl_add_u64 v[182:183], v[182:183], 0, s[68:69]
	s_mov_b32 m0, s28
	ds_read_b128 v[174:177], v149 offset:49152
	ds_read_b128 v[178:181], v149 offset:50176
	ds_read_b128 v[194:197], v149 offset:51200
	ds_read_b128 v[198:201], v149 offset:52224
	ds_read_b128 v[202:205], v149 offset:53248
	ds_read_b128 v[206:209], v149 offset:54272
	ds_read_b128 v[224:227], v149 offset:55296
	ds_read_b128 v[228:231], v149 offset:56320
	global_load_lds_dwordx4 v[182:183], off
	s_add_i32 m0, s28, 0x2000
	s_add_u32 s28, s40, 0x40080
	v_lshl_add_u64 v[182:183], v[210:211], 0, s[68:69]
	s_addc_u32 s29, s41, 0
	s_add_i32 s40, s43, s20
	global_load_lds_dwordx4 v[182:183], off
	v_lshl_add_u64 v[182:183], s[28:29], 0, v[184:185]
	s_mov_b32 m0, s40
	s_nop 0
	global_load_lds_dwordx4 v[182:183], off
	v_lshl_add_u64 v[182:183], s[28:29], 0, v[128:129]
	s_add_i32 m0, s40, 0x2000
	s_nop 0
	global_load_lds_dwordx4 v[182:183], off
	v_lshl_add_u64 v[182:183], v[216:217], 0, s[68:69]
	s_mov_b32 m0, s47
	s_nop 0
	global_load_lds_dwordx4 v[182:183], off
	v_lshl_add_u64 v[182:183], v[218:219], 0, s[68:69]
	s_mov_b32 m0, s50
	s_nop 0
	global_load_lds_dwordx4 v[182:183], off
	s_waitcnt vmcnt(6)
	s_waitcnt lgkmcnt(0)
	s_barrier
	s_setprio 1
	s_waitcnt lgkmcnt(0)
	v_mfma_f32_16x16x32_bf16 v[60:63], v[138:141], v[174:177], v[60:63]
	v_mfma_f32_16x16x32_bf16 v[56:59], v[150:153], v[174:177], v[56:59]
	v_mfma_f32_16x16x32_bf16 v[44:47], v[138:141], v[194:197], v[44:47]
	v_mfma_f32_16x16x32_bf16 v[40:43], v[150:153], v[194:197], v[40:43]
	v_mfma_f32_16x16x32_bf16 v[28:31], v[138:141], v[202:205], v[28:31]
	v_mfma_f32_16x16x32_bf16 v[24:27], v[150:153], v[202:205], v[24:27]
	v_mfma_f32_16x16x32_bf16 v[12:15], v[138:141], v[224:227], v[12:15]
	v_mfma_f32_16x16x32_bf16 v[8:11], v[150:153], v[224:227], v[8:11]
	v_mfma_f32_16x16x32_bf16 v[60:63], v[142:145], v[178:181], v[60:63]
	v_mfma_f32_16x16x32_bf16 v[56:59], v[154:157], v[178:181], v[56:59]
	v_mfma_f32_16x16x32_bf16 v[44:47], v[142:145], v[198:201], v[44:47]
	v_mfma_f32_16x16x32_bf16 v[40:43], v[154:157], v[198:201], v[40:43]
	v_mfma_f32_16x16x32_bf16 v[28:31], v[142:145], v[206:209], v[28:31]
	v_mfma_f32_16x16x32_bf16 v[24:27], v[154:157], v[206:209], v[24:27]
	v_mfma_f32_16x16x32_bf16 v[12:15], v[142:145], v[228:231], v[12:15]
	v_mfma_f32_16x16x32_bf16 v[8:11], v[154:157], v[228:231], v[8:11]
	s_setprio 0
	s_setprio 1
	v_mfma_f32_16x16x32_bf16 v[52:55], v[158:161], v[174:177], v[52:55]
	v_mfma_f32_16x16x32_bf16 v[48:51], v[166:169], v[174:177], v[48:51]
	v_mfma_f32_16x16x32_bf16 v[36:39], v[158:161], v[194:197], v[36:39]
	v_mfma_f32_16x16x32_bf16 v[32:35], v[166:169], v[194:197], v[32:35]
	v_mfma_f32_16x16x32_bf16 v[20:23], v[158:161], v[202:205], v[20:23]
	v_mfma_f32_16x16x32_bf16 v[16:19], v[166:169], v[202:205], v[16:19]
	v_mfma_f32_16x16x32_bf16 v[4:7], v[158:161], v[224:227], v[4:7]
	v_mfma_f32_16x16x32_bf16 v[0:3], v[166:169], v[224:227], v[0:3]
	v_mfma_f32_16x16x32_bf16 v[52:55], v[162:165], v[178:181], v[52:55]
	v_mfma_f32_16x16x32_bf16 v[48:51], v[170:173], v[178:181], v[48:51]
	v_mfma_f32_16x16x32_bf16 v[36:39], v[162:165], v[198:201], v[36:39]
	v_mfma_f32_16x16x32_bf16 v[32:35], v[170:173], v[198:201], v[32:35]
	v_mfma_f32_16x16x32_bf16 v[20:23], v[162:165], v[206:209], v[20:23]
	v_mfma_f32_16x16x32_bf16 v[16:19], v[170:173], v[206:209], v[16:19]
	v_mfma_f32_16x16x32_bf16 v[4:7], v[162:165], v[228:231], v[4:7]
	v_mfma_f32_16x16x32_bf16 v[0:3], v[170:173], v[228:231], v[0:3]
	s_setprio 0
	s_barrier
	s_add_i32 s60, s60, 2
	s_add_u32 s30, s30, 0x100
	s_addc_u32 s31, s31, 0
	s_add_u32 s58, s58, 0x100
	s_addc_u32 s59, s59, 0
	s_cmp_gt_u32 s60, 13
	s_cbranch_scc0 .LBB0_842
	s_and_b64 vcc, exec, s[6:7]
	s_cbranch_vccz .LBB0_845
	s_barrier

.LBB0_991:
	s_add_u32 s28, s40, 0xfff80080
	s_addc_u32 s29, s41, -1
	s_add_i32 s48, 0, 0x10000
	s_cmp_eq_u32 s79, 28
	s_cselect_b32 s45, s11, s29
	s_cselect_b32 s44, s13, s28
	s_cselect_b32 s43, s60, s63
	s_cselect_b32 s42, s61, s62
	s_add_i32 s49, 0, 0x14000
	s_waitcnt vmcnt(0)
	v_add_u32_e32 v60, s48, v169
	v_add_u32_e32 v166, s49, v169
	ds_read_b128 v[40:43], v60
	ds_read_b128 v[44:47], v60 offset:1024
	ds_read_b128 v[56:59], v60 offset:2048
	ds_read_b128 v[60:63], v60 offset:3072
	ds_read_b128 v[144:147], v166
	ds_read_b128 v[148:151], v166 offset:1024
	ds_read_b128 v[162:165], v166 offset:2048
	ds_read_b128 v[172:175], v166 offset:3072
	v_lshl_add_u64 v[166:167], s[40:41], 0, v[158:159]
	s_add_i32 m0, s26, 0xc000
	ds_read_b128 v[176:179], v171
	ds_read_b128 v[180:183], v171 offset:1024
	ds_read_b128 v[194:197], v171 offset:2048
	ds_read_b128 v[198:201], v171 offset:3072
	ds_read_b128 v[202:205], v171 offset:4096
	ds_read_b128 v[206:209], v171 offset:5120
	ds_read_b128 v[224:227], v171 offset:6144
	ds_read_b128 v[228:231], v171 offset:7168
	global_load_lds_dwordx4 v[166:167], off
	v_lshl_add_u64 v[166:167], s[40:41], 0, v[160:161]
	s_add_i32 m0, s26, 0xe000
	s_nop 0
	global_load_lds_dwordx4 v[166:167], off
	s_waitcnt vmcnt(8)
	s_waitcnt lgkmcnt(0)
	s_barrier
	s_setprio 1
	s_waitcnt lgkmcnt(0)
	v_mfma_f32_16x16x32_bf16 v[140:143], v[40:43], v[176:179], v[140:143]
	v_mfma_f32_16x16x32_bf16 v[136:139], v[56:59], v[176:179], v[136:139]
	v_mfma_f32_16x16x32_bf16 v[124:127], v[40:43], v[194:197], v[124:127]
	v_mfma_f32_16x16x32_bf16 v[120:123], v[56:59], v[194:197], v[120:123]
	v_mfma_f32_16x16x32_bf16 v[108:111], v[40:43], v[202:205], v[108:111]
	v_mfma_f32_16x16x32_bf16 v[104:107], v[56:59], v[202:205], v[104:107]
	v_mfma_f32_16x16x32_bf16 v[92:95], v[40:43], v[224:227], v[92:95]
	v_mfma_f32_16x16x32_bf16 v[88:91], v[56:59], v[224:227], v[88:91]
	v_mfma_f32_16x16x32_bf16 v[140:143], v[44:47], v[180:183], v[140:143]
	v_mfma_f32_16x16x32_bf16 v[136:139], v[60:63], v[180:183], v[136:139]
	v_mfma_f32_16x16x32_bf16 v[124:127], v[44:47], v[198:201], v[124:127]
	v_mfma_f32_16x16x32_bf16 v[120:123], v[60:63], v[198:201], v[120:123]
	v_mfma_f32_16x16x32_bf16 v[108:111], v[44:47], v[206:209], v[108:111]
	v_mfma_f32_16x16x32_bf16 v[104:107], v[60:63], v[206:209], v[104:107]
	v_mfma_f32_16x16x32_bf16 v[92:95], v[44:47], v[228:231], v[92:95]
	v_mfma_f32_16x16x32_bf16 v[88:91], v[60:63], v[228:231], v[88:91]
	s_setprio 0
	s_setprio 1
	v_mfma_f32_16x16x32_bf16 v[132:135], v[144:147], v[176:179], v[132:135]
	v_mfma_f32_16x16x32_bf16 v[128:131], v[162:165], v[176:179], v[128:131]
	v_mfma_f32_16x16x32_bf16 v[116:119], v[144:147], v[194:197], v[116:119]
	v_mfma_f32_16x16x32_bf16 v[112:115], v[162:165], v[194:197], v[112:115]
	v_mfma_f32_16x16x32_bf16 v[100:103], v[144:147], v[202:205], v[100:103]
	v_mfma_f32_16x16x32_bf16 v[96:99], v[162:165], v[202:205], v[96:99]
	v_mfma_f32_16x16x32_bf16 v[84:87], v[144:147], v[224:227], v[84:87]
	v_mfma_f32_16x16x32_bf16 v[80:83], v[162:165], v[224:227], v[80:83]
	v_mfma_f32_16x16x32_bf16 v[132:135], v[148:151], v[180:183], v[132:135]
	v_mfma_f32_16x16x32_bf16 v[128:131], v[172:175], v[180:183], v[128:131]
	v_mfma_f32_16x16x32_bf16 v[116:119], v[148:151], v[198:201], v[116:119]
	v_mfma_f32_16x16x32_bf16 v[112:115], v[172:175], v[198:201], v[112:115]
	v_mfma_f32_16x16x32_bf16 v[100:103], v[148:151], v[206:209], v[100:103]
	v_mfma_f32_16x16x32_bf16 v[96:99], v[172:175], v[206:209], v[96:99]
	v_mfma_f32_16x16x32_bf16 v[84:87], v[148:151], v[228:231], v[84:87]
	v_mfma_f32_16x16x32_bf16 v[80:83], v[172:175], v[228:231], v[80:83]
	s_setprio 0
	s_barrier
	s_add_i32 s28, s48, s46
	v_lshl_add_u64 v[166:167], s[42:43], 0, v[184:185]
	s_mov_b32 m0, s28
	ds_read_b128 v[176:179], v171 offset:16384
	ds_read_b128 v[180:183], v171 offset:17408
	ds_read_b128 v[194:197], v171 offset:18432
	ds_read_b128 v[198:201], v171 offset:19456
	ds_read_b128 v[202:205], v171 offset:20480
	ds_read_b128 v[206:209], v171 offset:21504
	ds_read_b128 v[224:227], v171 offset:22528
	ds_read_b128 v[228:231], v171 offset:23552
	global_load_lds_dwordx4 v[166:167], off
	s_add_i32 m0, s28, 0x2000
	s_add_u32 s28, s42, 0x80000
	v_lshl_add_u64 v[210:211], s[42:43], 0, v[152:153]
	s_addc_u32 s29, s43, 0
	s_add_i32 s48, s49, s46
	global_load_lds_dwordx4 v[210:211], off
	v_lshl_add_u64 v[216:217], s[28:29], 0, v[184:185]
	s_mov_b32 m0, s48
	v_lshl_add_u64 v[218:219], s[44:45], 0, v[154:155]
	global_load_lds_dwordx4 v[216:217], off
	v_lshl_add_u64 v[216:217], s[28:29], 0, v[152:153]
	s_add_i32 m0, s48, 0x2000
	s_nop 0
	global_load_lds_dwordx4 v[216:217], off
	v_lshl_add_u64 v[216:217], s[44:45], 0, v[156:157]
	s_waitcnt vmcnt(6)
	s_waitcnt lgkmcnt(0)
	s_barrier
	s_setprio 1
	s_waitcnt lgkmcnt(0)
	v_mfma_f32_16x16x32_bf16 v[76:79], v[40:43], v[176:179], v[76:79]
	v_mfma_f32_16x16x32_bf16 v[72:75], v[56:59], v[176:179], v[72:75]
	v_mfma_f32_16x16x32_bf16 v[52:55], v[40:43], v[194:197], v[52:55]
	v_mfma_f32_16x16x32_bf16 v[48:51], v[56:59], v[194:197], v[48:51]
	v_mfma_f32_16x16x32_bf16 v[28:31], v[40:43], v[202:205], v[28:31]
	v_mfma_f32_16x16x32_bf16 v[24:27], v[56:59], v[202:205], v[24:27]
	v_mfma_f32_16x16x32_bf16 v[12:15], v[40:43], v[224:227], v[12:15]
	v_mfma_f32_16x16x32_bf16 v[8:11], v[56:59], v[224:227], v[8:11]
	v_mfma_f32_16x16x32_bf16 v[76:79], v[44:47], v[180:183], v[76:79]
	v_mfma_f32_16x16x32_bf16 v[72:75], v[60:63], v[180:183], v[72:75]
	v_mfma_f32_16x16x32_bf16 v[52:55], v[44:47], v[198:201], v[52:55]
	v_mfma_f32_16x16x32_bf16 v[48:51], v[60:63], v[198:201], v[48:51]
	v_mfma_f32_16x16x32_bf16 v[28:31], v[44:47], v[206:209], v[28:31]
	v_mfma_f32_16x16x32_bf16 v[24:27], v[60:63], v[206:209], v[24:27]
	v_mfma_f32_16x16x32_bf16 v[12:15], v[44:47], v[228:231], v[12:15]
	v_mfma_f32_16x16x32_bf16 v[8:11], v[60:63], v[228:231], v[8:11]
	s_setprio 0
	s_setprio 1
	v_mfma_f32_16x16x32_bf16 v[36:39], v[144:147], v[194:197], v[36:39]
	v_mfma_f32_16x16x32_bf16 v[32:35], v[162:165], v[194:197], v[32:35]
	v_mfma_f32_16x16x32_bf16 v[20:23], v[144:147], v[202:205], v[20:23]
	v_mfma_f32_16x16x32_bf16 v[16:19], v[162:165], v[202:205], v[16:19]
	v_mfma_f32_16x16x32_bf16 v[4:7], v[144:147], v[224:227], v[4:7]
	v_mfma_f32_16x16x32_bf16 v[0:3], v[162:165], v[224:227], v[0:3]
	v_mfma_f32_16x16x32_bf16 v[40:43], v[144:147], v[176:179], v[68:71]
	v_mfma_f32_16x16x32_bf16 v[44:47], v[162:165], v[176:179], v[64:67]
	v_mfma_f32_16x16x32_bf16 v[36:39], v[148:151], v[198:201], v[36:39]
	v_mfma_f32_16x16x32_bf16 v[32:35], v[172:175], v[198:201], v[32:35]
	v_mfma_f32_16x16x32_bf16 v[20:23], v[148:151], v[206:209], v[20:23]
	v_mfma_f32_16x16x32_bf16 v[16:19], v[172:175], v[206:209], v[16:19]
	v_mfma_f32_16x16x32_bf16 v[4:7], v[148:151], v[228:231], v[4:7]
	v_mfma_f32_16x16x32_bf16 v[0:3], v[172:175], v[228:231], v[0:3]
	v_mfma_f32_16x16x32_bf16 v[40:43], v[148:151], v[180:183], v[40:43]
	v_mfma_f32_16x16x32_bf16 v[44:47], v[172:175], v[180:183], v[44:47]
	s_setprio 0
	s_barrier
	s_add_i32 s48, 0, 0x18000
	s_add_i32 s49, 0, 0x1c000
	v_add_u32_e32 v68, s48, v169
	v_add_u32_e32 v172, s49, v169
	ds_read_b128 v[56:59], v68
	ds_read_b128 v[60:63], v68 offset:1024
	ds_read_b128 v[64:67], v68 offset:2048
	ds_read_b128 v[68:71], v68 offset:3072
	ds_read_b128 v[144:147], v172
	ds_read_b128 v[148:151], v172 offset:1024
	ds_read_b128 v[162:165], v172 offset:2048
	ds_read_b128 v[172:175], v172 offset:3072
	s_add_u32 s28, s44, 0x80000
	s_addc_u32 s29, s45, 0
	s_mov_b32 m0, s47
	v_lshl_add_u64 v[232:233], s[28:29], 0, v[156:157]
	ds_read_b128 v[176:179], v171 offset:32768
	ds_read_b128 v[180:183], v171 offset:33792
	ds_read_b128 v[194:197], v171 offset:34816
	ds_read_b128 v[198:201], v171 offset:35840
	ds_read_b128 v[202:205], v171 offset:36864
	ds_read_b128 v[206:209], v171 offset:37888
	ds_read_b128 v[224:227], v171 offset:38912
	ds_read_b128 v[228:231], v171 offset:39936
	global_load_lds_dwordx4 v[232:233], off
	v_lshl_add_u64 v[232:233], s[28:29], 0, v[154:155]
	s_mov_b32 m0, s50
	s_nop 0
	global_load_lds_dwordx4 v[232:233], off
	s_mov_b32 m0, s26
	s_nop 0
	global_load_lds_dwordx4 v[216:217], off
	s_mov_b32 m0, s27
	s_nop 0
	global_load_lds_dwordx4 v[218:219], off
	s_waitcnt vmcnt(8)
	s_waitcnt lgkmcnt(0)
	s_barrier
	s_setprio 1
	s_waitcnt lgkmcnt(0)
	v_mfma_f32_16x16x32_bf16 v[140:143], v[56:59], v[176:179], v[140:143]
	v_mfma_f32_16x16x32_bf16 v[136:139], v[64:67], v[176:179], v[136:139]
	v_mfma_f32_16x16x32_bf16 v[124:127], v[56:59], v[194:197], v[124:127]
	v_mfma_f32_16x16x32_bf16 v[120:123], v[64:67], v[194:197], v[120:123]
	v_mfma_f32_16x16x32_bf16 v[108:111], v[56:59], v[202:205], v[108:111]
	v_mfma_f32_16x16x32_bf16 v[104:107], v[64:67], v[202:205], v[104:107]
	v_mfma_f32_16x16x32_bf16 v[92:95], v[56:59], v[224:227], v[92:95]
	v_mfma_f32_16x16x32_bf16 v[88:91], v[64:67], v[224:227], v[88:91]
	v_mfma_f32_16x16x32_bf16 v[140:143], v[60:63], v[180:183], v[140:143]
	v_mfma_f32_16x16x32_bf16 v[136:139], v[68:71], v[180:183], v[136:139]
	v_mfma_f32_16x16x32_bf16 v[124:127], v[60:63], v[198:201], v[124:127]
	v_mfma_f32_16x16x32_bf16 v[120:123], v[68:71], v[198:201], v[120:123]
	v_mfma_f32_16x16x32_bf16 v[108:111], v[60:63], v[206:209], v[108:111]
	v_mfma_f32_16x16x32_bf16 v[104:107], v[68:71], v[206:209], v[104:107]
	v_mfma_f32_16x16x32_bf16 v[92:95], v[60:63], v[228:231], v[92:95]
	v_mfma_f32_16x16x32_bf16 v[88:91], v[68:71], v[228:231], v[88:91]
	s_setprio 0
	s_setprio 1
	v_mfma_f32_16x16x32_bf16 v[132:135], v[144:147], v[176:179], v[132:135]
	v_mfma_f32_16x16x32_bf16 v[128:131], v[162:165], v[176:179], v[128:131]
	v_mfma_f32_16x16x32_bf16 v[116:119], v[144:147], v[194:197], v[116:119]
	v_mfma_f32_16x16x32_bf16 v[112:115], v[162:165], v[194:197], v[112:115]
	v_mfma_f32_16x16x32_bf16 v[100:103], v[144:147], v[202:205], v[100:103]
	v_mfma_f32_16x16x32_bf16 v[96:99], v[162:165], v[202:205], v[96:99]
	v_mfma_f32_16x16x32_bf16 v[84:87], v[144:147], v[224:227], v[84:87]
	v_mfma_f32_16x16x32_bf16 v[80:83], v[162:165], v[224:227], v[80:83]
	v_mfma_f32_16x16x32_bf16 v[132:135], v[148:151], v[180:183], v[132:135]
	v_mfma_f32_16x16x32_bf16 v[128:131], v[172:175], v[180:183], v[128:131]
	v_mfma_f32_16x16x32_bf16 v[116:119], v[148:151], v[198:201], v[116:119]
	v_mfma_f32_16x16x32_bf16 v[112:115], v[172:175], v[198:201], v[112:115]
	v_mfma_f32_16x16x32_bf16 v[100:103], v[148:151], v[206:209], v[100:103]
	v_mfma_f32_16x16x32_bf16 v[96:99], v[172:175], v[206:209], v[96:99]
	v_mfma_f32_16x16x32_bf16 v[84:87], v[148:151], v[228:231], v[84:87]
	v_mfma_f32_16x16x32_bf16 v[80:83], v[172:175], v[228:231], v[80:83]
	s_setprio 0
	s_barrier
	s_add_i32 s28, s48, s46
	v_lshl_add_u64 v[166:167], v[166:167], 0, s[68:69]
	s_mov_b32 m0, s28
	ds_read_b128 v[176:179], v171 offset:49152
	ds_read_b128 v[180:183], v171 offset:50176
	ds_read_b128 v[194:197], v171 offset:51200
	ds_read_b128 v[198:201], v171 offset:52224
	ds_read_b128 v[202:205], v171 offset:53248
	ds_read_b128 v[206:209], v171 offset:54272
	ds_read_b128 v[224:227], v171 offset:55296
	ds_read_b128 v[228:231], v171 offset:56320
	global_load_lds_dwordx4 v[166:167], off
	s_add_i32 m0, s28, 0x2000
	s_add_u32 s28, s42, 0x80080
	v_lshl_add_u64 v[166:167], v[210:211], 0, s[68:69]
	s_addc_u32 s29, s43, 0
	s_add_i32 s42, s49, s46
	global_load_lds_dwordx4 v[166:167], off
	v_lshl_add_u64 v[166:167], s[28:29], 0, v[184:185]
	s_mov_b32 m0, s42
	s_nop 0
	global_load_lds_dwordx4 v[166:167], off
	v_lshl_add_u64 v[166:167], s[28:29], 0, v[152:153]
	s_add_i32 m0, s42, 0x2000
	s_nop 0
	global_load_lds_dwordx4 v[166:167], off
	v_lshl_add_u64 v[166:167], v[216:217], 0, s[68:69]
	s_mov_b32 m0, s53
	s_nop 0
	global_load_lds_dwordx4 v[166:167], off
	v_lshl_add_u64 v[166:167], v[218:219], 0, s[68:69]
	s_mov_b32 m0, s58
	s_nop 0
	global_load_lds_dwordx4 v[166:167], off
	s_waitcnt vmcnt(6)
	s_waitcnt lgkmcnt(0)
	s_barrier
	s_setprio 1
	s_waitcnt lgkmcnt(0)
	v_mfma_f32_16x16x32_bf16 v[76:79], v[56:59], v[176:179], v[76:79]
	v_mfma_f32_16x16x32_bf16 v[72:75], v[64:67], v[176:179], v[72:75]
	v_mfma_f32_16x16x32_bf16 v[52:55], v[56:59], v[194:197], v[52:55]
	v_mfma_f32_16x16x32_bf16 v[48:51], v[64:67], v[194:197], v[48:51]
	v_mfma_f32_16x16x32_bf16 v[28:31], v[56:59], v[202:205], v[28:31]
	v_mfma_f32_16x16x32_bf16 v[24:27], v[64:67], v[202:205], v[24:27]
	v_mfma_f32_16x16x32_bf16 v[12:15], v[56:59], v[224:227], v[12:15]
	v_mfma_f32_16x16x32_bf16 v[8:11], v[64:67], v[224:227], v[8:11]
	v_mfma_f32_16x16x32_bf16 v[76:79], v[60:63], v[180:183], v[76:79]
	v_mfma_f32_16x16x32_bf16 v[72:75], v[68:71], v[180:183], v[72:75]
	v_mfma_f32_16x16x32_bf16 v[52:55], v[60:63], v[198:201], v[52:55]
	v_mfma_f32_16x16x32_bf16 v[48:51], v[68:71], v[198:201], v[48:51]
	v_mfma_f32_16x16x32_bf16 v[28:31], v[60:63], v[206:209], v[28:31]
	v_mfma_f32_16x16x32_bf16 v[24:27], v[68:71], v[206:209], v[24:27]
	v_mfma_f32_16x16x32_bf16 v[12:15], v[60:63], v[228:231], v[12:15]
	v_mfma_f32_16x16x32_bf16 v[8:11], v[68:71], v[228:231], v[8:11]
	s_setprio 0
	s_setprio 1
	v_mfma_f32_16x16x32_bf16 v[40:43], v[144:147], v[176:179], v[40:43]
	v_mfma_f32_16x16x32_bf16 v[68:71], v[148:151], v[180:183], v[40:43]
	v_mfma_f32_16x16x32_bf16 v[40:43], v[162:165], v[176:179], v[44:47]
	v_mfma_f32_16x16x32_bf16 v[36:39], v[144:147], v[194:197], v[36:39]
	v_mfma_f32_16x16x32_bf16 v[32:35], v[162:165], v[194:197], v[32:35]
	v_mfma_f32_16x16x32_bf16 v[20:23], v[144:147], v[202:205], v[20:23]
	v_mfma_f32_16x16x32_bf16 v[16:19], v[162:165], v[202:205], v[16:19]
	v_mfma_f32_16x16x32_bf16 v[4:7], v[144:147], v[224:227], v[4:7]
	v_mfma_f32_16x16x32_bf16 v[0:3], v[162:165], v[224:227], v[0:3]
	v_mfma_f32_16x16x32_bf16 v[64:67], v[172:175], v[180:183], v[40:43]
	v_mfma_f32_16x16x32_bf16 v[36:39], v[148:151], v[198:201], v[36:39]
	v_mfma_f32_16x16x32_bf16 v[32:35], v[172:175], v[198:201], v[32:35]
	v_mfma_f32_16x16x32_bf16 v[20:23], v[148:151], v[206:209], v[20:23]
	v_mfma_f32_16x16x32_bf16 v[16:19], v[172:175], v[206:209], v[16:19]
	v_mfma_f32_16x16x32_bf16 v[4:7], v[148:151], v[228:231], v[4:7]
	v_mfma_f32_16x16x32_bf16 v[0:3], v[172:175], v[228:231], v[0:3]
	s_setprio 0
	s_barrier
	s_add_i32 s79, s79, 2
	s_add_u32 s40, s40, 0x100
	s_addc_u32 s41, s41, 0
	s_add_u32 s62, s62, 0x100
	s_addc_u32 s63, s63, 0
	s_cmp_gt_u32 s79, 29
	s_cbranch_scc0 .LBB0_991
	s_and_b64 vcc, exec, s[8:9]
	s_cbranch_vccz .LBB0_994
	s_barrier

.LBB0_1419:
	s_add_u32 s28, s24, 0xfff80080
	s_addc_u32 s29, s25, -1
	s_add_i32 s48, 0, 0x10000
	s_cmp_eq_u32 s17, 28
	s_cselect_b32 s31, s9, s29
	s_cselect_b32 s30, s11, s28
	s_cselect_b64 vcc, -1, 0
	s_add_i32 s28, 0, 0x14000
	v_add_u32_e32 v164, s48, v147
	v_add_u32_e32 v180, s28, v147
	ds_read_b128 v[152:155], v164
	ds_read_b128 v[156:159], v164 offset:1024
	ds_read_b128 v[160:163], v164 offset:2048
	ds_read_b128 v[164:167], v164 offset:3072
	ds_read_b128 v[168:171], v180
	ds_read_b128 v[172:175], v180 offset:1024
	ds_read_b128 v[176:179], v180 offset:2048
	ds_read_b128 v[180:183], v180 offset:3072
	v_cndmask_b32_e32 v211, v145, v150, vcc
	v_cndmask_b32_e32 v210, v144, v151, vcc
	v_lshl_add_u64 v[216:217], s[24:25], 0, v[136:137]
	s_add_i32 m0, s19, 0xc000
	ds_read_b128 v[194:197], v149
	ds_read_b128 v[198:201], v149 offset:1024
	ds_read_b128 v[202:205], v149 offset:2048
	ds_read_b128 v[206:209], v149 offset:3072
	ds_read_b128 v[224:227], v149 offset:4096
	ds_read_b128 v[228:231], v149 offset:5120
	ds_read_b128 v[232:235], v149 offset:6144
	ds_read_b128 v[236:239], v149 offset:7168
	global_load_lds_dwordx4 v[216:217], off
	v_lshl_add_u64 v[216:217], s[24:25], 0, v[138:139]
	s_add_i32 m0, s19, 0xe000
	s_nop 0
	global_load_lds_dwordx4 v[216:217], off
	s_waitcnt vmcnt(8)
	s_waitcnt lgkmcnt(0)
	s_barrier
	s_setprio 1
	s_waitcnt lgkmcnt(0)
	v_mfma_f32_16x16x32_bf16 v[124:127], v[152:155], v[194:197], v[124:127]
	v_mfma_f32_16x16x32_bf16 v[116:119], v[160:163], v[194:197], v[116:119]
	v_mfma_f32_16x16x32_bf16 v[108:111], v[152:155], v[202:205], v[108:111]
	v_mfma_f32_16x16x32_bf16 v[100:103], v[160:163], v[202:205], v[100:103]
	v_mfma_f32_16x16x32_bf16 v[92:95], v[152:155], v[224:227], v[92:95]
	v_mfma_f32_16x16x32_bf16 v[84:87], v[160:163], v[224:227], v[84:87]
	v_mfma_f32_16x16x32_bf16 v[76:79], v[152:155], v[232:235], v[76:79]
	v_mfma_f32_16x16x32_bf16 v[68:71], v[160:163], v[232:235], v[68:71]
	v_mfma_f32_16x16x32_bf16 v[124:127], v[156:159], v[198:201], v[124:127]
	v_mfma_f32_16x16x32_bf16 v[116:119], v[164:167], v[198:201], v[116:119]
	v_mfma_f32_16x16x32_bf16 v[108:111], v[156:159], v[206:209], v[108:111]
	v_mfma_f32_16x16x32_bf16 v[100:103], v[164:167], v[206:209], v[100:103]
	v_mfma_f32_16x16x32_bf16 v[92:95], v[156:159], v[228:231], v[92:95]
	v_mfma_f32_16x16x32_bf16 v[84:87], v[164:167], v[228:231], v[84:87]
	v_mfma_f32_16x16x32_bf16 v[76:79], v[156:159], v[236:239], v[76:79]
	v_mfma_f32_16x16x32_bf16 v[68:71], v[164:167], v[236:239], v[68:71]
	s_setprio 0
	s_setprio 1
	v_mfma_f32_16x16x32_bf16 v[120:123], v[168:171], v[194:197], v[120:123]
	v_mfma_f32_16x16x32_bf16 v[112:115], v[176:179], v[194:197], v[112:115]
	v_mfma_f32_16x16x32_bf16 v[104:107], v[168:171], v[202:205], v[104:107]
	v_mfma_f32_16x16x32_bf16 v[96:99], v[176:179], v[202:205], v[96:99]
	v_mfma_f32_16x16x32_bf16 v[88:91], v[168:171], v[224:227], v[88:91]
	v_mfma_f32_16x16x32_bf16 v[80:83], v[176:179], v[224:227], v[80:83]
	v_mfma_f32_16x16x32_bf16 v[72:75], v[168:171], v[232:235], v[72:75]
	v_mfma_f32_16x16x32_bf16 v[64:67], v[176:179], v[232:235], v[64:67]
	v_mfma_f32_16x16x32_bf16 v[120:123], v[172:175], v[198:201], v[120:123]
	v_mfma_f32_16x16x32_bf16 v[112:115], v[180:183], v[198:201], v[112:115]
	v_mfma_f32_16x16x32_bf16 v[104:107], v[172:175], v[206:209], v[104:107]
	v_mfma_f32_16x16x32_bf16 v[96:99], v[180:183], v[206:209], v[96:99]
	v_mfma_f32_16x16x32_bf16 v[88:91], v[172:175], v[228:231], v[88:91]
	v_mfma_f32_16x16x32_bf16 v[80:83], v[180:183], v[228:231], v[80:83]
	v_mfma_f32_16x16x32_bf16 v[72:75], v[172:175], v[236:239], v[72:75]
	v_mfma_f32_16x16x32_bf16 v[64:67], v[180:183], v[236:239], v[64:67]
	s_setprio 0
	s_barrier
	s_add_i32 s29, s48, s50
	v_lshl_add_u64 v[216:217], v[210:211], 0, v[130:131]
	s_mov_b32 m0, s29
	ds_read_b128 v[194:197], v149 offset:16384
	ds_read_b128 v[198:201], v149 offset:17408
	ds_read_b128 v[202:205], v149 offset:18432
	ds_read_b128 v[206:209], v149 offset:19456
	ds_read_b128 v[224:227], v149 offset:20480
	ds_read_b128 v[228:231], v149 offset:21504
	ds_read_b128 v[232:235], v149 offset:22528
	ds_read_b128 v[236:239], v149 offset:23552
	global_load_lds_dwordx4 v[216:217], off
	v_lshl_add_u64 v[218:219], v[210:211], 0, v[134:135]
	s_add_i32 m0, s29, 0x2000
	v_lshl_add_u64 v[220:221], v[210:211], 0, s[72:73]
	s_add_i32 s28, s28, s50
	global_load_lds_dwordx4 v[218:219], off
	v_lshl_add_u64 v[240:241], v[220:221], 0, v[130:131]
	s_mov_b32 m0, s28
	v_lshl_add_u64 v[220:221], v[220:221], 0, v[134:135]
	global_load_lds_dwordx4 v[240:241], off
	s_add_i32 m0, s28, 0x2000
	v_lshl_add_u64 v[240:241], s[30:31], 0, v[132:133]
	global_load_lds_dwordx4 v[220:221], off
	v_lshl_add_u64 v[220:221], s[30:31], 0, v[128:129]
	s_waitcnt vmcnt(6)
	s_waitcnt lgkmcnt(0)
	s_barrier
	s_setprio 1
	s_waitcnt lgkmcnt(0)
	v_mfma_f32_16x16x32_bf16 v[60:63], v[152:155], v[194:197], v[60:63]
	v_mfma_f32_16x16x32_bf16 v[52:55], v[160:163], v[194:197], v[52:55]
	v_mfma_f32_16x16x32_bf16 v[44:47], v[152:155], v[202:205], v[44:47]
	v_mfma_f32_16x16x32_bf16 v[36:39], v[160:163], v[202:205], v[36:39]
	v_mfma_f32_16x16x32_bf16 v[28:31], v[152:155], v[224:227], v[28:31]
	v_mfma_f32_16x16x32_bf16 v[20:23], v[160:163], v[224:227], v[20:23]
	v_mfma_f32_16x16x32_bf16 v[12:15], v[152:155], v[232:235], v[12:15]
	v_mfma_f32_16x16x32_bf16 v[4:7], v[160:163], v[232:235], v[4:7]
	v_mfma_f32_16x16x32_bf16 v[60:63], v[156:159], v[198:201], v[60:63]
	v_mfma_f32_16x16x32_bf16 v[52:55], v[164:167], v[198:201], v[52:55]
	v_mfma_f32_16x16x32_bf16 v[44:47], v[156:159], v[206:209], v[44:47]
	v_mfma_f32_16x16x32_bf16 v[36:39], v[164:167], v[206:209], v[36:39]
	v_mfma_f32_16x16x32_bf16 v[28:31], v[156:159], v[228:231], v[28:31]
	v_mfma_f32_16x16x32_bf16 v[20:23], v[164:167], v[228:231], v[20:23]
	v_mfma_f32_16x16x32_bf16 v[12:15], v[156:159], v[236:239], v[12:15]
	v_mfma_f32_16x16x32_bf16 v[4:7], v[164:167], v[236:239], v[4:7]
	s_setprio 0
	s_setprio 1
	v_mfma_f32_16x16x32_bf16 v[56:59], v[168:171], v[194:197], v[56:59]
	v_mfma_f32_16x16x32_bf16 v[48:51], v[176:179], v[194:197], v[48:51]
	v_mfma_f32_16x16x32_bf16 v[40:43], v[168:171], v[202:205], v[40:43]
	v_mfma_f32_16x16x32_bf16 v[32:35], v[176:179], v[202:205], v[32:35]
	v_mfma_f32_16x16x32_bf16 v[24:27], v[168:171], v[224:227], v[24:27]
	v_mfma_f32_16x16x32_bf16 v[16:19], v[176:179], v[224:227], v[16:19]
	v_mfma_f32_16x16x32_bf16 v[8:11], v[168:171], v[232:235], v[8:11]
	v_mfma_f32_16x16x32_bf16 v[0:3], v[176:179], v[232:235], v[0:3]
	v_mfma_f32_16x16x32_bf16 v[56:59], v[172:175], v[198:201], v[56:59]
	v_mfma_f32_16x16x32_bf16 v[48:51], v[180:183], v[198:201], v[48:51]
	v_mfma_f32_16x16x32_bf16 v[40:43], v[172:175], v[206:209], v[40:43]
	v_mfma_f32_16x16x32_bf16 v[32:35], v[180:183], v[206:209], v[32:35]
	v_mfma_f32_16x16x32_bf16 v[24:27], v[172:175], v[228:231], v[24:27]
	v_mfma_f32_16x16x32_bf16 v[16:19], v[180:183], v[228:231], v[16:19]
	v_mfma_f32_16x16x32_bf16 v[8:11], v[172:175], v[236:239], v[8:11]
	v_mfma_f32_16x16x32_bf16 v[0:3], v[180:183], v[236:239], v[0:3]
	s_setprio 0
	s_barrier
	s_add_i32 s48, 0, 0x18000
	s_add_i32 s49, 0, 0x1c000
	v_add_u32_e32 v164, s48, v147
	v_add_u32_e32 v180, s49, v147
	ds_read_b128 v[152:155], v164
	ds_read_b128 v[156:159], v164 offset:1024
	ds_read_b128 v[160:163], v164 offset:2048
	ds_read_b128 v[164:167], v164 offset:3072
	ds_read_b128 v[168:171], v180
	ds_read_b128 v[172:175], v180 offset:1024
	ds_read_b128 v[176:179], v180 offset:2048
	ds_read_b128 v[180:183], v180 offset:3072
	s_add_u32 s28, s30, 0x80000
	s_addc_u32 s29, s31, 0
	s_mov_b32 m0, s52
	v_lshl_add_u64 v[242:243], s[28:29], 0, v[128:129]
	ds_read_b128 v[194:197], v149 offset:32768
	ds_read_b128 v[198:201], v149 offset:33792
	ds_read_b128 v[202:205], v149 offset:34816
	ds_read_b128 v[206:209], v149 offset:35840
	ds_read_b128 v[224:227], v149 offset:36864
	ds_read_b128 v[228:231], v149 offset:37888
	ds_read_b128 v[232:235], v149 offset:38912
	ds_read_b128 v[236:239], v149 offset:39936
	global_load_lds_dwordx4 v[242:243], off
	v_lshl_add_u64 v[242:243], s[28:29], 0, v[132:133]
	s_mov_b32 m0, s53
	s_nop 0
	global_load_lds_dwordx4 v[242:243], off
	s_mov_b32 m0, s19
	s_nop 0
	global_load_lds_dwordx4 v[220:221], off
	s_mov_b32 m0, s51
	s_nop 0
	global_load_lds_dwordx4 v[240:241], off
	s_waitcnt vmcnt(8)
	s_waitcnt lgkmcnt(0)
	s_barrier
	s_setprio 1
	s_waitcnt lgkmcnt(0)
	v_mfma_f32_16x16x32_bf16 v[124:127], v[152:155], v[194:197], v[124:127]
	v_mfma_f32_16x16x32_bf16 v[116:119], v[160:163], v[194:197], v[116:119]
	v_mfma_f32_16x16x32_bf16 v[108:111], v[152:155], v[202:205], v[108:111]
	v_mfma_f32_16x16x32_bf16 v[100:103], v[160:163], v[202:205], v[100:103]
	v_mfma_f32_16x16x32_bf16 v[92:95], v[152:155], v[224:227], v[92:95]
	v_mfma_f32_16x16x32_bf16 v[84:87], v[160:163], v[224:227], v[84:87]
	v_mfma_f32_16x16x32_bf16 v[76:79], v[152:155], v[232:235], v[76:79]
	v_mfma_f32_16x16x32_bf16 v[68:71], v[160:163], v[232:235], v[68:71]
	v_mfma_f32_16x16x32_bf16 v[124:127], v[156:159], v[198:201], v[124:127]
	v_mfma_f32_16x16x32_bf16 v[116:119], v[164:167], v[198:201], v[116:119]
	v_mfma_f32_16x16x32_bf16 v[108:111], v[156:159], v[206:209], v[108:111]
	v_mfma_f32_16x16x32_bf16 v[100:103], v[164:167], v[206:209], v[100:103]
	v_mfma_f32_16x16x32_bf16 v[92:95], v[156:159], v[228:231], v[92:95]
	v_mfma_f32_16x16x32_bf16 v[84:87], v[164:167], v[228:231], v[84:87]
	v_mfma_f32_16x16x32_bf16 v[76:79], v[156:159], v[236:239], v[76:79]
	v_mfma_f32_16x16x32_bf16 v[68:71], v[164:167], v[236:239], v[68:71]
	s_setprio 0
	s_setprio 1
	v_mfma_f32_16x16x32_bf16 v[120:123], v[168:171], v[194:197], v[120:123]
	v_mfma_f32_16x16x32_bf16 v[112:115], v[176:179], v[194:197], v[112:115]
	v_mfma_f32_16x16x32_bf16 v[104:107], v[168:171], v[202:205], v[104:107]
	v_mfma_f32_16x16x32_bf16 v[96:99], v[176:179], v[202:205], v[96:99]
	v_mfma_f32_16x16x32_bf16 v[88:91], v[168:171], v[224:227], v[88:91]
	v_mfma_f32_16x16x32_bf16 v[80:83], v[176:179], v[224:227], v[80:83]
	v_mfma_f32_16x16x32_bf16 v[72:75], v[168:171], v[232:235], v[72:75]
	v_mfma_f32_16x16x32_bf16 v[64:67], v[176:179], v[232:235], v[64:67]
	v_mfma_f32_16x16x32_bf16 v[120:123], v[172:175], v[198:201], v[120:123]
	v_mfma_f32_16x16x32_bf16 v[112:115], v[180:183], v[198:201], v[112:115]
	v_mfma_f32_16x16x32_bf16 v[104:107], v[172:175], v[206:209], v[104:107]
	v_mfma_f32_16x16x32_bf16 v[96:99], v[180:183], v[206:209], v[96:99]
	v_mfma_f32_16x16x32_bf16 v[88:91], v[172:175], v[228:231], v[88:91]
	v_mfma_f32_16x16x32_bf16 v[80:83], v[180:183], v[228:231], v[80:83]
	v_mfma_f32_16x16x32_bf16 v[72:75], v[172:175], v[236:239], v[72:75]
	v_mfma_f32_16x16x32_bf16 v[64:67], v[180:183], v[236:239], v[64:67]
	s_setprio 0
	s_barrier
	s_add_i32 s28, s48, s50
	v_lshl_add_u64 v[216:217], v[216:217], 0, s[68:69]
	s_mov_b32 m0, s28
	ds_read_b128 v[194:197], v149 offset:49152
	ds_read_b128 v[198:201], v149 offset:50176
	ds_read_b128 v[202:205], v149 offset:51200
	ds_read_b128 v[206:209], v149 offset:52224
	ds_read_b128 v[224:227], v149 offset:53248
	ds_read_b128 v[228:231], v149 offset:54272
	ds_read_b128 v[232:235], v149 offset:55296
	ds_read_b128 v[236:239], v149 offset:56320
	global_load_lds_dwordx4 v[216:217], off
	v_lshl_add_u64 v[216:217], v[218:219], 0, s[68:69]
	s_add_i32 m0, s28, 0x2000
	v_lshl_add_u64 v[210:211], v[210:211], 0, s[74:75]
	s_add_i32 s28, s49, s50
	global_load_lds_dwordx4 v[216:217], off
	v_lshl_add_u64 v[216:217], v[210:211], 0, v[130:131]
	s_mov_b32 m0, s28
	v_lshl_add_u64 v[210:211], v[210:211], 0, v[134:135]
	global_load_lds_dwordx4 v[216:217], off
	s_add_i32 m0, s28, 0x2000
	s_nop 0
	global_load_lds_dwordx4 v[210:211], off
	v_lshl_add_u64 v[210:211], v[220:221], 0, s[68:69]
	s_mov_b32 m0, s58
	s_nop 0
	global_load_lds_dwordx4 v[210:211], off
	v_lshl_add_u64 v[210:211], v[240:241], 0, s[68:69]
	s_mov_b32 m0, s59
	s_nop 0
	global_load_lds_dwordx4 v[210:211], off
	s_waitcnt vmcnt(6)
	s_waitcnt lgkmcnt(0)
	s_barrier
	s_setprio 1
	s_waitcnt lgkmcnt(0)
	v_mfma_f32_16x16x32_bf16 v[60:63], v[152:155], v[194:197], v[60:63]
	v_mfma_f32_16x16x32_bf16 v[52:55], v[160:163], v[194:197], v[52:55]
	v_mfma_f32_16x16x32_bf16 v[44:47], v[152:155], v[202:205], v[44:47]
	v_mfma_f32_16x16x32_bf16 v[36:39], v[160:163], v[202:205], v[36:39]
	v_mfma_f32_16x16x32_bf16 v[28:31], v[152:155], v[224:227], v[28:31]
	v_mfma_f32_16x16x32_bf16 v[20:23], v[160:163], v[224:227], v[20:23]
	v_mfma_f32_16x16x32_bf16 v[12:15], v[152:155], v[232:235], v[12:15]
	v_mfma_f32_16x16x32_bf16 v[4:7], v[160:163], v[232:235], v[4:7]
	v_mfma_f32_16x16x32_bf16 v[60:63], v[156:159], v[198:201], v[60:63]
	v_mfma_f32_16x16x32_bf16 v[52:55], v[164:167], v[198:201], v[52:55]
	v_mfma_f32_16x16x32_bf16 v[44:47], v[156:159], v[206:209], v[44:47]
	v_mfma_f32_16x16x32_bf16 v[36:39], v[164:167], v[206:209], v[36:39]
	v_mfma_f32_16x16x32_bf16 v[28:31], v[156:159], v[228:231], v[28:31]
	v_mfma_f32_16x16x32_bf16 v[20:23], v[164:167], v[228:231], v[20:23]
	v_mfma_f32_16x16x32_bf16 v[12:15], v[156:159], v[236:239], v[12:15]
	v_mfma_f32_16x16x32_bf16 v[4:7], v[164:167], v[236:239], v[4:7]
	s_setprio 0
	s_setprio 1
	v_mfma_f32_16x16x32_bf16 v[56:59], v[168:171], v[194:197], v[56:59]
	v_mfma_f32_16x16x32_bf16 v[48:51], v[176:179], v[194:197], v[48:51]
	v_mfma_f32_16x16x32_bf16 v[40:43], v[168:171], v[202:205], v[40:43]
	v_mfma_f32_16x16x32_bf16 v[32:35], v[176:179], v[202:205], v[32:35]
	v_mfma_f32_16x16x32_bf16 v[24:27], v[168:171], v[224:227], v[24:27]
	v_mfma_f32_16x16x32_bf16 v[16:19], v[176:179], v[224:227], v[16:19]
	v_mfma_f32_16x16x32_bf16 v[8:11], v[168:171], v[232:235], v[8:11]
	v_mfma_f32_16x16x32_bf16 v[0:3], v[176:179], v[232:235], v[0:3]
	v_mfma_f32_16x16x32_bf16 v[56:59], v[172:175], v[198:201], v[56:59]
	v_mfma_f32_16x16x32_bf16 v[48:51], v[180:183], v[198:201], v[48:51]
	v_mfma_f32_16x16x32_bf16 v[40:43], v[172:175], v[206:209], v[40:43]
	v_mfma_f32_16x16x32_bf16 v[32:35], v[180:183], v[206:209], v[32:35]
	v_mfma_f32_16x16x32_bf16 v[24:27], v[172:175], v[228:231], v[24:27]
	v_mfma_f32_16x16x32_bf16 v[16:19], v[180:183], v[228:231], v[16:19]
	v_mfma_f32_16x16x32_bf16 v[8:11], v[172:175], v[236:239], v[8:11]
	v_mfma_f32_16x16x32_bf16 v[0:3], v[180:183], v[236:239], v[0:3]
	s_setprio 0
	s_barrier
	s_add_i32 s17, s17, 2
	s_add_u32 s24, s24, 0x100
	s_addc_u32 s25, s25, 0
	s_cmp_gt_u32 s17, 29
	v_lshl_add_u64 v[144:145], v[144:145], 0, s[76:77]
	s_cbranch_scc0 .LBB0_1419
	s_and_b64 vcc, exec, s[6:7]
	s_cbranch_vccz .LBB0_1422
	s_barrier

.LBB0_1491:
	s_add_u32 s14, s12, 0x100
	s_addc_u32 s15, s13, 0
	s_add_i32 s28, 0, 0x10000
	s_cmp_eq_u32 s59, 40
	s_cselect_b32 s17, s53, s15
	s_cselect_b32 s16, s58, s14
	s_cselect_b64 vcc, -1, 0
	s_add_i32 s29, 0, 0x14000
	v_add_u32_e32 v164, s28, v147
	v_add_u32_e32 v180, s29, v147
	ds_read_b128 v[152:155], v164
	ds_read_b128 v[156:159], v164 offset:1024
	ds_read_b128 v[160:163], v164 offset:2048
	ds_read_b128 v[164:167], v164 offset:3072
	ds_read_b128 v[168:171], v180
	ds_read_b128 v[172:175], v180 offset:1024
	ds_read_b128 v[176:179], v180 offset:2048
	ds_read_b128 v[180:183], v180 offset:3072
	v_cndmask_b32_e32 v211, v145, v150, vcc
	v_cndmask_b32_e32 v210, v144, v151, vcc
	v_lshl_add_u64 v[216:217], s[12:13], 0, v[136:137]
	s_add_i32 m0, s40, 0xc000
	ds_read_b128 v[194:197], v149
	ds_read_b128 v[198:201], v149 offset:1024
	ds_read_b128 v[202:205], v149 offset:2048
	ds_read_b128 v[206:209], v149 offset:3072
	ds_read_b128 v[224:227], v149 offset:4096
	ds_read_b128 v[228:231], v149 offset:5120
	ds_read_b128 v[232:235], v149 offset:6144
	ds_read_b128 v[236:239], v149 offset:7168
	global_load_lds_dwordx4 v[216:217], off
	v_lshl_add_u64 v[216:217], s[12:13], 0, v[138:139]
	s_add_i32 m0, s40, 0xe000
	s_nop 0
	global_load_lds_dwordx4 v[216:217], off
	s_waitcnt vmcnt(8)
	s_waitcnt lgkmcnt(0)
	s_barrier
	s_setprio 1
	s_waitcnt lgkmcnt(0)
	v_mfma_f32_16x16x32_bf16 v[124:127], v[152:155], v[194:197], v[124:127]
	v_mfma_f32_16x16x32_bf16 v[120:123], v[160:163], v[194:197], v[120:123]
	v_mfma_f32_16x16x32_bf16 v[116:119], v[152:155], v[202:205], v[116:119]
	v_mfma_f32_16x16x32_bf16 v[108:111], v[160:163], v[202:205], v[108:111]
	v_mfma_f32_16x16x32_bf16 v[100:103], v[152:155], v[224:227], v[100:103]
	v_mfma_f32_16x16x32_bf16 v[92:95], v[160:163], v[224:227], v[92:95]
	v_mfma_f32_16x16x32_bf16 v[80:83], v[152:155], v[232:235], v[80:83]
	v_mfma_f32_16x16x32_bf16 v[72:75], v[160:163], v[232:235], v[72:75]
	v_mfma_f32_16x16x32_bf16 v[124:127], v[156:159], v[198:201], v[124:127]
	v_mfma_f32_16x16x32_bf16 v[120:123], v[164:167], v[198:201], v[120:123]
	v_mfma_f32_16x16x32_bf16 v[116:119], v[156:159], v[206:209], v[116:119]
	v_mfma_f32_16x16x32_bf16 v[108:111], v[164:167], v[206:209], v[108:111]
	v_mfma_f32_16x16x32_bf16 v[100:103], v[156:159], v[228:231], v[100:103]
	v_mfma_f32_16x16x32_bf16 v[92:95], v[164:167], v[228:231], v[92:95]
	v_mfma_f32_16x16x32_bf16 v[80:83], v[156:159], v[236:239], v[80:83]
	v_mfma_f32_16x16x32_bf16 v[72:75], v[164:167], v[236:239], v[72:75]
	s_setprio 0
	s_setprio 1
	v_mfma_f32_16x16x32_bf16 v[112:115], v[168:171], v[194:197], v[112:115]
	v_mfma_f32_16x16x32_bf16 v[104:107], v[176:179], v[194:197], v[104:107]
	v_mfma_f32_16x16x32_bf16 v[96:99], v[168:171], v[202:205], v[96:99]
	v_mfma_f32_16x16x32_bf16 v[88:91], v[176:179], v[202:205], v[88:91]
	v_mfma_f32_16x16x32_bf16 v[84:87], v[168:171], v[224:227], v[84:87]
	v_mfma_f32_16x16x32_bf16 v[76:79], v[176:179], v[224:227], v[76:79]
	v_mfma_f32_16x16x32_bf16 v[68:71], v[168:171], v[232:235], v[68:71]
	v_mfma_f32_16x16x32_bf16 v[64:67], v[176:179], v[232:235], v[64:67]
	v_mfma_f32_16x16x32_bf16 v[112:115], v[172:175], v[198:201], v[112:115]
	v_mfma_f32_16x16x32_bf16 v[104:107], v[180:183], v[198:201], v[104:107]
	v_mfma_f32_16x16x32_bf16 v[96:99], v[172:175], v[206:209], v[96:99]
	v_mfma_f32_16x16x32_bf16 v[88:91], v[180:183], v[206:209], v[88:91]
	v_mfma_f32_16x16x32_bf16 v[84:87], v[172:175], v[228:231], v[84:87]
	v_mfma_f32_16x16x32_bf16 v[76:79], v[180:183], v[228:231], v[76:79]
	v_mfma_f32_16x16x32_bf16 v[68:71], v[172:175], v[236:239], v[68:71]
	v_mfma_f32_16x16x32_bf16 v[64:67], v[180:183], v[236:239], v[64:67]
	s_setprio 0
	s_barrier
	s_add_i32 s12, s28, s30
	v_lshl_add_u64 v[216:217], v[210:211], 0, v[132:133]
	s_mov_b32 m0, s12
	ds_read_b128 v[194:197], v149 offset:16384
	ds_read_b128 v[198:201], v149 offset:17408
	ds_read_b128 v[202:205], v149 offset:18432
	ds_read_b128 v[206:209], v149 offset:19456
	ds_read_b128 v[224:227], v149 offset:20480
	ds_read_b128 v[228:231], v149 offset:21504
	ds_read_b128 v[232:235], v149 offset:22528
	ds_read_b128 v[236:239], v149 offset:23552
	global_load_lds_dwordx4 v[216:217], off
	v_lshl_add_u64 v[218:219], v[210:211], 0, v[128:129]
	s_add_i32 m0, s12, 0x2000
	v_lshl_add_u64 v[220:221], v[210:211], 0, s[72:73]
	s_add_i32 s12, s29, s30
	global_load_lds_dwordx4 v[218:219], off
	v_lshl_add_u64 v[240:241], v[220:221], 0, v[132:133]
	s_mov_b32 m0, s12
	v_lshl_add_u64 v[220:221], v[220:221], 0, v[128:129]
	global_load_lds_dwordx4 v[240:241], off
	s_add_i32 m0, s12, 0x2000
	v_lshl_add_u64 v[240:241], s[16:17], 0, v[130:131]
	global_load_lds_dwordx4 v[220:221], off
	v_lshl_add_u64 v[220:221], s[16:17], 0, v[134:135]
	s_waitcnt vmcnt(6)
	s_waitcnt lgkmcnt(0)
	s_barrier
	s_setprio 1
	s_waitcnt lgkmcnt(0)
	v_mfma_f32_16x16x32_bf16 v[60:63], v[152:155], v[194:197], v[60:63]
	v_mfma_f32_16x16x32_bf16 v[56:59], v[160:163], v[194:197], v[56:59]
	v_mfma_f32_16x16x32_bf16 v[52:55], v[152:155], v[202:205], v[52:55]
	v_mfma_f32_16x16x32_bf16 v[44:47], v[160:163], v[202:205], v[44:47]
	v_mfma_f32_16x16x32_bf16 v[36:39], v[152:155], v[224:227], v[36:39]
	v_mfma_f32_16x16x32_bf16 v[28:31], v[160:163], v[224:227], v[28:31]
	v_mfma_f32_16x16x32_bf16 v[20:23], v[152:155], v[232:235], v[20:23]
	v_mfma_f32_16x16x32_bf16 v[12:15], v[160:163], v[232:235], v[12:15]
	v_mfma_f32_16x16x32_bf16 v[60:63], v[156:159], v[198:201], v[60:63]
	v_mfma_f32_16x16x32_bf16 v[56:59], v[164:167], v[198:201], v[56:59]
	v_mfma_f32_16x16x32_bf16 v[52:55], v[156:159], v[206:209], v[52:55]
	v_mfma_f32_16x16x32_bf16 v[44:47], v[164:167], v[206:209], v[44:47]
	v_mfma_f32_16x16x32_bf16 v[36:39], v[156:159], v[228:231], v[36:39]
	v_mfma_f32_16x16x32_bf16 v[28:31], v[164:167], v[228:231], v[28:31]
	v_mfma_f32_16x16x32_bf16 v[20:23], v[156:159], v[236:239], v[20:23]
	v_mfma_f32_16x16x32_bf16 v[12:15], v[164:167], v[236:239], v[12:15]
	s_setprio 0
	s_setprio 1
	v_mfma_f32_16x16x32_bf16 v[48:51], v[168:171], v[194:197], v[48:51]
	v_mfma_f32_16x16x32_bf16 v[40:43], v[176:179], v[194:197], v[40:43]
	v_mfma_f32_16x16x32_bf16 v[32:35], v[168:171], v[202:205], v[32:35]
	v_mfma_f32_16x16x32_bf16 v[24:27], v[176:179], v[202:205], v[24:27]
	v_mfma_f32_16x16x32_bf16 v[16:19], v[168:171], v[224:227], v[16:19]
	v_mfma_f32_16x16x32_bf16 v[8:11], v[176:179], v[224:227], v[8:11]
	v_mfma_f32_16x16x32_bf16 v[4:7], v[168:171], v[232:235], v[4:7]
	v_mfma_f32_16x16x32_bf16 v[0:3], v[176:179], v[232:235], v[0:3]
	v_mfma_f32_16x16x32_bf16 v[48:51], v[172:175], v[198:201], v[48:51]
	v_mfma_f32_16x16x32_bf16 v[40:43], v[180:183], v[198:201], v[40:43]
	v_mfma_f32_16x16x32_bf16 v[32:35], v[172:175], v[206:209], v[32:35]
	v_mfma_f32_16x16x32_bf16 v[24:27], v[180:183], v[206:209], v[24:27]
	v_mfma_f32_16x16x32_bf16 v[16:19], v[172:175], v[228:231], v[16:19]
	v_mfma_f32_16x16x32_bf16 v[8:11], v[180:183], v[228:231], v[8:11]
	v_mfma_f32_16x16x32_bf16 v[4:7], v[172:175], v[236:239], v[4:7]
	v_mfma_f32_16x16x32_bf16 v[0:3], v[180:183], v[236:239], v[0:3]
	s_setprio 0
	s_barrier
	s_add_i32 s28, 0, 0x18000
	s_add_i32 s29, 0, 0x1c000
	v_add_u32_e32 v164, s28, v147
	v_add_u32_e32 v180, s29, v147
	ds_read_b128 v[152:155], v164
	ds_read_b128 v[156:159], v164 offset:1024
	ds_read_b128 v[160:163], v164 offset:2048
	ds_read_b128 v[164:167], v164 offset:3072
	ds_read_b128 v[168:171], v180
	ds_read_b128 v[172:175], v180 offset:1024
	ds_read_b128 v[176:179], v180 offset:2048
	ds_read_b128 v[180:183], v180 offset:3072
	s_add_u32 s12, s16, 0xb0000
	s_addc_u32 s13, s17, 0
	s_mov_b32 m0, s42
	v_lshl_add_u64 v[242:243], s[12:13], 0, v[134:135]
	ds_read_b128 v[194:197], v149 offset:32768
	ds_read_b128 v[198:201], v149 offset:33792
	ds_read_b128 v[202:205], v149 offset:34816
	ds_read_b128 v[206:209], v149 offset:35840
	ds_read_b128 v[224:227], v149 offset:36864
	ds_read_b128 v[228:231], v149 offset:37888
	ds_read_b128 v[232:235], v149 offset:38912
	ds_read_b128 v[236:239], v149 offset:39936
	global_load_lds_dwordx4 v[242:243], off
	v_lshl_add_u64 v[242:243], s[12:13], 0, v[130:131]
	s_mov_b32 m0, s43
	s_nop 0
	global_load_lds_dwordx4 v[242:243], off
	s_mov_b32 m0, s40
	s_nop 0
	global_load_lds_dwordx4 v[220:221], off
	s_mov_b32 m0, s41
	s_nop 0
	global_load_lds_dwordx4 v[240:241], off
	s_waitcnt vmcnt(8)
	s_waitcnt lgkmcnt(0)
	s_barrier
	s_setprio 1
	s_waitcnt lgkmcnt(0)
	v_mfma_f32_16x16x32_bf16 v[124:127], v[152:155], v[194:197], v[124:127]
	v_mfma_f32_16x16x32_bf16 v[120:123], v[160:163], v[194:197], v[120:123]
	v_mfma_f32_16x16x32_bf16 v[116:119], v[152:155], v[202:205], v[116:119]
	v_mfma_f32_16x16x32_bf16 v[108:111], v[160:163], v[202:205], v[108:111]
	v_mfma_f32_16x16x32_bf16 v[100:103], v[152:155], v[224:227], v[100:103]
	v_mfma_f32_16x16x32_bf16 v[92:95], v[160:163], v[224:227], v[92:95]
	v_mfma_f32_16x16x32_bf16 v[80:83], v[152:155], v[232:235], v[80:83]
	v_mfma_f32_16x16x32_bf16 v[72:75], v[160:163], v[232:235], v[72:75]
	v_mfma_f32_16x16x32_bf16 v[124:127], v[156:159], v[198:201], v[124:127]
	v_mfma_f32_16x16x32_bf16 v[120:123], v[164:167], v[198:201], v[120:123]
	v_mfma_f32_16x16x32_bf16 v[116:119], v[156:159], v[206:209], v[116:119]
	v_mfma_f32_16x16x32_bf16 v[108:111], v[164:167], v[206:209], v[108:111]
	v_mfma_f32_16x16x32_bf16 v[100:103], v[156:159], v[228:231], v[100:103]
	v_mfma_f32_16x16x32_bf16 v[92:95], v[164:167], v[228:231], v[92:95]
	v_mfma_f32_16x16x32_bf16 v[80:83], v[156:159], v[236:239], v[80:83]
	v_mfma_f32_16x16x32_bf16 v[72:75], v[164:167], v[236:239], v[72:75]
	s_setprio 0
	s_setprio 1
	v_mfma_f32_16x16x32_bf16 v[112:115], v[168:171], v[194:197], v[112:115]
	v_mfma_f32_16x16x32_bf16 v[104:107], v[176:179], v[194:197], v[104:107]
	v_mfma_f32_16x16x32_bf16 v[96:99], v[168:171], v[202:205], v[96:99]
	v_mfma_f32_16x16x32_bf16 v[88:91], v[176:179], v[202:205], v[88:91]
	v_mfma_f32_16x16x32_bf16 v[84:87], v[168:171], v[224:227], v[84:87]
	v_mfma_f32_16x16x32_bf16 v[76:79], v[176:179], v[224:227], v[76:79]
	v_mfma_f32_16x16x32_bf16 v[68:71], v[168:171], v[232:235], v[68:71]
	v_mfma_f32_16x16x32_bf16 v[64:67], v[176:179], v[232:235], v[64:67]
	v_mfma_f32_16x16x32_bf16 v[112:115], v[172:175], v[198:201], v[112:115]
	v_mfma_f32_16x16x32_bf16 v[104:107], v[180:183], v[198:201], v[104:107]
	v_mfma_f32_16x16x32_bf16 v[96:99], v[172:175], v[206:209], v[96:99]
	v_mfma_f32_16x16x32_bf16 v[88:91], v[180:183], v[206:209], v[88:91]
	v_mfma_f32_16x16x32_bf16 v[84:87], v[172:175], v[228:231], v[84:87]
	v_mfma_f32_16x16x32_bf16 v[76:79], v[180:183], v[228:231], v[76:79]
	v_mfma_f32_16x16x32_bf16 v[68:71], v[172:175], v[236:239], v[68:71]
	v_mfma_f32_16x16x32_bf16 v[64:67], v[180:183], v[236:239], v[64:67]
	s_setprio 0
	s_barrier
	s_add_i32 s12, s28, s30
	v_lshl_add_u64 v[216:217], v[216:217], 0, s[68:69]
	s_mov_b32 m0, s12
	ds_read_b128 v[194:197], v149 offset:49152
	ds_read_b128 v[198:201], v149 offset:50176
	ds_read_b128 v[202:205], v149 offset:51200
	ds_read_b128 v[206:209], v149 offset:52224
	ds_read_b128 v[224:227], v149 offset:53248
	ds_read_b128 v[228:231], v149 offset:54272
	ds_read_b128 v[232:235], v149 offset:55296
	ds_read_b128 v[236:239], v149 offset:56320
	global_load_lds_dwordx4 v[216:217], off
	v_lshl_add_u64 v[216:217], v[218:219], 0, s[68:69]
	s_add_i32 m0, s12, 0x2000
	v_lshl_add_u64 v[210:211], v[210:211], 0, s[74:75]
	s_add_i32 s12, s29, s30
	global_load_lds_dwordx4 v[216:217], off
	v_lshl_add_u64 v[216:217], v[210:211], 0, v[132:133]
	s_mov_b32 m0, s12
	v_lshl_add_u64 v[210:211], v[210:211], 0, v[128:129]
	global_load_lds_dwordx4 v[216:217], off
	s_add_i32 m0, s12, 0x2000
	s_nop 0
	global_load_lds_dwordx4 v[210:211], off
	v_lshl_add_u64 v[210:211], v[220:221], 0, s[68:69]
	s_mov_b32 m0, s44
	s_nop 0
	global_load_lds_dwordx4 v[210:211], off
	v_lshl_add_u64 v[210:211], v[240:241], 0, s[68:69]
	s_mov_b32 m0, s45
	s_nop 0
	global_load_lds_dwordx4 v[210:211], off
	s_waitcnt vmcnt(6)
	s_waitcnt lgkmcnt(0)
	s_barrier
	s_setprio 1
	s_waitcnt lgkmcnt(0)
	v_mfma_f32_16x16x32_bf16 v[60:63], v[152:155], v[194:197], v[60:63]
	v_mfma_f32_16x16x32_bf16 v[56:59], v[160:163], v[194:197], v[56:59]
	v_mfma_f32_16x16x32_bf16 v[52:55], v[152:155], v[202:205], v[52:55]
	v_mfma_f32_16x16x32_bf16 v[44:47], v[160:163], v[202:205], v[44:47]
	v_mfma_f32_16x16x32_bf16 v[36:39], v[152:155], v[224:227], v[36:39]
	v_mfma_f32_16x16x32_bf16 v[28:31], v[160:163], v[224:227], v[28:31]
	v_mfma_f32_16x16x32_bf16 v[20:23], v[152:155], v[232:235], v[20:23]
	v_mfma_f32_16x16x32_bf16 v[12:15], v[160:163], v[232:235], v[12:15]
	v_mfma_f32_16x16x32_bf16 v[60:63], v[156:159], v[198:201], v[60:63]
	v_mfma_f32_16x16x32_bf16 v[56:59], v[164:167], v[198:201], v[56:59]
	v_mfma_f32_16x16x32_bf16 v[52:55], v[156:159], v[206:209], v[52:55]
	v_mfma_f32_16x16x32_bf16 v[44:47], v[164:167], v[206:209], v[44:47]
	v_mfma_f32_16x16x32_bf16 v[36:39], v[156:159], v[228:231], v[36:39]
	v_mfma_f32_16x16x32_bf16 v[28:31], v[164:167], v[228:231], v[28:31]
	v_mfma_f32_16x16x32_bf16 v[20:23], v[156:159], v[236:239], v[20:23]
	v_mfma_f32_16x16x32_bf16 v[12:15], v[164:167], v[236:239], v[12:15]
	s_setprio 0
	s_setprio 1
	v_mfma_f32_16x16x32_bf16 v[48:51], v[168:171], v[194:197], v[48:51]
	v_mfma_f32_16x16x32_bf16 v[40:43], v[176:179], v[194:197], v[40:43]
	v_mfma_f32_16x16x32_bf16 v[32:35], v[168:171], v[202:205], v[32:35]
	v_mfma_f32_16x16x32_bf16 v[24:27], v[176:179], v[202:205], v[24:27]
	v_mfma_f32_16x16x32_bf16 v[16:19], v[168:171], v[224:227], v[16:19]
	v_mfma_f32_16x16x32_bf16 v[8:11], v[176:179], v[224:227], v[8:11]
	v_mfma_f32_16x16x32_bf16 v[4:7], v[168:171], v[232:235], v[4:7]
	v_mfma_f32_16x16x32_bf16 v[0:3], v[176:179], v[232:235], v[0:3]
	v_mfma_f32_16x16x32_bf16 v[48:51], v[172:175], v[198:201], v[48:51]
	v_mfma_f32_16x16x32_bf16 v[40:43], v[180:183], v[198:201], v[40:43]
	v_mfma_f32_16x16x32_bf16 v[32:35], v[172:175], v[206:209], v[32:35]
	v_mfma_f32_16x16x32_bf16 v[24:27], v[180:183], v[206:209], v[24:27]
	v_mfma_f32_16x16x32_bf16 v[16:19], v[172:175], v[228:231], v[16:19]
	v_mfma_f32_16x16x32_bf16 v[8:11], v[180:183], v[228:231], v[8:11]
	v_mfma_f32_16x16x32_bf16 v[4:7], v[172:175], v[236:239], v[4:7]
	v_mfma_f32_16x16x32_bf16 v[0:3], v[180:183], v[236:239], v[0:3]
	s_setprio 0
	s_barrier
	s_add_i32 s59, s59, 2
	v_lshl_add_u64 v[144:145], v[144:145], 0, s[60:61]
	s_cmp_gt_u32 s59, 41
	s_mov_b64 s[12:13], s[14:15]
	s_cbranch_scc0 .LBB0_1491
	s_mov_b64 s[14:15], 0xb0000
	s_and_b64 vcc, exec, s[6:7]
	s_cbranch_vccz .LBB0_1494
	s_barrier

.LBB0_1587:
	s_add_u32 s28, s24, 0xfff80080
	s_addc_u32 s29, s25, -1
	s_add_i32 s48, 0, 0x10000
	s_cmp_eq_u32 s51, 28
	s_cselect_b32 s39, s9, s29
	s_cselect_b32 s38, s11, s28
	s_cselect_b32 s31, s45, s50
	s_cselect_b32 s30, s46, s47
	s_add_i32 s49, 0, 0x14000
	v_add_u32_e32 v154, s48, v139
	v_add_u32_e32 v170, s49, v139
	ds_read_b128 v[142:145], v154
	ds_read_b128 v[146:149], v154 offset:1024
	ds_read_b128 v[150:153], v154 offset:2048
	ds_read_b128 v[154:157], v154 offset:3072
	ds_read_b128 v[158:161], v170
	ds_read_b128 v[162:165], v170 offset:1024
	ds_read_b128 v[166:169], v170 offset:2048
	ds_read_b128 v[170:173], v170 offset:3072
	v_lshl_add_u64 v[182:183], s[24:25], 0, v[134:135]
	s_add_i32 m0, s20, 0xc000
	ds_read_b128 v[174:177], v141
	ds_read_b128 v[178:181], v141 offset:1024
	ds_read_b128 v[194:197], v141 offset:2048
	ds_read_b128 v[198:201], v141 offset:3072
	ds_read_b128 v[202:205], v141 offset:4096
	ds_read_b128 v[206:209], v141 offset:5120
	ds_read_b128 v[224:227], v141 offset:6144
	ds_read_b128 v[228:231], v141 offset:7168
	global_load_lds_dwordx4 v[182:183], off
	v_lshl_add_u64 v[182:183], s[24:25], 0, v[136:137]
	s_add_i32 m0, s20, 0xe000
	s_nop 0
	global_load_lds_dwordx4 v[182:183], off
	s_waitcnt vmcnt(8)
	s_waitcnt lgkmcnt(0)
	s_barrier
	s_setprio 1
	s_waitcnt lgkmcnt(0)
	v_mfma_f32_16x16x32_bf16 v[124:127], v[142:145], v[174:177], v[124:127]
	v_mfma_f32_16x16x32_bf16 v[116:119], v[150:153], v[174:177], v[116:119]
	v_mfma_f32_16x16x32_bf16 v[108:111], v[142:145], v[194:197], v[108:111]
	v_mfma_f32_16x16x32_bf16 v[100:103], v[150:153], v[194:197], v[100:103]
	v_mfma_f32_16x16x32_bf16 v[92:95], v[142:145], v[202:205], v[92:95]
	v_mfma_f32_16x16x32_bf16 v[84:87], v[150:153], v[202:205], v[84:87]
	v_mfma_f32_16x16x32_bf16 v[76:79], v[142:145], v[224:227], v[76:79]
	v_mfma_f32_16x16x32_bf16 v[68:71], v[150:153], v[224:227], v[68:71]
	v_mfma_f32_16x16x32_bf16 v[124:127], v[146:149], v[178:181], v[124:127]
	v_mfma_f32_16x16x32_bf16 v[116:119], v[154:157], v[178:181], v[116:119]
	v_mfma_f32_16x16x32_bf16 v[108:111], v[146:149], v[198:201], v[108:111]
	v_mfma_f32_16x16x32_bf16 v[100:103], v[154:157], v[198:201], v[100:103]
	v_mfma_f32_16x16x32_bf16 v[92:95], v[146:149], v[206:209], v[92:95]
	v_mfma_f32_16x16x32_bf16 v[84:87], v[154:157], v[206:209], v[84:87]
	v_mfma_f32_16x16x32_bf16 v[76:79], v[146:149], v[228:231], v[76:79]
	v_mfma_f32_16x16x32_bf16 v[68:71], v[154:157], v[228:231], v[68:71]
	s_setprio 0
	s_setprio 1
	v_mfma_f32_16x16x32_bf16 v[120:123], v[158:161], v[174:177], v[120:123]
	v_mfma_f32_16x16x32_bf16 v[112:115], v[166:169], v[174:177], v[112:115]
	v_mfma_f32_16x16x32_bf16 v[104:107], v[158:161], v[194:197], v[104:107]
	v_mfma_f32_16x16x32_bf16 v[96:99], v[166:169], v[194:197], v[96:99]
	v_mfma_f32_16x16x32_bf16 v[88:91], v[158:161], v[202:205], v[88:91]
	v_mfma_f32_16x16x32_bf16 v[80:83], v[166:169], v[202:205], v[80:83]
	v_mfma_f32_16x16x32_bf16 v[72:75], v[158:161], v[224:227], v[72:75]
	v_mfma_f32_16x16x32_bf16 v[64:67], v[166:169], v[224:227], v[64:67]
	v_mfma_f32_16x16x32_bf16 v[120:123], v[162:165], v[178:181], v[120:123]
	v_mfma_f32_16x16x32_bf16 v[112:115], v[170:173], v[178:181], v[112:115]
	v_mfma_f32_16x16x32_bf16 v[104:107], v[162:165], v[198:201], v[104:107]
	v_mfma_f32_16x16x32_bf16 v[96:99], v[170:173], v[198:201], v[96:99]
	v_mfma_f32_16x16x32_bf16 v[88:91], v[162:165], v[206:209], v[88:91]
	v_mfma_f32_16x16x32_bf16 v[80:83], v[170:173], v[206:209], v[80:83]
	v_mfma_f32_16x16x32_bf16 v[72:75], v[162:165], v[228:231], v[72:75]
	v_mfma_f32_16x16x32_bf16 v[64:67], v[170:173], v[228:231], v[64:67]
	s_setprio 0
	s_barrier
	s_add_i32 s28, s48, s4
	v_lshl_add_u64 v[182:183], s[30:31], 0, v[184:185]
	s_mov_b32 m0, s28
	ds_read_b128 v[174:177], v141 offset:16384
	ds_read_b128 v[178:181], v141 offset:17408
	ds_read_b128 v[194:197], v141 offset:18432
	ds_read_b128 v[198:201], v141 offset:19456
	ds_read_b128 v[202:205], v141 offset:20480
	ds_read_b128 v[206:209], v141 offset:21504
	ds_read_b128 v[224:227], v141 offset:22528
	ds_read_b128 v[228:231], v141 offset:23552
	global_load_lds_dwordx4 v[182:183], off
	s_add_i32 m0, s28, 0x2000
	s_add_u32 s28, s30, 0x80000
	v_lshl_add_u64 v[210:211], s[30:31], 0, v[128:129]
	s_addc_u32 s29, s31, 0
	s_add_i32 s48, s49, s4
	global_load_lds_dwordx4 v[210:211], off
	v_lshl_add_u64 v[216:217], s[28:29], 0, v[184:185]
	s_mov_b32 m0, s48
	v_lshl_add_u64 v[218:219], s[38:39], 0, v[130:131]
	global_load_lds_dwordx4 v[216:217], off
	v_lshl_add_u64 v[216:217], s[28:29], 0, v[128:129]
	s_add_i32 m0, s48, 0x2000
	s_nop 0
	global_load_lds_dwordx4 v[216:217], off
	v_lshl_add_u64 v[216:217], s[38:39], 0, v[132:133]
	s_waitcnt vmcnt(6)
	s_waitcnt lgkmcnt(0)
	s_barrier
	s_setprio 1
	s_waitcnt lgkmcnt(0)
	v_mfma_f32_16x16x32_bf16 v[60:63], v[142:145], v[174:177], v[60:63]
	v_mfma_f32_16x16x32_bf16 v[52:55], v[150:153], v[174:177], v[52:55]
	v_mfma_f32_16x16x32_bf16 v[44:47], v[142:145], v[194:197], v[44:47]
	v_mfma_f32_16x16x32_bf16 v[36:39], v[150:153], v[194:197], v[36:39]
	v_mfma_f32_16x16x32_bf16 v[28:31], v[142:145], v[202:205], v[28:31]
	v_mfma_f32_16x16x32_bf16 v[20:23], v[150:153], v[202:205], v[20:23]
	v_mfma_f32_16x16x32_bf16 v[12:15], v[142:145], v[224:227], v[12:15]
	v_mfma_f32_16x16x32_bf16 v[4:7], v[150:153], v[224:227], v[4:7]
	v_mfma_f32_16x16x32_bf16 v[60:63], v[146:149], v[178:181], v[60:63]
	v_mfma_f32_16x16x32_bf16 v[52:55], v[154:157], v[178:181], v[52:55]
	v_mfma_f32_16x16x32_bf16 v[44:47], v[146:149], v[198:201], v[44:47]
	v_mfma_f32_16x16x32_bf16 v[36:39], v[154:157], v[198:201], v[36:39]
	v_mfma_f32_16x16x32_bf16 v[28:31], v[146:149], v[206:209], v[28:31]
	v_mfma_f32_16x16x32_bf16 v[20:23], v[154:157], v[206:209], v[20:23]
	v_mfma_f32_16x16x32_bf16 v[12:15], v[146:149], v[228:231], v[12:15]
	v_mfma_f32_16x16x32_bf16 v[4:7], v[154:157], v[228:231], v[4:7]
	s_setprio 0
	s_setprio 1
	v_mfma_f32_16x16x32_bf16 v[56:59], v[158:161], v[174:177], v[56:59]
	v_mfma_f32_16x16x32_bf16 v[48:51], v[166:169], v[174:177], v[48:51]
	v_mfma_f32_16x16x32_bf16 v[40:43], v[158:161], v[194:197], v[40:43]
	v_mfma_f32_16x16x32_bf16 v[32:35], v[166:169], v[194:197], v[32:35]
	v_mfma_f32_16x16x32_bf16 v[24:27], v[158:161], v[202:205], v[24:27]
	v_mfma_f32_16x16x32_bf16 v[16:19], v[166:169], v[202:205], v[16:19]
	v_mfma_f32_16x16x32_bf16 v[8:11], v[158:161], v[224:227], v[8:11]
	v_mfma_f32_16x16x32_bf16 v[0:3], v[166:169], v[224:227], v[0:3]
	v_mfma_f32_16x16x32_bf16 v[56:59], v[162:165], v[178:181], v[56:59]
	v_mfma_f32_16x16x32_bf16 v[48:51], v[170:173], v[178:181], v[48:51]
	v_mfma_f32_16x16x32_bf16 v[40:43], v[162:165], v[198:201], v[40:43]
	v_mfma_f32_16x16x32_bf16 v[32:35], v[170:173], v[198:201], v[32:35]
	v_mfma_f32_16x16x32_bf16 v[24:27], v[162:165], v[206:209], v[24:27]
	v_mfma_f32_16x16x32_bf16 v[16:19], v[170:173], v[206:209], v[16:19]
	v_mfma_f32_16x16x32_bf16 v[8:11], v[162:165], v[228:231], v[8:11]
	v_mfma_f32_16x16x32_bf16 v[0:3], v[170:173], v[228:231], v[0:3]
	s_setprio 0
	s_barrier
	s_add_i32 s48, 0, 0x18000
	s_add_i32 s49, 0, 0x1c000
	v_add_u32_e32 v154, s48, v139
	v_add_u32_e32 v170, s49, v139
	ds_read_b128 v[142:145], v154
	ds_read_b128 v[146:149], v154 offset:1024
	ds_read_b128 v[150:153], v154 offset:2048
	ds_read_b128 v[154:157], v154 offset:3072
	ds_read_b128 v[158:161], v170
	ds_read_b128 v[162:165], v170 offset:1024
	ds_read_b128 v[166:169], v170 offset:2048
	ds_read_b128 v[170:173], v170 offset:3072
	s_add_u32 s28, s38, 0x80000
	s_addc_u32 s29, s39, 0
	s_mov_b32 m0, s26
	v_lshl_add_u64 v[232:233], s[28:29], 0, v[132:133]
	ds_read_b128 v[174:177], v141 offset:32768
	ds_read_b128 v[178:181], v141 offset:33792
	ds_read_b128 v[194:197], v141 offset:34816
	ds_read_b128 v[198:201], v141 offset:35840
	ds_read_b128 v[202:205], v141 offset:36864
	ds_read_b128 v[206:209], v141 offset:37888
	ds_read_b128 v[224:227], v141 offset:38912
	ds_read_b128 v[228:231], v141 offset:39936
	global_load_lds_dwordx4 v[232:233], off
	v_lshl_add_u64 v[232:233], s[28:29], 0, v[130:131]
	s_mov_b32 m0, s27
	s_nop 0
	global_load_lds_dwordx4 v[232:233], off
	s_mov_b32 m0, s20
	s_nop 0
	global_load_lds_dwordx4 v[216:217], off
	s_mov_b32 m0, s21
	s_nop 0
	global_load_lds_dwordx4 v[218:219], off
	s_waitcnt vmcnt(8)
	s_waitcnt lgkmcnt(0)
	s_barrier
	s_setprio 1
	s_waitcnt lgkmcnt(0)
	v_mfma_f32_16x16x32_bf16 v[124:127], v[142:145], v[174:177], v[124:127]
	v_mfma_f32_16x16x32_bf16 v[116:119], v[150:153], v[174:177], v[116:119]
	v_mfma_f32_16x16x32_bf16 v[108:111], v[142:145], v[194:197], v[108:111]
	v_mfma_f32_16x16x32_bf16 v[100:103], v[150:153], v[194:197], v[100:103]
	v_mfma_f32_16x16x32_bf16 v[92:95], v[142:145], v[202:205], v[92:95]
	v_mfma_f32_16x16x32_bf16 v[84:87], v[150:153], v[202:205], v[84:87]
	v_mfma_f32_16x16x32_bf16 v[76:79], v[142:145], v[224:227], v[76:79]
	v_mfma_f32_16x16x32_bf16 v[68:71], v[150:153], v[224:227], v[68:71]
	v_mfma_f32_16x16x32_bf16 v[124:127], v[146:149], v[178:181], v[124:127]
	v_mfma_f32_16x16x32_bf16 v[116:119], v[154:157], v[178:181], v[116:119]
	v_mfma_f32_16x16x32_bf16 v[108:111], v[146:149], v[198:201], v[108:111]
	v_mfma_f32_16x16x32_bf16 v[100:103], v[154:157], v[198:201], v[100:103]
	v_mfma_f32_16x16x32_bf16 v[92:95], v[146:149], v[206:209], v[92:95]
	v_mfma_f32_16x16x32_bf16 v[84:87], v[154:157], v[206:209], v[84:87]
	v_mfma_f32_16x16x32_bf16 v[76:79], v[146:149], v[228:231], v[76:79]
	v_mfma_f32_16x16x32_bf16 v[68:71], v[154:157], v[228:231], v[68:71]
	s_setprio 0
	s_setprio 1
	v_mfma_f32_16x16x32_bf16 v[120:123], v[158:161], v[174:177], v[120:123]
	v_mfma_f32_16x16x32_bf16 v[112:115], v[166:169], v[174:177], v[112:115]
	v_mfma_f32_16x16x32_bf16 v[104:107], v[158:161], v[194:197], v[104:107]
	v_mfma_f32_16x16x32_bf16 v[96:99], v[166:169], v[194:197], v[96:99]
	v_mfma_f32_16x16x32_bf16 v[88:91], v[158:161], v[202:205], v[88:91]
	v_mfma_f32_16x16x32_bf16 v[80:83], v[166:169], v[202:205], v[80:83]
	v_mfma_f32_16x16x32_bf16 v[72:75], v[158:161], v[224:227], v[72:75]
	v_mfma_f32_16x16x32_bf16 v[64:67], v[166:169], v[224:227], v[64:67]
	v_mfma_f32_16x16x32_bf16 v[120:123], v[162:165], v[178:181], v[120:123]
	v_mfma_f32_16x16x32_bf16 v[112:115], v[170:173], v[178:181], v[112:115]
	v_mfma_f32_16x16x32_bf16 v[104:107], v[162:165], v[198:201], v[104:107]
	v_mfma_f32_16x16x32_bf16 v[96:99], v[170:173], v[198:201], v[96:99]
	v_mfma_f32_16x16x32_bf16 v[88:91], v[162:165], v[206:209], v[88:91]
	v_mfma_f32_16x16x32_bf16 v[80:83], v[170:173], v[206:209], v[80:83]
	v_mfma_f32_16x16x32_bf16 v[72:75], v[162:165], v[228:231], v[72:75]
	v_mfma_f32_16x16x32_bf16 v[64:67], v[170:173], v[228:231], v[64:67]
	s_setprio 0
	s_barrier
	s_add_i32 s28, s48, s4
	v_lshl_add_u64 v[182:183], v[182:183], 0, s[68:69]
	s_mov_b32 m0, s28
	ds_read_b128 v[174:177], v141 offset:49152
	ds_read_b128 v[178:181], v141 offset:50176
	ds_read_b128 v[194:197], v141 offset:51200
	ds_read_b128 v[198:201], v141 offset:52224
	ds_read_b128 v[202:205], v141 offset:53248
	ds_read_b128 v[206:209], v141 offset:54272
	ds_read_b128 v[224:227], v141 offset:55296
	ds_read_b128 v[228:231], v141 offset:56320
	global_load_lds_dwordx4 v[182:183], off
	s_add_i32 m0, s28, 0x2000
	s_add_u32 s28, s30, 0x80080
	v_lshl_add_u64 v[182:183], v[210:211], 0, s[68:69]
	s_addc_u32 s29, s31, 0
	s_add_i32 s30, s49, s4
	global_load_lds_dwordx4 v[182:183], off
	v_lshl_add_u64 v[182:183], s[28:29], 0, v[184:185]
	s_mov_b32 m0, s30
	s_nop 0
	global_load_lds_dwordx4 v[182:183], off
	v_lshl_add_u64 v[182:183], s[28:29], 0, v[128:129]
	s_add_i32 m0, s30, 0x2000
	s_nop 0
	global_load_lds_dwordx4 v[182:183], off
	v_lshl_add_u64 v[182:183], v[216:217], 0, s[68:69]
	s_mov_b32 m0, s40
	s_nop 0
	global_load_lds_dwordx4 v[182:183], off
	v_lshl_add_u64 v[182:183], v[218:219], 0, s[68:69]
	s_mov_b32 m0, s41
	s_nop 0
	global_load_lds_dwordx4 v[182:183], off
	s_waitcnt vmcnt(6)
	s_waitcnt lgkmcnt(0)
	s_barrier
	s_setprio 1
	s_waitcnt lgkmcnt(0)
	v_mfma_f32_16x16x32_bf16 v[60:63], v[142:145], v[174:177], v[60:63]
	v_mfma_f32_16x16x32_bf16 v[52:55], v[150:153], v[174:177], v[52:55]
	v_mfma_f32_16x16x32_bf16 v[44:47], v[142:145], v[194:197], v[44:47]
	v_mfma_f32_16x16x32_bf16 v[36:39], v[150:153], v[194:197], v[36:39]
	v_mfma_f32_16x16x32_bf16 v[28:31], v[142:145], v[202:205], v[28:31]
	v_mfma_f32_16x16x32_bf16 v[20:23], v[150:153], v[202:205], v[20:23]
	v_mfma_f32_16x16x32_bf16 v[12:15], v[142:145], v[224:227], v[12:15]
	v_mfma_f32_16x16x32_bf16 v[4:7], v[150:153], v[224:227], v[4:7]
	v_mfma_f32_16x16x32_bf16 v[60:63], v[146:149], v[178:181], v[60:63]
	v_mfma_f32_16x16x32_bf16 v[52:55], v[154:157], v[178:181], v[52:55]
	v_mfma_f32_16x16x32_bf16 v[44:47], v[146:149], v[198:201], v[44:47]
	v_mfma_f32_16x16x32_bf16 v[36:39], v[154:157], v[198:201], v[36:39]
	v_mfma_f32_16x16x32_bf16 v[28:31], v[146:149], v[206:209], v[28:31]
	v_mfma_f32_16x16x32_bf16 v[20:23], v[154:157], v[206:209], v[20:23]
	v_mfma_f32_16x16x32_bf16 v[12:15], v[146:149], v[228:231], v[12:15]
	v_mfma_f32_16x16x32_bf16 v[4:7], v[154:157], v[228:231], v[4:7]
	s_setprio 0
	s_setprio 1
	v_mfma_f32_16x16x32_bf16 v[56:59], v[158:161], v[174:177], v[56:59]
	v_mfma_f32_16x16x32_bf16 v[48:51], v[166:169], v[174:177], v[48:51]
	v_mfma_f32_16x16x32_bf16 v[40:43], v[158:161], v[194:197], v[40:43]
	v_mfma_f32_16x16x32_bf16 v[32:35], v[166:169], v[194:197], v[32:35]
	v_mfma_f32_16x16x32_bf16 v[24:27], v[158:161], v[202:205], v[24:27]
	v_mfma_f32_16x16x32_bf16 v[16:19], v[166:169], v[202:205], v[16:19]
	v_mfma_f32_16x16x32_bf16 v[8:11], v[158:161], v[224:227], v[8:11]
	v_mfma_f32_16x16x32_bf16 v[0:3], v[166:169], v[224:227], v[0:3]
	v_mfma_f32_16x16x32_bf16 v[56:59], v[162:165], v[178:181], v[56:59]
	v_mfma_f32_16x16x32_bf16 v[48:51], v[170:173], v[178:181], v[48:51]
	v_mfma_f32_16x16x32_bf16 v[40:43], v[162:165], v[198:201], v[40:43]
	v_mfma_f32_16x16x32_bf16 v[32:35], v[170:173], v[198:201], v[32:35]
	v_mfma_f32_16x16x32_bf16 v[24:27], v[162:165], v[206:209], v[24:27]
	v_mfma_f32_16x16x32_bf16 v[16:19], v[170:173], v[206:209], v[16:19]
	v_mfma_f32_16x16x32_bf16 v[8:11], v[162:165], v[228:231], v[8:11]
	v_mfma_f32_16x16x32_bf16 v[0:3], v[170:173], v[228:231], v[0:3]
	s_setprio 0
	s_barrier
	s_add_i32 s51, s51, 2
	s_add_u32 s24, s24, 0x100
	s_addc_u32 s25, s25, 0
	s_add_u32 s47, s47, 0x100
	s_addc_u32 s50, s50, 0
	s_cmp_gt_u32 s51, 29
	s_cbranch_scc0 .LBB0_1587
	s_and_b64 vcc, exec, s[6:7]
	s_cbranch_vccz .LBB0_1590
	s_barrier

.LBB0_1661:
	s_add_u32 s24, s18, 0x100
	s_addc_u32 s25, s19, 0
	s_add_i32 s28, 0, 0x10000
	s_cmpk_eq_i32 s61, 0x54
	s_cselect_b32 s39, s51, s25
	s_cselect_b32 s38, s52, s24
	s_cselect_b32 s31, s53, s60
	s_cselect_b32 s30, s58, s59
	s_add_i32 s29, 0, 0x14000
	s_waitcnt vmcnt(0)
	v_add_u32_e32 v84, s28, v163
	v_add_u32_e32 v170, s29, v163
	ds_read_b128 v[64:67], v84
	ds_read_b128 v[68:71], v84 offset:1024
	ds_read_b128 v[80:83], v84 offset:2048
	ds_read_b128 v[84:87], v84 offset:3072
	ds_read_b128 v[154:157], v170
	ds_read_b128 v[158:161], v170 offset:1024
	ds_read_b128 v[166:169], v170 offset:2048
	ds_read_b128 v[170:173], v170 offset:3072
	v_lshl_add_u64 v[182:183], s[18:19], 0, v[150:151]
	s_add_i32 m0, s20, 0xc000
	ds_read_b128 v[174:177], v165
	ds_read_b128 v[178:181], v165 offset:1024
	ds_read_b128 v[194:197], v165 offset:2048
	ds_read_b128 v[198:201], v165 offset:3072
	ds_read_b128 v[202:205], v165 offset:4096
	ds_read_b128 v[206:209], v165 offset:5120
	ds_read_b128 v[224:227], v165 offset:6144
	ds_read_b128 v[228:231], v165 offset:7168
	global_load_lds_dwordx4 v[182:183], off
	v_lshl_add_u64 v[182:183], s[18:19], 0, v[152:153]
	s_add_i32 m0, s20, 0xe000
	s_nop 0
	global_load_lds_dwordx4 v[182:183], off
	s_waitcnt vmcnt(8)
	s_waitcnt lgkmcnt(0)
	s_barrier
	s_setprio 1
	s_waitcnt lgkmcnt(0)
	v_mfma_f32_16x16x32_bf16 v[140:143], v[64:67], v[174:177], v[140:143]
	v_mfma_f32_16x16x32_bf16 v[136:139], v[80:83], v[174:177], v[136:139]
	v_mfma_f32_16x16x32_bf16 v[124:127], v[64:67], v[194:197], v[124:127]
	v_mfma_f32_16x16x32_bf16 v[120:123], v[80:83], v[194:197], v[120:123]
	v_mfma_f32_16x16x32_bf16 v[108:111], v[64:67], v[202:205], v[108:111]
	v_mfma_f32_16x16x32_bf16 v[104:107], v[80:83], v[202:205], v[104:107]
	v_mfma_f32_16x16x32_bf16 v[92:95], v[64:67], v[224:227], v[92:95]
	v_mfma_f32_16x16x32_bf16 v[88:91], v[80:83], v[224:227], v[88:91]
	v_mfma_f32_16x16x32_bf16 v[140:143], v[68:71], v[178:181], v[140:143]
	v_mfma_f32_16x16x32_bf16 v[136:139], v[84:87], v[178:181], v[136:139]
	v_mfma_f32_16x16x32_bf16 v[124:127], v[68:71], v[198:201], v[124:127]
	v_mfma_f32_16x16x32_bf16 v[120:123], v[84:87], v[198:201], v[120:123]
	v_mfma_f32_16x16x32_bf16 v[108:111], v[68:71], v[206:209], v[108:111]
	v_mfma_f32_16x16x32_bf16 v[104:107], v[84:87], v[206:209], v[104:107]
	v_mfma_f32_16x16x32_bf16 v[92:95], v[68:71], v[228:231], v[92:95]
	v_mfma_f32_16x16x32_bf16 v[88:91], v[84:87], v[228:231], v[88:91]
	s_setprio 0
	s_setprio 1
	v_mfma_f32_16x16x32_bf16 v[132:135], v[154:157], v[174:177], v[132:135]
	v_mfma_f32_16x16x32_bf16 v[128:131], v[166:169], v[174:177], v[128:131]
	v_mfma_f32_16x16x32_bf16 v[116:119], v[154:157], v[194:197], v[116:119]
	v_mfma_f32_16x16x32_bf16 v[112:115], v[166:169], v[194:197], v[112:115]
	v_mfma_f32_16x16x32_bf16 v[100:103], v[154:157], v[202:205], v[100:103]
	v_mfma_f32_16x16x32_bf16 v[96:99], v[166:169], v[202:205], v[96:99]
	v_mfma_f32_16x16x32_bf16 v[76:79], v[154:157], v[224:227], v[76:79]
	v_mfma_f32_16x16x32_bf16 v[72:75], v[166:169], v[224:227], v[72:75]
	v_mfma_f32_16x16x32_bf16 v[132:135], v[158:161], v[178:181], v[132:135]
	v_mfma_f32_16x16x32_bf16 v[128:131], v[170:173], v[178:181], v[128:131]
	v_mfma_f32_16x16x32_bf16 v[116:119], v[158:161], v[198:201], v[116:119]
	v_mfma_f32_16x16x32_bf16 v[112:115], v[170:173], v[198:201], v[112:115]
	v_mfma_f32_16x16x32_bf16 v[100:103], v[158:161], v[206:209], v[100:103]
	v_mfma_f32_16x16x32_bf16 v[96:99], v[170:173], v[206:209], v[96:99]
	v_mfma_f32_16x16x32_bf16 v[76:79], v[158:161], v[228:231], v[76:79]
	v_mfma_f32_16x16x32_bf16 v[72:75], v[170:173], v[228:231], v[72:75]
	s_setprio 0
	s_barrier
	s_add_i32 s18, s28, s4
	v_lshl_add_u64 v[182:183], s[30:31], 0, v[184:185]
	s_mov_b32 m0, s18
	ds_read_b128 v[174:177], v165 offset:16384
	ds_read_b128 v[178:181], v165 offset:17408
	ds_read_b128 v[194:197], v165 offset:18432
	ds_read_b128 v[198:201], v165 offset:19456
	ds_read_b128 v[202:205], v165 offset:20480
	ds_read_b128 v[206:209], v165 offset:21504
	ds_read_b128 v[224:227], v165 offset:22528
	ds_read_b128 v[228:231], v165 offset:23552
	global_load_lds_dwordx4 v[182:183], off
	s_add_i32 m0, s18, 0x2000
	s_add_u32 s18, s30, 0x160000
	v_lshl_add_u64 v[210:211], s[30:31], 0, v[144:145]
	s_addc_u32 s19, s31, 0
	s_add_i32 s28, s29, s4
	global_load_lds_dwordx4 v[210:211], off
	v_lshl_add_u64 v[216:217], s[18:19], 0, v[184:185]
	s_mov_b32 m0, s28
	v_lshl_add_u64 v[218:219], s[38:39], 0, v[146:147]
	global_load_lds_dwordx4 v[216:217], off
	v_lshl_add_u64 v[216:217], s[18:19], 0, v[144:145]
	s_add_i32 m0, s28, 0x2000
	s_nop 0
	global_load_lds_dwordx4 v[216:217], off
	v_lshl_add_u64 v[216:217], s[38:39], 0, v[148:149]
	s_waitcnt vmcnt(6)
	s_waitcnt lgkmcnt(0)
	s_barrier
	s_setprio 1
	s_waitcnt lgkmcnt(0)
	v_mfma_f32_16x16x32_bf16 v[60:63], v[64:67], v[174:177], v[60:63]
	v_mfma_f32_16x16x32_bf16 v[56:59], v[80:83], v[174:177], v[56:59]
	v_mfma_f32_16x16x32_bf16 v[44:47], v[64:67], v[194:197], v[44:47]
	v_mfma_f32_16x16x32_bf16 v[40:43], v[80:83], v[194:197], v[40:43]
	v_mfma_f32_16x16x32_bf16 v[28:31], v[64:67], v[202:205], v[28:31]
	v_mfma_f32_16x16x32_bf16 v[24:27], v[80:83], v[202:205], v[24:27]
	v_mfma_f32_16x16x32_bf16 v[12:15], v[64:67], v[224:227], v[12:15]
	v_mfma_f32_16x16x32_bf16 v[8:11], v[80:83], v[224:227], v[8:11]
	v_mfma_f32_16x16x32_bf16 v[60:63], v[68:71], v[178:181], v[60:63]
	v_mfma_f32_16x16x32_bf16 v[56:59], v[84:87], v[178:181], v[56:59]
	v_mfma_f32_16x16x32_bf16 v[44:47], v[68:71], v[198:201], v[44:47]
	v_mfma_f32_16x16x32_bf16 v[40:43], v[84:87], v[198:201], v[40:43]
	v_mfma_f32_16x16x32_bf16 v[28:31], v[68:71], v[206:209], v[28:31]
	v_mfma_f32_16x16x32_bf16 v[24:27], v[84:87], v[206:209], v[24:27]
	v_mfma_f32_16x16x32_bf16 v[12:15], v[68:71], v[228:231], v[12:15]
	v_mfma_f32_16x16x32_bf16 v[8:11], v[84:87], v[228:231], v[8:11]
	s_setprio 0
	s_setprio 1
	v_mfma_f32_16x16x32_bf16 v[52:55], v[154:157], v[174:177], v[52:55]
	v_mfma_f32_16x16x32_bf16 v[48:51], v[166:169], v[174:177], v[48:51]
	v_mfma_f32_16x16x32_bf16 v[36:39], v[154:157], v[194:197], v[36:39]
	v_mfma_f32_16x16x32_bf16 v[32:35], v[166:169], v[194:197], v[32:35]
	v_mfma_f32_16x16x32_bf16 v[20:23], v[154:157], v[202:205], v[20:23]
	v_mfma_f32_16x16x32_bf16 v[16:19], v[166:169], v[202:205], v[16:19]
	v_mfma_f32_16x16x32_bf16 v[4:7], v[154:157], v[224:227], v[4:7]
	v_mfma_f32_16x16x32_bf16 v[0:3], v[166:169], v[224:227], v[0:3]
	v_mfma_f32_16x16x32_bf16 v[52:55], v[158:161], v[178:181], v[52:55]
	v_mfma_f32_16x16x32_bf16 v[48:51], v[170:173], v[178:181], v[48:51]
	v_mfma_f32_16x16x32_bf16 v[36:39], v[158:161], v[198:201], v[36:39]
	v_mfma_f32_16x16x32_bf16 v[32:35], v[170:173], v[198:201], v[32:35]
	v_mfma_f32_16x16x32_bf16 v[20:23], v[158:161], v[206:209], v[20:23]
	v_mfma_f32_16x16x32_bf16 v[16:19], v[170:173], v[206:209], v[16:19]
	v_mfma_f32_16x16x32_bf16 v[4:7], v[158:161], v[228:231], v[4:7]
	v_mfma_f32_16x16x32_bf16 v[0:3], v[170:173], v[228:231], v[0:3]
	s_setprio 0
	s_barrier
	s_add_i32 s28, 0, 0x18000
	s_add_i32 s29, 0, 0x1c000
	v_add_u32_e32 v84, s28, v163
	v_add_u32_e32 v170, s29, v163
	ds_read_b128 v[64:67], v84
	ds_read_b128 v[68:71], v84 offset:1024
	ds_read_b128 v[80:83], v84 offset:2048
	ds_read_b128 v[84:87], v84 offset:3072
	ds_read_b128 v[154:157], v170
	ds_read_b128 v[158:161], v170 offset:1024
	ds_read_b128 v[166:169], v170 offset:2048
	ds_read_b128 v[170:173], v170 offset:3072
	s_add_u32 s18, s38, 0x160000
	s_addc_u32 s19, s39, 0
	s_mov_b32 m0, s26
	v_lshl_add_u64 v[232:233], s[18:19], 0, v[148:149]
	ds_read_b128 v[174:177], v165 offset:32768
	ds_read_b128 v[178:181], v165 offset:33792
	ds_read_b128 v[194:197], v165 offset:34816
	ds_read_b128 v[198:201], v165 offset:35840
	ds_read_b128 v[202:205], v165 offset:36864
	ds_read_b128 v[206:209], v165 offset:37888
	ds_read_b128 v[224:227], v165 offset:38912
	ds_read_b128 v[228:231], v165 offset:39936
	global_load_lds_dwordx4 v[232:233], off
	v_lshl_add_u64 v[232:233], s[18:19], 0, v[146:147]
	s_mov_b32 m0, s27
	s_nop 0
	global_load_lds_dwordx4 v[232:233], off
	s_mov_b32 m0, s20
	s_nop 0
	global_load_lds_dwordx4 v[216:217], off
	s_mov_b32 m0, s21
	s_nop 0
	global_load_lds_dwordx4 v[218:219], off
	s_waitcnt vmcnt(8)
	s_waitcnt lgkmcnt(0)
	s_barrier
	s_setprio 1
	s_waitcnt lgkmcnt(0)
	v_mfma_f32_16x16x32_bf16 v[140:143], v[64:67], v[174:177], v[140:143]
	v_mfma_f32_16x16x32_bf16 v[136:139], v[80:83], v[174:177], v[136:139]
	v_mfma_f32_16x16x32_bf16 v[124:127], v[64:67], v[194:197], v[124:127]
	v_mfma_f32_16x16x32_bf16 v[120:123], v[80:83], v[194:197], v[120:123]
	v_mfma_f32_16x16x32_bf16 v[108:111], v[64:67], v[202:205], v[108:111]
	v_mfma_f32_16x16x32_bf16 v[104:107], v[80:83], v[202:205], v[104:107]
	v_mfma_f32_16x16x32_bf16 v[92:95], v[64:67], v[224:227], v[92:95]
	v_mfma_f32_16x16x32_bf16 v[88:91], v[80:83], v[224:227], v[88:91]
	v_mfma_f32_16x16x32_bf16 v[140:143], v[68:71], v[178:181], v[140:143]
	v_mfma_f32_16x16x32_bf16 v[136:139], v[84:87], v[178:181], v[136:139]
	v_mfma_f32_16x16x32_bf16 v[124:127], v[68:71], v[198:201], v[124:127]
	v_mfma_f32_16x16x32_bf16 v[120:123], v[84:87], v[198:201], v[120:123]
	v_mfma_f32_16x16x32_bf16 v[108:111], v[68:71], v[206:209], v[108:111]
	v_mfma_f32_16x16x32_bf16 v[104:107], v[84:87], v[206:209], v[104:107]
	v_mfma_f32_16x16x32_bf16 v[92:95], v[68:71], v[228:231], v[92:95]
	v_mfma_f32_16x16x32_bf16 v[88:91], v[84:87], v[228:231], v[88:91]
	s_setprio 0
	s_setprio 1
	v_mfma_f32_16x16x32_bf16 v[132:135], v[154:157], v[174:177], v[132:135]
	v_mfma_f32_16x16x32_bf16 v[128:131], v[166:169], v[174:177], v[128:131]
	v_mfma_f32_16x16x32_bf16 v[116:119], v[154:157], v[194:197], v[116:119]
	v_mfma_f32_16x16x32_bf16 v[112:115], v[166:169], v[194:197], v[112:115]
	v_mfma_f32_16x16x32_bf16 v[100:103], v[154:157], v[202:205], v[100:103]
	v_mfma_f32_16x16x32_bf16 v[96:99], v[166:169], v[202:205], v[96:99]
	v_mfma_f32_16x16x32_bf16 v[76:79], v[154:157], v[224:227], v[76:79]
	v_mfma_f32_16x16x32_bf16 v[72:75], v[166:169], v[224:227], v[72:75]
	v_mfma_f32_16x16x32_bf16 v[132:135], v[158:161], v[178:181], v[132:135]
	v_mfma_f32_16x16x32_bf16 v[128:131], v[170:173], v[178:181], v[128:131]
	v_mfma_f32_16x16x32_bf16 v[116:119], v[158:161], v[198:201], v[116:119]
	v_mfma_f32_16x16x32_bf16 v[112:115], v[170:173], v[198:201], v[112:115]
	v_mfma_f32_16x16x32_bf16 v[100:103], v[158:161], v[206:209], v[100:103]
	v_mfma_f32_16x16x32_bf16 v[96:99], v[170:173], v[206:209], v[96:99]
	v_mfma_f32_16x16x32_bf16 v[76:79], v[158:161], v[228:231], v[76:79]
	v_mfma_f32_16x16x32_bf16 v[72:75], v[170:173], v[228:231], v[72:75]
	s_setprio 0
	s_barrier
	s_add_i32 s18, s28, s4
	v_lshl_add_u64 v[182:183], v[182:183], 0, s[68:69]
	s_mov_b32 m0, s18
	ds_read_b128 v[174:177], v165 offset:49152
	ds_read_b128 v[178:181], v165 offset:50176
	ds_read_b128 v[194:197], v165 offset:51200
	ds_read_b128 v[198:201], v165 offset:52224
	ds_read_b128 v[202:205], v165 offset:53248
	ds_read_b128 v[206:209], v165 offset:54272
	ds_read_b128 v[224:227], v165 offset:55296
	ds_read_b128 v[228:231], v165 offset:56320
	global_load_lds_dwordx4 v[182:183], off
	s_add_i32 m0, s18, 0x2000
	s_add_u32 s18, s30, 0x160080
	v_lshl_add_u64 v[182:183], v[210:211], 0, s[68:69]
	s_addc_u32 s19, s31, 0
	s_add_i32 s28, s29, s4
	global_load_lds_dwordx4 v[182:183], off
	v_lshl_add_u64 v[182:183], s[18:19], 0, v[184:185]
	s_mov_b32 m0, s28
	s_nop 0
	global_load_lds_dwordx4 v[182:183], off
	v_lshl_add_u64 v[182:183], s[18:19], 0, v[144:145]
	s_add_i32 m0, s28, 0x2000
	s_nop 0
	global_load_lds_dwordx4 v[182:183], off
	v_lshl_add_u64 v[182:183], v[216:217], 0, s[68:69]
	s_mov_b32 m0, s42
	s_nop 0
	global_load_lds_dwordx4 v[182:183], off
	v_lshl_add_u64 v[182:183], v[218:219], 0, s[68:69]
	s_mov_b32 m0, s43
	s_nop 0
	global_load_lds_dwordx4 v[182:183], off
	s_waitcnt vmcnt(6)
	s_waitcnt lgkmcnt(0)
	s_barrier
	s_setprio 1
	s_waitcnt lgkmcnt(0)
	v_mfma_f32_16x16x32_bf16 v[60:63], v[64:67], v[174:177], v[60:63]
	v_mfma_f32_16x16x32_bf16 v[56:59], v[80:83], v[174:177], v[56:59]
	v_mfma_f32_16x16x32_bf16 v[44:47], v[64:67], v[194:197], v[44:47]
	v_mfma_f32_16x16x32_bf16 v[40:43], v[80:83], v[194:197], v[40:43]
	v_mfma_f32_16x16x32_bf16 v[28:31], v[64:67], v[202:205], v[28:31]
	v_mfma_f32_16x16x32_bf16 v[24:27], v[80:83], v[202:205], v[24:27]
	v_mfma_f32_16x16x32_bf16 v[12:15], v[64:67], v[224:227], v[12:15]
	v_mfma_f32_16x16x32_bf16 v[8:11], v[80:83], v[224:227], v[8:11]
	v_mfma_f32_16x16x32_bf16 v[60:63], v[68:71], v[178:181], v[60:63]
	v_mfma_f32_16x16x32_bf16 v[56:59], v[84:87], v[178:181], v[56:59]
	v_mfma_f32_16x16x32_bf16 v[44:47], v[68:71], v[198:201], v[44:47]
	v_mfma_f32_16x16x32_bf16 v[40:43], v[84:87], v[198:201], v[40:43]
	v_mfma_f32_16x16x32_bf16 v[28:31], v[68:71], v[206:209], v[28:31]
	v_mfma_f32_16x16x32_bf16 v[24:27], v[84:87], v[206:209], v[24:27]
	v_mfma_f32_16x16x32_bf16 v[12:15], v[68:71], v[228:231], v[12:15]
	v_mfma_f32_16x16x32_bf16 v[8:11], v[84:87], v[228:231], v[8:11]
	s_setprio 0
	s_setprio 1
	v_mfma_f32_16x16x32_bf16 v[52:55], v[154:157], v[174:177], v[52:55]
	v_mfma_f32_16x16x32_bf16 v[48:51], v[166:169], v[174:177], v[48:51]
	v_mfma_f32_16x16x32_bf16 v[36:39], v[154:157], v[194:197], v[36:39]
	v_mfma_f32_16x16x32_bf16 v[32:35], v[166:169], v[194:197], v[32:35]
	v_mfma_f32_16x16x32_bf16 v[20:23], v[154:157], v[202:205], v[20:23]
	v_mfma_f32_16x16x32_bf16 v[16:19], v[166:169], v[202:205], v[16:19]
	v_mfma_f32_16x16x32_bf16 v[4:7], v[154:157], v[224:227], v[4:7]
	v_mfma_f32_16x16x32_bf16 v[0:3], v[166:169], v[224:227], v[0:3]
	v_mfma_f32_16x16x32_bf16 v[52:55], v[158:161], v[178:181], v[52:55]
	v_mfma_f32_16x16x32_bf16 v[48:51], v[170:173], v[178:181], v[48:51]
	v_mfma_f32_16x16x32_bf16 v[36:39], v[158:161], v[198:201], v[36:39]
	v_mfma_f32_16x16x32_bf16 v[32:35], v[170:173], v[198:201], v[32:35]
	v_mfma_f32_16x16x32_bf16 v[20:23], v[158:161], v[206:209], v[20:23]
	v_mfma_f32_16x16x32_bf16 v[16:19], v[170:173], v[206:209], v[16:19]
	v_mfma_f32_16x16x32_bf16 v[4:7], v[158:161], v[228:231], v[4:7]
	v_mfma_f32_16x16x32_bf16 v[0:3], v[170:173], v[228:231], v[0:3]
	s_setprio 0
	s_barrier
	s_add_i32 s61, s61, 2
	s_add_u32 s59, s59, 0x100
	s_addc_u32 s60, s60, 0
	s_cmpk_gt_u32 s61, 0x55
	s_mov_b64 s[18:19], s[24:25]
	s_cbranch_scc0 .LBB0_1661
	s_and_b64 vcc, exec, s[8:9]
	s_cbranch_vccz .LBB0_1664
	s_barrier

.LBB0_1741:
	s_add_u32 s38, s36, 0x100
	s_addc_u32 s39, s37, 0
	s_add_i32 s28, 0, 0x10000
	s_cmp_eq_u32 s59, 4
	s_cselect_b32 s43, s11, s39
	s_cselect_b32 s42, s50, s38
	s_cselect_b32 s41, s51, s58
	s_cselect_b32 s40, s52, s53
	s_add_i32 s48, 0, 0x14000
	v_add_u32_e32 v124, s28, v172
	v_add_u32_e32 v170, s48, v172
	ds_read_b128 v[112:115], v124
	ds_read_b128 v[116:119], v124 offset:1024
	ds_read_b128 v[120:123], v124 offset:2048
	ds_read_b128 v[124:127], v124 offset:3072
	ds_read_b128 v[176:179], v170
	ds_read_b128 v[180:183], v170 offset:1024
	ds_read_b128 v[194:197], v170 offset:2048
	ds_read_b128 v[198:201], v170 offset:3072
	v_lshl_add_u64 v[170:171], s[36:37], 0, v[166:167]
	s_add_i32 m0, s20, 0xc000
	ds_read_b128 v[202:205], v174
	ds_read_b128 v[206:209], v174 offset:1024
	ds_read_b128 v[224:227], v174 offset:2048
	ds_read_b128 v[228:231], v174 offset:3072
	ds_read_b128 v[232:235], v174 offset:4096
	ds_read_b128 v[236:239], v174 offset:5120
	ds_read_b128 v[240:243], v174 offset:6144
	ds_read_b128 v[244:247], v174 offset:7168
	global_load_lds_dwordx4 v[170:171], off
	v_lshl_add_u64 v[170:171], s[36:37], 0, v[168:169]
	s_add_i32 m0, s20, 0xe000
	s_nop 0
	global_load_lds_dwordx4 v[170:171], off
	s_waitcnt vmcnt(8)
	s_waitcnt lgkmcnt(0)
	s_barrier
	s_setprio 1
	s_waitcnt lgkmcnt(0)
	v_mfma_f32_16x16x32_bf16 v[140:143], v[112:115], v[202:205], v[140:143]
	v_mfma_f32_16x16x32_bf16 v[136:139], v[120:123], v[202:205], v[136:139]
	v_mfma_f32_16x16x32_bf16 v[108:111], v[112:115], v[224:227], v[108:111]
	v_mfma_f32_16x16x32_bf16 v[104:107], v[120:123], v[224:227], v[104:107]
	v_mfma_f32_16x16x32_bf16 v[92:95], v[112:115], v[232:235], v[92:95]
	v_mfma_f32_16x16x32_bf16 v[88:91], v[120:123], v[232:235], v[88:91]
	v_mfma_f32_16x16x32_bf16 v[76:79], v[112:115], v[240:243], v[76:79]
	v_mfma_f32_16x16x32_bf16 v[72:75], v[120:123], v[240:243], v[72:75]
	v_mfma_f32_16x16x32_bf16 v[140:143], v[116:119], v[206:209], v[140:143]
	v_mfma_f32_16x16x32_bf16 v[136:139], v[124:127], v[206:209], v[136:139]
	v_mfma_f32_16x16x32_bf16 v[108:111], v[116:119], v[228:231], v[108:111]
	v_mfma_f32_16x16x32_bf16 v[104:107], v[124:127], v[228:231], v[104:107]
	v_mfma_f32_16x16x32_bf16 v[92:95], v[116:119], v[236:239], v[92:95]
	v_mfma_f32_16x16x32_bf16 v[88:91], v[124:127], v[236:239], v[88:91]
	v_mfma_f32_16x16x32_bf16 v[76:79], v[116:119], v[244:247], v[76:79]
	v_mfma_f32_16x16x32_bf16 v[72:75], v[124:127], v[244:247], v[72:75]
	s_setprio 0
	s_setprio 1
	v_mfma_f32_16x16x32_bf16 v[132:135], v[176:179], v[202:205], v[132:135]
	v_mfma_f32_16x16x32_bf16 v[128:131], v[194:197], v[202:205], v[128:131]
	v_mfma_f32_16x16x32_bf16 v[100:103], v[176:179], v[224:227], v[100:103]
	v_mfma_f32_16x16x32_bf16 v[96:99], v[194:197], v[224:227], v[96:99]
	v_mfma_f32_16x16x32_bf16 v[84:87], v[176:179], v[232:235], v[84:87]
	v_mfma_f32_16x16x32_bf16 v[80:83], v[194:197], v[232:235], v[80:83]
	v_mfma_f32_16x16x32_bf16 v[68:71], v[176:179], v[240:243], v[68:71]
	v_mfma_f32_16x16x32_bf16 v[64:67], v[194:197], v[240:243], v[64:67]
	v_mfma_f32_16x16x32_bf16 v[132:135], v[180:183], v[206:209], v[132:135]
	v_mfma_f32_16x16x32_bf16 v[128:131], v[198:201], v[206:209], v[128:131]
	v_mfma_f32_16x16x32_bf16 v[100:103], v[180:183], v[228:231], v[100:103]
	v_mfma_f32_16x16x32_bf16 v[96:99], v[198:201], v[228:231], v[96:99]
	v_mfma_f32_16x16x32_bf16 v[84:87], v[180:183], v[236:239], v[84:87]
	v_mfma_f32_16x16x32_bf16 v[80:83], v[198:201], v[236:239], v[80:83]
	v_mfma_f32_16x16x32_bf16 v[68:71], v[180:183], v[244:247], v[68:71]
	v_mfma_f32_16x16x32_bf16 v[64:67], v[198:201], v[244:247], v[64:67]
	s_setprio 0
	s_barrier
	s_add_i32 s28, s28, s4
	v_lshl_add_u64 v[170:171], s[40:41], 0, v[184:185]
	s_mov_b32 m0, s28
	ds_read_b128 v[202:205], v174 offset:16384
	ds_read_b128 v[206:209], v174 offset:17408
	ds_read_b128 v[224:227], v174 offset:18432
	ds_read_b128 v[228:231], v174 offset:19456
	ds_read_b128 v[232:235], v174 offset:20480
	ds_read_b128 v[236:239], v174 offset:21504
	ds_read_b128 v[240:243], v174 offset:22528
	ds_read_b128 v[244:247], v174 offset:23552
	global_load_lds_dwordx4 v[170:171], off
	s_add_i32 m0, s28, 0x2000
	s_add_u32 s28, s40, 0x160000
	v_lshl_add_u64 v[210:211], s[40:41], 0, v[144:145]
	s_addc_u32 s29, s41, 0
	s_add_i32 s36, s48, s4
	global_load_lds_dwordx4 v[210:211], off
	v_lshl_add_u64 v[216:217], s[28:29], 0, v[184:185]
	s_mov_b32 m0, s36
	v_lshl_add_u64 v[218:219], s[42:43], 0, v[146:147]
	global_load_lds_dwordx4 v[216:217], off
	v_lshl_add_u64 v[216:217], s[28:29], 0, v[144:145]
	s_add_i32 m0, s36, 0x2000
	s_nop 0
	global_load_lds_dwordx4 v[216:217], off
	v_lshl_add_u64 v[216:217], s[42:43], 0, v[148:149]
	s_waitcnt vmcnt(6)
	s_waitcnt lgkmcnt(0)
	s_barrier
	s_setprio 1
	s_waitcnt lgkmcnt(0)
	v_mfma_f32_16x16x32_bf16 v[60:63], v[112:115], v[202:205], v[60:63]
	v_mfma_f32_16x16x32_bf16 v[56:59], v[120:123], v[202:205], v[56:59]
	v_mfma_f32_16x16x32_bf16 v[44:47], v[112:115], v[224:227], v[44:47]
	v_mfma_f32_16x16x32_bf16 v[40:43], v[120:123], v[224:227], v[40:43]
	v_mfma_f32_16x16x32_bf16 v[36:39], v[112:115], v[232:235], v[36:39]
	v_mfma_f32_16x16x32_bf16 v[28:31], v[120:123], v[232:235], v[28:31]
	v_mfma_f32_16x16x32_bf16 v[20:23], v[112:115], v[240:243], v[20:23]
	v_mfma_f32_16x16x32_bf16 v[12:15], v[120:123], v[240:243], v[12:15]
	v_mfma_f32_16x16x32_bf16 v[60:63], v[116:119], v[206:209], v[60:63]
	v_mfma_f32_16x16x32_bf16 v[56:59], v[124:127], v[206:209], v[56:59]
	v_mfma_f32_16x16x32_bf16 v[44:47], v[116:119], v[228:231], v[44:47]
	v_mfma_f32_16x16x32_bf16 v[40:43], v[124:127], v[228:231], v[40:43]
	v_mfma_f32_16x16x32_bf16 v[36:39], v[116:119], v[236:239], v[36:39]
	v_mfma_f32_16x16x32_bf16 v[28:31], v[124:127], v[236:239], v[28:31]
	v_mfma_f32_16x16x32_bf16 v[20:23], v[116:119], v[244:247], v[20:23]
	v_mfma_f32_16x16x32_bf16 v[12:15], v[124:127], v[244:247], v[12:15]
	s_setprio 0
	s_setprio 1
	v_mfma_f32_16x16x32_bf16 v[52:55], v[176:179], v[202:205], v[52:55]
	v_mfma_f32_16x16x32_bf16 v[48:51], v[194:197], v[202:205], v[48:51]
	v_mfma_f32_16x16x32_bf16 v[32:35], v[176:179], v[224:227], v[32:35]
	v_mfma_f32_16x16x32_bf16 v[24:27], v[194:197], v[224:227], v[24:27]
	v_mfma_f32_16x16x32_bf16 v[16:19], v[176:179], v[232:235], v[16:19]
	v_mfma_f32_16x16x32_bf16 v[8:11], v[194:197], v[232:235], v[8:11]
	v_mfma_f32_16x16x32_bf16 v[4:7], v[176:179], v[240:243], v[4:7]
	v_mfma_f32_16x16x32_bf16 v[0:3], v[194:197], v[240:243], v[0:3]
	v_mfma_f32_16x16x32_bf16 v[52:55], v[180:183], v[206:209], v[52:55]
	v_mfma_f32_16x16x32_bf16 v[48:51], v[198:201], v[206:209], v[48:51]
	v_mfma_f32_16x16x32_bf16 v[32:35], v[180:183], v[228:231], v[32:35]
	v_mfma_f32_16x16x32_bf16 v[24:27], v[198:201], v[228:231], v[24:27]
	v_mfma_f32_16x16x32_bf16 v[16:19], v[180:183], v[236:239], v[16:19]
	v_mfma_f32_16x16x32_bf16 v[8:11], v[198:201], v[236:239], v[8:11]
	v_mfma_f32_16x16x32_bf16 v[4:7], v[180:183], v[244:247], v[4:7]
	v_mfma_f32_16x16x32_bf16 v[0:3], v[198:201], v[244:247], v[0:3]
	s_setprio 0
	s_barrier
	s_add_i32 s36, 0, 0x18000
	s_add_i32 s37, 0, 0x1c000
	v_add_u32_e32 v124, s36, v172
	v_add_u32_e32 v175, s37, v172
	ds_read_b128 v[112:115], v124
	ds_read_b128 v[116:119], v124 offset:1024
	ds_read_b128 v[120:123], v124 offset:2048
	ds_read_b128 v[124:127], v124 offset:3072
	ds_read_b128 v[176:179], v175
	ds_read_b128 v[180:183], v175 offset:1024
	ds_read_b128 v[194:197], v175 offset:2048
	ds_read_b128 v[198:201], v175 offset:3072
	s_add_u32 s28, s42, 0x160000
	s_addc_u32 s29, s43, 0
	s_mov_b32 m0, s26
	v_lshl_add_u64 v[220:221], s[28:29], 0, v[148:149]
	ds_read_b128 v[202:205], v174 offset:32768
	ds_read_b128 v[206:209], v174 offset:33792
	ds_read_b128 v[224:227], v174 offset:34816
	ds_read_b128 v[228:231], v174 offset:35840
	ds_read_b128 v[232:235], v174 offset:36864
	ds_read_b128 v[236:239], v174 offset:37888
	ds_read_b128 v[240:243], v174 offset:38912
	ds_read_b128 v[244:247], v174 offset:39936
	global_load_lds_dwordx4 v[220:221], off
	v_lshl_add_u64 v[220:221], s[28:29], 0, v[146:147]
	s_mov_b32 m0, s27
	s_nop 0
	global_load_lds_dwordx4 v[220:221], off
	s_mov_b32 m0, s20
	s_nop 0
	global_load_lds_dwordx4 v[216:217], off
	s_mov_b32 m0, s21
	s_nop 0
	global_load_lds_dwordx4 v[218:219], off
	s_waitcnt vmcnt(8)
	s_waitcnt lgkmcnt(0)
	s_barrier
	s_setprio 1
	s_waitcnt lgkmcnt(0)
	v_mfma_f32_16x16x32_bf16 v[140:143], v[112:115], v[202:205], v[140:143]
	v_mfma_f32_16x16x32_bf16 v[136:139], v[120:123], v[202:205], v[136:139]
	v_mfma_f32_16x16x32_bf16 v[108:111], v[112:115], v[224:227], v[108:111]
	v_mfma_f32_16x16x32_bf16 v[104:107], v[120:123], v[224:227], v[104:107]
	v_mfma_f32_16x16x32_bf16 v[92:95], v[112:115], v[232:235], v[92:95]
	v_mfma_f32_16x16x32_bf16 v[88:91], v[120:123], v[232:235], v[88:91]
	v_mfma_f32_16x16x32_bf16 v[76:79], v[112:115], v[240:243], v[76:79]
	v_mfma_f32_16x16x32_bf16 v[72:75], v[120:123], v[240:243], v[72:75]
	v_mfma_f32_16x16x32_bf16 v[140:143], v[116:119], v[206:209], v[140:143]
	v_mfma_f32_16x16x32_bf16 v[136:139], v[124:127], v[206:209], v[136:139]
	v_mfma_f32_16x16x32_bf16 v[108:111], v[116:119], v[228:231], v[108:111]
	v_mfma_f32_16x16x32_bf16 v[104:107], v[124:127], v[228:231], v[104:107]
	v_mfma_f32_16x16x32_bf16 v[92:95], v[116:119], v[236:239], v[92:95]
	v_mfma_f32_16x16x32_bf16 v[88:91], v[124:127], v[236:239], v[88:91]
	v_mfma_f32_16x16x32_bf16 v[76:79], v[116:119], v[244:247], v[76:79]
	v_mfma_f32_16x16x32_bf16 v[72:75], v[124:127], v[244:247], v[72:75]
	s_setprio 0
	s_setprio 1
	v_mfma_f32_16x16x32_bf16 v[132:135], v[176:179], v[202:205], v[132:135]
	v_mfma_f32_16x16x32_bf16 v[128:131], v[194:197], v[202:205], v[128:131]
	v_mfma_f32_16x16x32_bf16 v[100:103], v[176:179], v[224:227], v[100:103]
	v_mfma_f32_16x16x32_bf16 v[96:99], v[194:197], v[224:227], v[96:99]
	v_mfma_f32_16x16x32_bf16 v[84:87], v[176:179], v[232:235], v[84:87]
	v_mfma_f32_16x16x32_bf16 v[80:83], v[194:197], v[232:235], v[80:83]
	v_mfma_f32_16x16x32_bf16 v[68:71], v[176:179], v[240:243], v[68:71]
	v_mfma_f32_16x16x32_bf16 v[64:67], v[194:197], v[240:243], v[64:67]
	v_mfma_f32_16x16x32_bf16 v[132:135], v[180:183], v[206:209], v[132:135]
	v_mfma_f32_16x16x32_bf16 v[128:131], v[198:201], v[206:209], v[128:131]
	v_mfma_f32_16x16x32_bf16 v[100:103], v[180:183], v[228:231], v[100:103]
	v_mfma_f32_16x16x32_bf16 v[96:99], v[198:201], v[228:231], v[96:99]
	v_mfma_f32_16x16x32_bf16 v[84:87], v[180:183], v[236:239], v[84:87]
	v_mfma_f32_16x16x32_bf16 v[80:83], v[198:201], v[236:239], v[80:83]
	v_mfma_f32_16x16x32_bf16 v[68:71], v[180:183], v[244:247], v[68:71]
	v_mfma_f32_16x16x32_bf16 v[64:67], v[198:201], v[244:247], v[64:67]
	s_setprio 0
	s_barrier
	s_add_i32 s28, s36, s4
	v_lshl_add_u64 v[170:171], v[170:171], 0, s[68:69]
	s_mov_b32 m0, s28
	ds_read_b128 v[202:205], v174 offset:49152
	ds_read_b128 v[206:209], v174 offset:50176
	ds_read_b128 v[224:227], v174 offset:51200
	ds_read_b128 v[228:231], v174 offset:52224
	ds_read_b128 v[232:235], v174 offset:53248
	ds_read_b128 v[236:239], v174 offset:54272
	ds_read_b128 v[240:243], v174 offset:55296
	ds_read_b128 v[244:247], v174 offset:56320
	global_load_lds_dwordx4 v[170:171], off
	s_add_i32 m0, s28, 0x2000
	s_add_u32 s28, s40, 0x160080
	v_lshl_add_u64 v[170:171], v[210:211], 0, s[68:69]
	s_addc_u32 s29, s41, 0
	s_add_i32 s36, s37, s4
	global_load_lds_dwordx4 v[170:171], off
	v_lshl_add_u64 v[170:171], s[28:29], 0, v[184:185]
	s_mov_b32 m0, s36
	s_nop 0
	global_load_lds_dwordx4 v[170:171], off
	v_lshl_add_u64 v[170:171], s[28:29], 0, v[144:145]
	s_add_i32 m0, s36, 0x2000
	s_nop 0
	global_load_lds_dwordx4 v[170:171], off
	v_lshl_add_u64 v[170:171], v[216:217], 0, s[68:69]
	s_mov_b32 m0, s44
	s_nop 0
	global_load_lds_dwordx4 v[170:171], off
	v_lshl_add_u64 v[170:171], v[218:219], 0, s[68:69]
	s_mov_b32 m0, s45
	s_nop 0
	global_load_lds_dwordx4 v[170:171], off
	s_waitcnt vmcnt(6)
	s_waitcnt lgkmcnt(0)
	s_barrier
	s_setprio 1
	s_waitcnt lgkmcnt(0)
	v_mfma_f32_16x16x32_bf16 v[60:63], v[112:115], v[202:205], v[60:63]
	v_mfma_f32_16x16x32_bf16 v[56:59], v[120:123], v[202:205], v[56:59]
	v_mfma_f32_16x16x32_bf16 v[44:47], v[112:115], v[224:227], v[44:47]
	v_mfma_f32_16x16x32_bf16 v[40:43], v[120:123], v[224:227], v[40:43]
	v_mfma_f32_16x16x32_bf16 v[36:39], v[112:115], v[232:235], v[36:39]
	v_mfma_f32_16x16x32_bf16 v[28:31], v[120:123], v[232:235], v[28:31]
	v_mfma_f32_16x16x32_bf16 v[20:23], v[112:115], v[240:243], v[20:23]
	v_mfma_f32_16x16x32_bf16 v[12:15], v[120:123], v[240:243], v[12:15]
	v_mfma_f32_16x16x32_bf16 v[60:63], v[116:119], v[206:209], v[60:63]
	v_mfma_f32_16x16x32_bf16 v[56:59], v[124:127], v[206:209], v[56:59]
	v_mfma_f32_16x16x32_bf16 v[44:47], v[116:119], v[228:231], v[44:47]
	v_mfma_f32_16x16x32_bf16 v[40:43], v[124:127], v[228:231], v[40:43]
	v_mfma_f32_16x16x32_bf16 v[36:39], v[116:119], v[236:239], v[36:39]
	v_mfma_f32_16x16x32_bf16 v[28:31], v[124:127], v[236:239], v[28:31]
	v_mfma_f32_16x16x32_bf16 v[20:23], v[116:119], v[244:247], v[20:23]
	v_mfma_f32_16x16x32_bf16 v[12:15], v[124:127], v[244:247], v[12:15]
	s_setprio 0
	s_setprio 1
	v_mfma_f32_16x16x32_bf16 v[52:55], v[176:179], v[202:205], v[52:55]
	v_mfma_f32_16x16x32_bf16 v[48:51], v[194:197], v[202:205], v[48:51]
	v_mfma_f32_16x16x32_bf16 v[32:35], v[176:179], v[224:227], v[32:35]
	v_mfma_f32_16x16x32_bf16 v[24:27], v[194:197], v[224:227], v[24:27]
	v_mfma_f32_16x16x32_bf16 v[16:19], v[176:179], v[232:235], v[16:19]
	v_mfma_f32_16x16x32_bf16 v[8:11], v[194:197], v[232:235], v[8:11]
	v_mfma_f32_16x16x32_bf16 v[4:7], v[176:179], v[240:243], v[4:7]
	v_mfma_f32_16x16x32_bf16 v[0:3], v[194:197], v[240:243], v[0:3]
	v_mfma_f32_16x16x32_bf16 v[52:55], v[180:183], v[206:209], v[52:55]
	v_mfma_f32_16x16x32_bf16 v[48:51], v[198:201], v[206:209], v[48:51]
	v_mfma_f32_16x16x32_bf16 v[32:35], v[180:183], v[228:231], v[32:35]
	v_mfma_f32_16x16x32_bf16 v[24:27], v[198:201], v[228:231], v[24:27]
	v_mfma_f32_16x16x32_bf16 v[16:19], v[180:183], v[236:239], v[16:19]
	v_mfma_f32_16x16x32_bf16 v[8:11], v[198:201], v[236:239], v[8:11]
	v_mfma_f32_16x16x32_bf16 v[4:7], v[180:183], v[244:247], v[4:7]
	v_mfma_f32_16x16x32_bf16 v[0:3], v[198:201], v[244:247], v[0:3]
	s_setprio 0
	s_barrier
	s_add_i32 s59, s59, 2
	s_add_u32 s53, s53, 0x100
	s_addc_u32 s58, s58, 0
	s_cmp_gt_u32 s59, 5
	s_mov_b64 s[36:37], s[38:39]
	s_cbranch_scc0 .LBB0_1741
	s_and_b64 vcc, exec, s[8:9]
	s_cbranch_vccz .LBB0_1744
	s_barrier
